# speedup vs baseline: 1.0140x; 1.0140x over previous
.LBB7_27:
	ds_read_b128 v[128:131], v170
	ds_read_b128 v[132:135], v170 offset:1024
	ds_read_b128 v[136:139], v170 offset:2048
	ds_read_b128 v[140:143], v170 offset:3072
	s_add_u32 s30, s28, 0xfffd0080
	s_addc_u32 s31, s29, -1
	s_cmp_eq_u32 s73, 8
	s_cselect_b32 s35, s9, s31
	s_cselect_b32 s34, s8, s30
	s_cselect_b32 s31, s1, s72
	s_cselect_b32 s30, s0, s71
	v_lshl_add_u64 v[162:163], s[28:29], 0, v[152:153]
	s_add_i32 m0, s43, 0xc000
	ds_read_b128 v[158:161], v171
	ds_read_b128 v[176:179], v171 offset:1024
	ds_read_b128 v[180:183], v171 offset:2048
	ds_read_b128 v[184:187], v171 offset:3072
	ds_read_b128 v[188:191], v171 offset:4096
	ds_read_b128 v[192:195], v171 offset:5120
	ds_read_b128 v[196:199], v171 offset:6144
	ds_read_b128 v[200:203], v171 offset:7168
	global_load_lds_dwordx4 v[162:163], off
	v_lshl_add_u64 v[162:163], s[28:29], 0, v[154:155]
	s_add_i32 m0, s43, 0xe000
	s_nop 0
	global_load_lds_dwordx4 v[162:163], off
	s_waitcnt lgkmcnt(8)
	s_setprio 1
	s_barrier
	s_waitcnt lgkmcnt(0)
	v_mfma_f32_16x16x32_f16 v[124:127], v[128:131], v[158:161], v[124:127]
	v_mfma_f32_16x16x32_f16 v[120:123], v[136:139], v[158:161], v[120:123]
	v_mfma_f32_16x16x32_f16 v[108:111], v[128:131], v[180:183], v[108:111]
	v_mfma_f32_16x16x32_f16 v[104:107], v[136:139], v[180:183], v[104:107]
	v_mfma_f32_16x16x32_f16 v[96:99], v[128:131], v[188:191], v[96:99]
	v_mfma_f32_16x16x32_f16 v[88:91], v[136:139], v[188:191], v[88:91]
	v_mfma_f32_16x16x32_f16 v[80:83], v[128:131], v[196:199], v[80:83]
	v_mfma_f32_16x16x32_f16 v[72:75], v[136:139], v[196:199], v[72:75]
	v_mfma_f32_16x16x32_f16 v[124:127], v[132:135], v[176:179], v[124:127]
	v_mfma_f32_16x16x32_f16 v[120:123], v[140:143], v[176:179], v[120:123]
	v_mfma_f32_16x16x32_f16 v[108:111], v[132:135], v[184:187], v[108:111]
	v_mfma_f32_16x16x32_f16 v[104:107], v[140:143], v[184:187], v[104:107]
	v_mfma_f32_16x16x32_f16 v[96:99], v[132:135], v[192:195], v[96:99]
	v_mfma_f32_16x16x32_f16 v[88:91], v[140:143], v[192:195], v[88:91]
	v_mfma_f32_16x16x32_f16 v[80:83], v[132:135], v[200:203], v[80:83]
	v_mfma_f32_16x16x32_f16 v[72:75], v[140:143], v[200:203], v[72:75]
	s_barrier
	s_setprio 0
	s_add_i32 s74, s65, s42
	v_lshl_add_u64 v[162:163], s[30:31], 0, v[146:147]
	s_mov_b32 m0, s74
	ds_read_b128 v[204:207], v172
	ds_read_b128 v[208:211], v172 offset:1024
	ds_read_b128 v[212:215], v172 offset:2048
	ds_read_b128 v[216:219], v172 offset:3072
	global_load_lds_dwordx4 v[162:163], off
	v_lshl_add_u64 v[220:221], s[30:31], 0, v[150:151]
	s_add_i32 m0, s74, 0x2000
	s_nop 0
	global_load_lds_dwordx4 v[220:221], off
	s_setprio 1
	s_barrier
	s_waitcnt lgkmcnt(0)
	v_mfma_f32_16x16x32_f16 v[116:119], v[204:207], v[158:161], v[116:119]
	v_mfma_f32_16x16x32_f16 v[112:115], v[212:215], v[158:161], v[112:115]
	v_mfma_f32_16x16x32_f16 v[100:103], v[204:207], v[180:183], v[100:103]
	v_mfma_f32_16x16x32_f16 v[92:95], v[212:215], v[180:183], v[92:95]
	v_mfma_f32_16x16x32_f16 v[84:87], v[204:207], v[188:191], v[84:87]
	v_mfma_f32_16x16x32_f16 v[76:79], v[212:215], v[188:191], v[76:79]
	v_mfma_f32_16x16x32_f16 v[68:71], v[204:207], v[196:199], v[68:71]
	v_mfma_f32_16x16x32_f16 v[64:67], v[212:215], v[196:199], v[64:67]
	v_mfma_f32_16x16x32_f16 v[116:119], v[208:211], v[176:179], v[116:119]
	v_mfma_f32_16x16x32_f16 v[112:115], v[216:219], v[176:179], v[112:115]
	v_mfma_f32_16x16x32_f16 v[100:103], v[208:211], v[184:187], v[100:103]
	v_mfma_f32_16x16x32_f16 v[92:95], v[216:219], v[184:187], v[92:95]
	v_mfma_f32_16x16x32_f16 v[84:87], v[208:211], v[192:195], v[84:87]
	v_mfma_f32_16x16x32_f16 v[76:79], v[216:219], v[192:195], v[76:79]
	v_mfma_f32_16x16x32_f16 v[68:71], v[208:211], v[200:203], v[68:71]
	v_mfma_f32_16x16x32_f16 v[64:67], v[216:219], v[200:203], v[64:67]
	s_barrier
	s_setprio 0
	s_mov_b32 m0, s43
	v_lshl_add_u64 v[222:223], s[34:35], 0, v[144:145]
	ds_read_b128 v[158:161], v171 offset:16384
	ds_read_b128 v[176:179], v171 offset:17408
	ds_read_b128 v[180:183], v171 offset:18432
	ds_read_b128 v[184:187], v171 offset:19456
	ds_read_b128 v[188:191], v171 offset:20480
	ds_read_b128 v[192:195], v171 offset:21504
	ds_read_b128 v[196:199], v171 offset:22528
	ds_read_b128 v[200:203], v171 offset:23552
	global_load_lds_dwordx4 v[222:223], off
	v_lshl_add_u64 v[224:225], s[34:35], 0, v[148:149]
	s_mov_b32 m0, s44
	s_nop 0
	global_load_lds_dwordx4 v[224:225], off
	s_setprio 1
	s_barrier
	s_waitcnt lgkmcnt(0)
	v_mfma_f32_16x16x32_f16 v[60:63], v[128:131], v[158:161], v[60:63]
	v_mfma_f32_16x16x32_f16 v[56:59], v[136:139], v[158:161], v[56:59]
	v_mfma_f32_16x16x32_f16 v[48:51], v[128:131], v[180:183], v[48:51]
	v_mfma_f32_16x16x32_f16 v[40:43], v[136:139], v[180:183], v[40:43]
	v_mfma_f32_16x16x32_f16 v[32:35], v[128:131], v[188:191], v[32:35]
	v_mfma_f32_16x16x32_f16 v[24:27], v[136:139], v[188:191], v[24:27]
	v_mfma_f32_16x16x32_f16 v[16:19], v[128:131], v[196:199], v[16:19]
	v_mfma_f32_16x16x32_f16 v[8:11], v[136:139], v[196:199], v[8:11]
	v_mfma_f32_16x16x32_f16 v[60:63], v[132:135], v[176:179], v[60:63]
	v_mfma_f32_16x16x32_f16 v[56:59], v[140:143], v[176:179], v[56:59]
	v_mfma_f32_16x16x32_f16 v[48:51], v[132:135], v[184:187], v[48:51]
	v_mfma_f32_16x16x32_f16 v[40:43], v[140:143], v[184:187], v[40:43]
	v_mfma_f32_16x16x32_f16 v[32:35], v[132:135], v[192:195], v[32:35]
	v_mfma_f32_16x16x32_f16 v[24:27], v[140:143], v[192:195], v[24:27]
	v_mfma_f32_16x16x32_f16 v[16:19], v[132:135], v[200:203], v[16:19]
	v_mfma_f32_16x16x32_f16 v[8:11], v[140:143], v[200:203], v[8:11]
	s_barrier
	s_setprio 0
	s_add_u32 s74, s30, 0xc000
	s_addc_u32 s75, s31, 0
	s_add_i32 s76, s66, s42
	v_lshl_add_u64 v[128:129], s[74:75], 0, v[146:147]
	s_mov_b32 m0, s76
	s_nop 0
	global_load_lds_dwordx4 v[128:129], off
	v_lshl_add_u64 v[128:129], s[74:75], 0, v[150:151]
	s_add_i32 m0, s76, 0x2000
	s_nop 0
	global_load_lds_dwordx4 v[128:129], off
	s_waitcnt vmcnt(6)
	s_setprio 1
	s_barrier
	v_mfma_f32_16x16x32_f16 v[52:55], v[204:207], v[158:161], v[52:55]
	v_mfma_f32_16x16x32_f16 v[44:47], v[212:215], v[158:161], v[44:47]
	v_mfma_f32_16x16x32_f16 v[36:39], v[204:207], v[180:183], v[36:39]
	v_mfma_f32_16x16x32_f16 v[28:31], v[212:215], v[180:183], v[28:31]
	v_mfma_f32_16x16x32_f16 v[20:23], v[204:207], v[188:191], v[20:23]
	v_mfma_f32_16x16x32_f16 v[12:15], v[212:215], v[188:191], v[12:15]
	v_mfma_f32_16x16x32_f16 v[4:7], v[204:207], v[196:199], v[4:7]
	v_mfma_f32_16x16x32_f16 v[0:3], v[212:215], v[196:199], v[0:3]
	v_mfma_f32_16x16x32_f16 v[52:55], v[208:211], v[176:179], v[52:55]
	v_mfma_f32_16x16x32_f16 v[44:47], v[216:219], v[176:179], v[44:47]
	v_mfma_f32_16x16x32_f16 v[36:39], v[208:211], v[184:187], v[36:39]
	v_mfma_f32_16x16x32_f16 v[28:31], v[216:219], v[184:187], v[28:31]
	v_mfma_f32_16x16x32_f16 v[20:23], v[208:211], v[192:195], v[20:23]
	v_mfma_f32_16x16x32_f16 v[12:15], v[216:219], v[192:195], v[12:15]
	v_mfma_f32_16x16x32_f16 v[4:7], v[208:211], v[200:203], v[4:7]
	v_mfma_f32_16x16x32_f16 v[0:3], v[216:219], v[200:203], v[0:3]
	s_barrier
	s_setprio 0
	s_add_i32 s74, 0, 0x18000
	v_add_u32_e32 v140, s74, v166
	ds_read_b128 v[128:131], v140
	ds_read_b128 v[132:135], v140 offset:1024
	ds_read_b128 v[136:139], v140 offset:2048
	ds_read_b128 v[140:143], v140 offset:3072
	s_add_u32 s34, s34, 0x30000
	s_addc_u32 s35, s35, 0
	s_mov_b32 m0, s45
	v_lshl_add_u64 v[204:205], s[34:35], 0, v[144:145]
	ds_read_b128 v[158:161], v171 offset:32768
	ds_read_b128 v[176:179], v171 offset:33792
	ds_read_b128 v[180:183], v171 offset:34816
	ds_read_b128 v[184:187], v171 offset:35840
	ds_read_b128 v[188:191], v171 offset:36864
	ds_read_b128 v[192:195], v171 offset:37888
	ds_read_b128 v[196:199], v171 offset:38912
	ds_read_b128 v[200:203], v171 offset:39936
	global_load_lds_dwordx4 v[204:205], off
	v_lshl_add_u64 v[204:205], s[34:35], 0, v[148:149]
	s_mov_b32 m0, s46
	s_nop 0
	global_load_lds_dwordx4 v[204:205], off
	s_waitcnt lgkmcnt(8)
	s_setprio 1
	s_barrier
	s_waitcnt lgkmcnt(0)
	v_mfma_f32_16x16x32_f16 v[124:127], v[128:131], v[158:161], v[124:127]
	v_mfma_f32_16x16x32_f16 v[120:123], v[136:139], v[158:161], v[120:123]
	v_mfma_f32_16x16x32_f16 v[108:111], v[128:131], v[180:183], v[108:111]
	v_mfma_f32_16x16x32_f16 v[104:107], v[136:139], v[180:183], v[104:107]
	v_mfma_f32_16x16x32_f16 v[96:99], v[128:131], v[188:191], v[96:99]
	v_mfma_f32_16x16x32_f16 v[88:91], v[136:139], v[188:191], v[88:91]
	v_mfma_f32_16x16x32_f16 v[80:83], v[128:131], v[196:199], v[80:83]
	v_mfma_f32_16x16x32_f16 v[72:75], v[136:139], v[196:199], v[72:75]
	v_mfma_f32_16x16x32_f16 v[124:127], v[132:135], v[176:179], v[124:127]
	v_mfma_f32_16x16x32_f16 v[120:123], v[140:143], v[176:179], v[120:123]
	v_mfma_f32_16x16x32_f16 v[108:111], v[132:135], v[184:187], v[108:111]
	v_mfma_f32_16x16x32_f16 v[104:107], v[140:143], v[184:187], v[104:107]
	v_mfma_f32_16x16x32_f16 v[96:99], v[132:135], v[192:195], v[96:99]
	v_mfma_f32_16x16x32_f16 v[88:91], v[140:143], v[192:195], v[88:91]
	v_mfma_f32_16x16x32_f16 v[80:83], v[132:135], v[200:203], v[80:83]
	v_mfma_f32_16x16x32_f16 v[72:75], v[140:143], v[200:203], v[72:75]
	s_barrier
	s_setprio 0
	s_add_i32 s34, 0, 0x1c000
	s_add_i32 s35, s74, s42
	v_add_u32_e32 v175, s34, v166
	v_lshl_add_u64 v[162:163], v[162:163], 0, s[26:27]
	s_mov_b32 m0, s35
	ds_read_b128 v[204:207], v175
	ds_read_b128 v[208:211], v175 offset:1024
	ds_read_b128 v[212:215], v175 offset:2048
	ds_read_b128 v[216:219], v175 offset:3072
	global_load_lds_dwordx4 v[162:163], off
	v_lshl_add_u64 v[162:163], v[220:221], 0, s[26:27]
	s_add_i32 m0, s35, 0x2000
	s_nop 0
	global_load_lds_dwordx4 v[162:163], off
	s_setprio 1
	s_barrier
	s_waitcnt lgkmcnt(0)
	v_mfma_f32_16x16x32_f16 v[116:119], v[204:207], v[158:161], v[116:119]
	v_mfma_f32_16x16x32_f16 v[112:115], v[212:215], v[158:161], v[112:115]
	v_mfma_f32_16x16x32_f16 v[100:103], v[204:207], v[180:183], v[100:103]
	v_mfma_f32_16x16x32_f16 v[92:95], v[212:215], v[180:183], v[92:95]
	v_mfma_f32_16x16x32_f16 v[84:87], v[204:207], v[188:191], v[84:87]
	v_mfma_f32_16x16x32_f16 v[76:79], v[212:215], v[188:191], v[76:79]
	v_mfma_f32_16x16x32_f16 v[68:71], v[204:207], v[196:199], v[68:71]
	v_mfma_f32_16x16x32_f16 v[64:67], v[212:215], v[196:199], v[64:67]
	v_mfma_f32_16x16x32_f16 v[116:119], v[208:211], v[176:179], v[116:119]
	v_mfma_f32_16x16x32_f16 v[112:115], v[216:219], v[176:179], v[112:115]
	v_mfma_f32_16x16x32_f16 v[100:103], v[208:211], v[184:187], v[100:103]
	v_mfma_f32_16x16x32_f16 v[92:95], v[216:219], v[184:187], v[92:95]
	v_mfma_f32_16x16x32_f16 v[84:87], v[208:211], v[192:195], v[84:87]
	v_mfma_f32_16x16x32_f16 v[76:79], v[216:219], v[192:195], v[76:79]
	v_mfma_f32_16x16x32_f16 v[68:71], v[208:211], v[200:203], v[68:71]
	v_mfma_f32_16x16x32_f16 v[64:67], v[216:219], v[200:203], v[64:67]
	s_barrier
	s_setprio 0
	s_mov_b32 m0, s49
	v_lshl_add_u64 v[162:163], v[222:223], 0, s[26:27]
	ds_read_b128 v[158:161], v171 offset:49152
	ds_read_b128 v[176:179], v171 offset:50176
	ds_read_b128 v[180:183], v171 offset:51200
	ds_read_b128 v[184:187], v171 offset:52224
	ds_read_b128 v[188:191], v171 offset:53248
	ds_read_b128 v[192:195], v171 offset:54272
	ds_read_b128 v[196:199], v171 offset:55296
	ds_read_b128 v[200:203], v171 offset:56320
	global_load_lds_dwordx4 v[162:163], off
	v_lshl_add_u64 v[162:163], v[224:225], 0, s[26:27]
	s_mov_b32 m0, s50
	s_nop 0
	global_load_lds_dwordx4 v[162:163], off
	s_setprio 1
	s_barrier
	s_waitcnt lgkmcnt(0)
	v_mfma_f32_16x16x32_f16 v[60:63], v[128:131], v[158:161], v[60:63]
	v_mfma_f32_16x16x32_f16 v[56:59], v[136:139], v[158:161], v[56:59]
	v_mfma_f32_16x16x32_f16 v[48:51], v[128:131], v[180:183], v[48:51]
	v_mfma_f32_16x16x32_f16 v[40:43], v[136:139], v[180:183], v[40:43]
	v_mfma_f32_16x16x32_f16 v[32:35], v[128:131], v[188:191], v[32:35]
	v_mfma_f32_16x16x32_f16 v[24:27], v[136:139], v[188:191], v[24:27]
	v_mfma_f32_16x16x32_f16 v[16:19], v[128:131], v[196:199], v[16:19]
	v_mfma_f32_16x16x32_f16 v[8:11], v[136:139], v[196:199], v[8:11]
	v_mfma_f32_16x16x32_f16 v[60:63], v[132:135], v[176:179], v[60:63]
	v_mfma_f32_16x16x32_f16 v[56:59], v[140:143], v[176:179], v[56:59]
	v_mfma_f32_16x16x32_f16 v[48:51], v[132:135], v[184:187], v[48:51]
	v_mfma_f32_16x16x32_f16 v[40:43], v[140:143], v[184:187], v[40:43]
	v_mfma_f32_16x16x32_f16 v[32:35], v[132:135], v[192:195], v[32:35]
	v_mfma_f32_16x16x32_f16 v[24:27], v[140:143], v[192:195], v[24:27]
	v_mfma_f32_16x16x32_f16 v[16:19], v[132:135], v[200:203], v[16:19]
	v_mfma_f32_16x16x32_f16 v[8:11], v[140:143], v[200:203], v[8:11]
	s_barrier
	s_setprio 0
	s_add_u32 s30, s30, 0xc080
	s_addc_u32 s31, s31, 0
	s_add_i32 s34, s34, s42
	v_lshl_add_u64 v[128:129], s[30:31], 0, v[146:147]
	s_mov_b32 m0, s34
	s_nop 0
	global_load_lds_dwordx4 v[128:129], off
	v_lshl_add_u64 v[128:129], s[30:31], 0, v[150:151]
	s_add_i32 m0, s34, 0x2000
	s_nop 0
	global_load_lds_dwordx4 v[128:129], off
	s_waitcnt vmcnt(6)
	s_setprio 1
	s_barrier
	v_mfma_f32_16x16x32_f16 v[52:55], v[204:207], v[158:161], v[52:55]
	v_mfma_f32_16x16x32_f16 v[44:47], v[212:215], v[158:161], v[44:47]
	v_mfma_f32_16x16x32_f16 v[36:39], v[204:207], v[180:183], v[36:39]
	v_mfma_f32_16x16x32_f16 v[28:31], v[212:215], v[180:183], v[28:31]
	v_mfma_f32_16x16x32_f16 v[20:23], v[204:207], v[188:191], v[20:23]
	v_mfma_f32_16x16x32_f16 v[12:15], v[212:215], v[188:191], v[12:15]
	v_mfma_f32_16x16x32_f16 v[4:7], v[204:207], v[196:199], v[4:7]
	v_mfma_f32_16x16x32_f16 v[0:3], v[212:215], v[196:199], v[0:3]
	v_mfma_f32_16x16x32_f16 v[52:55], v[208:211], v[176:179], v[52:55]
	v_mfma_f32_16x16x32_f16 v[44:47], v[216:219], v[176:179], v[44:47]
	v_mfma_f32_16x16x32_f16 v[36:39], v[208:211], v[184:187], v[36:39]
	v_mfma_f32_16x16x32_f16 v[28:31], v[216:219], v[184:187], v[28:31]
	v_mfma_f32_16x16x32_f16 v[20:23], v[208:211], v[192:195], v[20:23]
	v_mfma_f32_16x16x32_f16 v[12:15], v[216:219], v[192:195], v[12:15]
	v_mfma_f32_16x16x32_f16 v[4:7], v[208:211], v[200:203], v[4:7]
	v_mfma_f32_16x16x32_f16 v[0:3], v[216:219], v[200:203], v[0:3]
	s_barrier
	s_setprio 0
	s_add_i32 s73, s73, 2
	s_add_u32 s28, s28, 0x100
	s_addc_u32 s29, s29, 0
	s_add_u32 s71, s71, 0x100
	s_addc_u32 s72, s72, 0
	s_cmp_gt_u32 s73, 9
	s_cbranch_scc0 .LBB7_27
	s_lshl_b32 s28, s70, 8
	s_add_i32 s28, s28, s48
	s_lshl_b32 s29, s67, 8
	s_or_b32 s29, s29, s51
	s_waitcnt vmcnt(6)
	v_pk_fma_f32 v[126:127], v[126:127], v[226:227], v[236:237] op_sel_hi:[1,0,1]
	v_pk_fma_f32 v[124:125], v[124:125], v[226:227], v[234:235] op_sel_hi:[1,0,1]
	v_pk_fma_f32 v[186:187], v[122:123], v[226:227], v[240:241] op_sel_hi:[1,0,1]
	v_pk_fma_f32 v[122:123], v[120:121], v[226:227], v[238:239] op_sel_hi:[1,0,1]
	v_cvt_pk_f16_f32 v120, v124, v125
	v_cvt_pk_f16_f32 v121, v126, v127
	v_cvt_pk_f16_f32 v122, v122, v123
	v_cvt_pk_f16_f32 v123, v186, v187
	ds_write_b128 v173, v[120:123]
	v_pk_fma_f32 v[118:119], v[118:119], v[226:227], v[244:245] op_sel_hi:[1,0,1]
	v_pk_fma_f32 v[116:117], v[116:117], v[226:227], v[242:243] op_sel_hi:[1,0,1]
	v_pk_fma_f32 v[120:121], v[114:115], v[226:227], v[248:249] op_sel_hi:[1,0,1]
	v_pk_fma_f32 v[114:115], v[112:113], v[226:227], v[246:247] op_sel_hi:[1,0,1]
	v_cvt_pk_f16_f32 v112, v116, v117
	v_cvt_pk_f16_f32 v113, v118, v119
	v_cvt_pk_f16_f32 v114, v114, v115
	v_cvt_pk_f16_f32 v115, v120, v121
	ds_write_b128 v173, v[112:115] offset:64
	v_or_b32_e32 v116, s28, v167
	ds_read_b128 v[112:115], v174
	v_mul_lo_u32 v116, v116, s10
	v_add_u32_e32 v120, s29, v116
	v_lshlrev_b32_e32 v121, 1, v120
	v_add_u32_e32 v122, v121, v168
	ds_read_b128 v[116:119], v174 offset:1152
	s_waitcnt lgkmcnt(0)
	buffer_store_dwordx4 v[112:115], v122, s[20:23], 0 offen nt
	v_pk_fma_f32 v[110:111], v[110:111], v[226:227], v[236:237] op_sel:[0,1,0]
	v_pk_fma_f32 v[108:109], v[108:109], v[226:227], v[234:235] op_sel:[0,1,0]
	v_pk_fma_f32 v[112:113], v[106:107], v[226:227], v[240:241] op_sel:[0,1,0]
	v_pk_fma_f32 v[106:107], v[104:105], v[226:227], v[238:239] op_sel:[0,1,0]
	v_cvt_pk_f16_f32 v104, v108, v109
	v_cvt_pk_f16_f32 v105, v110, v111
	v_cvt_pk_f16_f32 v106, v106, v107
	v_cvt_pk_f16_f32 v107, v112, v113
	ds_write_b128 v173, v[104:107]
	v_pk_fma_f32 v[102:103], v[102:103], v[226:227], v[244:245] op_sel:[0,1,0]
	v_pk_fma_f32 v[100:101], v[100:101], v[226:227], v[242:243] op_sel:[0,1,0]
	v_pk_fma_f32 v[104:105], v[94:95], v[226:227], v[248:249] op_sel:[0,1,0]
	v_pk_fma_f32 v[94:95], v[92:93], v[226:227], v[246:247] op_sel:[0,1,0]
	v_cvt_pk_f16_f32 v92, v100, v101
	v_cvt_pk_f16_f32 v93, v102, v103
	v_cvt_pk_f16_f32 v94, v94, v95
	v_cvt_pk_f16_f32 v95, v104, v105
	ds_write_b128 v173, v[92:95] offset:64
	ds_read_b128 v[92:95], v174
	ds_read_b128 v[100:103], v174 offset:1152
	v_add_u32_e32 v104, s55, v121
	v_add_u32_e32 v114, v121, v169
	v_add_u32_e32 v105, v104, v168
	buffer_store_dwordx4 v[116:119], v114, s[20:23], 0 offen nt
	s_waitcnt lgkmcnt(1)
	buffer_store_dwordx4 v[92:95], v105, s[20:23], 0 offen nt
	v_pk_fma_f32 v[86:87], v[86:87], v[228:229], v[244:245] op_sel_hi:[1,0,1]
	v_pk_fma_f32 v[84:85], v[84:85], v[228:229], v[242:243] op_sel_hi:[1,0,1]
	v_pk_fma_f32 v[92:93], v[98:99], v[228:229], v[236:237] op_sel_hi:[1,0,1]
	v_pk_fma_f32 v[94:95], v[96:97], v[228:229], v[234:235] op_sel_hi:[1,0,1]
	v_pk_fma_f32 v[96:97], v[90:91], v[228:229], v[240:241] op_sel_hi:[1,0,1]
	v_pk_fma_f32 v[90:91], v[88:89], v[228:229], v[238:239] op_sel_hi:[1,0,1]
	v_cvt_pk_f16_f32 v88, v94, v95
	v_cvt_pk_f16_f32 v89, v92, v93
	v_cvt_pk_f16_f32 v90, v90, v91
	v_cvt_pk_f16_f32 v91, v96, v97
	ds_write_b128 v173, v[88:91]
	v_pk_fma_f32 v[88:89], v[78:79], v[228:229], v[248:249] op_sel_hi:[1,0,1]
	v_pk_fma_f32 v[78:79], v[76:77], v[228:229], v[246:247] op_sel_hi:[1,0,1]
	v_cvt_pk_f16_f32 v76, v84, v85
	v_cvt_pk_f16_f32 v77, v86, v87
	v_cvt_pk_f16_f32 v78, v78, v79
	v_cvt_pk_f16_f32 v79, v88, v89
	ds_write_b128 v173, v[76:79] offset:64
	ds_read_b128 v[76:79], v174
	ds_read_b128 v[84:87], v174 offset:1152
	v_add_u32_e32 v88, s55, v104
	v_add_u32_e32 v105, v104, v169
	v_add_u32_e32 v89, v88, v168
	s_waitcnt lgkmcnt(4)
	buffer_store_dwordx4 v[100:103], v105, s[20:23], 0 offen nt
	s_waitcnt lgkmcnt(1)
	buffer_store_dwordx4 v[76:79], v89, s[20:23], 0 offen nt
	v_pk_fma_f32 v[70:71], v[70:71], v[228:229], v[244:245] op_sel:[0,1,0]
	v_pk_fma_f32 v[68:69], v[68:69], v[228:229], v[242:243] op_sel:[0,1,0]
	v_add_u32_e32 v76, v88, v169
	s_waitcnt lgkmcnt(0)
	buffer_store_dwordx4 v[84:87], v76, s[20:23], 0 offen nt
	v_pk_fma_f32 v[76:77], v[82:83], v[228:229], v[236:237] op_sel:[0,1,0]
	v_pk_fma_f32 v[78:79], v[80:81], v[228:229], v[234:235] op_sel:[0,1,0]
	v_pk_fma_f32 v[80:81], v[74:75], v[228:229], v[240:241] op_sel:[0,1,0]
	v_pk_fma_f32 v[74:75], v[72:73], v[228:229], v[238:239] op_sel:[0,1,0]
	v_cvt_pk_f16_f32 v72, v78, v79
	v_cvt_pk_f16_f32 v73, v76, v77
	v_cvt_pk_f16_f32 v74, v74, v75
	v_cvt_pk_f16_f32 v75, v80, v81
	ds_write_b128 v173, v[72:75]
	v_pk_fma_f32 v[72:73], v[66:67], v[228:229], v[248:249] op_sel:[0,1,0]
	v_pk_fma_f32 v[66:67], v[64:65], v[228:229], v[246:247] op_sel:[0,1,0]
	v_cvt_pk_f16_f32 v64, v68, v69
	v_cvt_pk_f16_f32 v65, v70, v71
	v_cvt_pk_f16_f32 v66, v66, v67
	v_cvt_pk_f16_f32 v67, v72, v73
	ds_write_b128 v173, v[64:67] offset:64
	ds_read_b128 v[64:67], v174
	ds_read_b128 v[68:71], v174 offset:1152
	v_add_u32_e32 v72, s56, v120
	v_lshlrev_b32_e32 v73, 1, v72
	v_add_u32_e32 v74, v73, v168
	s_waitcnt lgkmcnt(1)
	buffer_store_dwordx4 v[64:67], v74, s[20:23], 0 offen nt
	v_pk_fma_f32 v[62:63], v[62:63], v[230:231], v[236:237] op_sel_hi:[1,0,1]
	v_pk_fma_f32 v[60:61], v[60:61], v[230:231], v[234:235] op_sel_hi:[1,0,1]
	v_pk_fma_f32 v[64:65], v[58:59], v[230:231], v[240:241] op_sel_hi:[1,0,1]
	v_pk_fma_f32 v[58:59], v[56:57], v[230:231], v[238:239] op_sel_hi:[1,0,1]
	v_cvt_pk_f16_f32 v56, v60, v61
	v_cvt_pk_f16_f32 v57, v62, v63
	v_cvt_pk_f16_f32 v58, v58, v59
	v_cvt_pk_f16_f32 v59, v64, v65
	ds_write_b128 v173, v[56:59]
	v_pk_fma_f32 v[54:55], v[54:55], v[230:231], v[244:245] op_sel_hi:[1,0,1]
	v_pk_fma_f32 v[52:53], v[52:53], v[230:231], v[242:243] op_sel_hi:[1,0,1]
	v_pk_fma_f32 v[56:57], v[46:47], v[230:231], v[248:249] op_sel_hi:[1,0,1]
	v_pk_fma_f32 v[46:47], v[44:45], v[230:231], v[246:247] op_sel_hi:[1,0,1]
	v_cvt_pk_f16_f32 v44, v52, v53
	v_cvt_pk_f16_f32 v45, v54, v55
	v_cvt_pk_f16_f32 v46, v46, v47
	v_cvt_pk_f16_f32 v47, v56, v57
	ds_write_b128 v173, v[44:47] offset:64
	ds_read_b128 v[44:47], v174
	ds_read_b128 v[52:55], v174 offset:1152
	v_add_u32_e32 v56, s62, v88
	v_add_u32_e32 v66, v73, v169
	v_add_u32_e32 v57, v56, v168
	s_waitcnt lgkmcnt(4)
	buffer_store_dwordx4 v[68:71], v66, s[20:23], 0 offen nt
	s_waitcnt lgkmcnt(1)
	buffer_store_dwordx4 v[44:47], v57, s[20:23], 0 offen nt
	v_pk_fma_f32 v[38:39], v[38:39], v[230:231], v[244:245] op_sel:[0,1,0]
	v_pk_fma_f32 v[36:37], v[36:37], v[230:231], v[242:243] op_sel:[0,1,0]
	v_add_u32_e32 v44, v56, v169
	s_waitcnt lgkmcnt(0)
	buffer_store_dwordx4 v[52:55], v44, s[20:23], 0 offen nt
	v_pk_fma_f32 v[44:45], v[50:51], v[230:231], v[236:237] op_sel:[0,1,0]
	v_pk_fma_f32 v[46:47], v[48:49], v[230:231], v[234:235] op_sel:[0,1,0]
	v_pk_fma_f32 v[48:49], v[42:43], v[230:231], v[240:241] op_sel:[0,1,0]
	v_pk_fma_f32 v[42:43], v[40:41], v[230:231], v[238:239] op_sel:[0,1,0]
	v_cvt_pk_f16_f32 v40, v46, v47
	v_cvt_pk_f16_f32 v41, v44, v45
	v_cvt_pk_f16_f32 v42, v42, v43
	v_cvt_pk_f16_f32 v43, v48, v49
	ds_write_b128 v173, v[40:43]
	v_pk_fma_f32 v[40:41], v[30:31], v[230:231], v[248:249] op_sel:[0,1,0]
	v_pk_fma_f32 v[30:31], v[28:29], v[230:231], v[246:247] op_sel:[0,1,0]
	v_cvt_pk_f16_f32 v28, v36, v37
	v_cvt_pk_f16_f32 v29, v38, v39
	v_cvt_pk_f16_f32 v30, v30, v31
	v_cvt_pk_f16_f32 v31, v40, v41
	ds_write_b128 v173, v[28:31] offset:64
	ds_read_b128 v[28:31], v174
	ds_read_b128 v[36:39], v174 offset:1152
	v_add_u32_e32 v40, s63, v72
	v_lshlrev_b32_e32 v41, 1, v40
	v_add_u32_e32 v42, v41, v168
	s_waitcnt lgkmcnt(1)
	buffer_store_dwordx4 v[28:31], v42, s[20:23], 0 offen nt
	v_pk_fma_f32 v[22:23], v[22:23], v[232:233], v[244:245] op_sel_hi:[1,0,1]
	v_pk_fma_f32 v[20:21], v[20:21], v[232:233], v[242:243] op_sel_hi:[1,0,1]
	v_add_u32_e32 v28, v41, v169
	s_waitcnt lgkmcnt(0)
	buffer_store_dwordx4 v[36:39], v28, s[20:23], 0 offen nt
	v_pk_fma_f32 v[28:29], v[34:35], v[232:233], v[236:237] op_sel_hi:[1,0,1]
	v_pk_fma_f32 v[30:31], v[32:33], v[232:233], v[234:235] op_sel_hi:[1,0,1]
	v_pk_fma_f32 v[32:33], v[26:27], v[232:233], v[240:241] op_sel_hi:[1,0,1]
	v_pk_fma_f32 v[26:27], v[24:25], v[232:233], v[238:239] op_sel_hi:[1,0,1]
	v_cvt_pk_f16_f32 v24, v30, v31
	v_cvt_pk_f16_f32 v25, v28, v29
	v_cvt_pk_f16_f32 v26, v26, v27
	v_cvt_pk_f16_f32 v27, v32, v33
	ds_write_b128 v173, v[24:27]
	v_pk_fma_f32 v[24:25], v[14:15], v[232:233], v[248:249] op_sel_hi:[1,0,1]
	v_pk_fma_f32 v[14:15], v[12:13], v[232:233], v[246:247] op_sel_hi:[1,0,1]
	v_cvt_pk_f16_f32 v12, v20, v21
	v_cvt_pk_f16_f32 v13, v22, v23
	v_cvt_pk_f16_f32 v14, v14, v15
	v_cvt_pk_f16_f32 v15, v24, v25
	ds_write_b128 v173, v[12:15] offset:64
	ds_read_b128 v[12:15], v174
	ds_read_b128 v[20:23], v174 offset:1152
	v_add_u32_e32 v24, s64, v40
	v_lshlrev_b32_e32 v25, 1, v24
	v_add_u32_e32 v26, v25, v168
	s_waitcnt lgkmcnt(1)
	buffer_store_dwordx4 v[12:15], v26, s[20:23], 0 offen nt
	v_pk_fma_f32 v[6:7], v[6:7], v[232:233], v[244:245] op_sel:[0,1,0]
	v_pk_fma_f32 v[4:5], v[4:5], v[232:233], v[242:243] op_sel:[0,1,0]
	v_pk_fma_f32 v[12:13], v[18:19], v[232:233], v[236:237] op_sel:[0,1,0]
	v_pk_fma_f32 v[14:15], v[16:17], v[232:233], v[234:235] op_sel:[0,1,0]
	v_pk_fma_f32 v[16:17], v[10:11], v[232:233], v[240:241] op_sel:[0,1,0]
	v_pk_fma_f32 v[10:11], v[8:9], v[232:233], v[238:239] op_sel:[0,1,0]
	v_cvt_pk_f16_f32 v8, v14, v15
	v_cvt_pk_f16_f32 v9, v12, v13
	v_cvt_pk_f16_f32 v10, v10, v11
	v_cvt_pk_f16_f32 v11, v16, v17
	ds_write_b128 v173, v[8:11]
	v_pk_fma_f32 v[8:9], v[2:3], v[232:233], v[248:249] op_sel:[0,1,0]
	v_pk_fma_f32 v[2:3], v[0:1], v[232:233], v[246:247] op_sel:[0,1,0]
	v_cvt_pk_f16_f32 v0, v4, v5
	v_cvt_pk_f16_f32 v1, v6, v7
	v_cvt_pk_f16_f32 v2, v2, v3
	v_cvt_pk_f16_f32 v3, v8, v9
	ds_write_b128 v173, v[0:3] offset:64
	ds_read_b128 v[0:3], v174
	ds_read_b128 v[4:7], v174 offset:1152
	v_add_lshl_u32 v8, v24, s64, 1
	v_add_u32_e32 v25, v25, v169
	v_add_u32_e32 v9, v8, v168
	s_waitcnt lgkmcnt(4)
	buffer_store_dwordx4 v[20:23], v25, s[20:23], 0 offen nt
	s_waitcnt lgkmcnt(1)
	buffer_store_dwordx4 v[0:3], v9, s[20:23], 0 offen nt
	s_mov_b32 s67, s68
	s_mov_b32 s70, s69
	v_add_u32_e32 v0, v8, v169
	s_mov_b64 s[30:31], s[0:1]
	s_mov_b64 s[28:29], s[8:9]
	s_mov_b64 vcc, s[6:7]
	s_waitcnt lgkmcnt(0)
	buffer_store_dwordx4 v[4:7], v0, s[20:23], 0 offen nt
	s_cbranch_vccz .LBB7_12
	s_waitcnt vmcnt(0)
	s_cmpk_gt_u32 s36, 0xff
	s_cbranch_scc1 .LBB7_31
	s_barrier

.LBB7_32:
	s_endpgm
	s_endpgm
	s_endpgm
	s_endpgm
	s_endpgm
	s_endpgm
	s_endpgm
	s_endpgm
	s_endpgm
	s_endpgm
	s_endpgm
	s_endpgm
	s_endpgm
	s_endpgm
	s_endpgm
	s_endpgm
	s_endpgm
	s_endpgm
	s_endpgm
	s_endpgm
	s_endpgm
	s_endpgm
	s_endpgm
	s_endpgm
	s_endpgm
	s_endpgm
	s_endpgm
	s_endpgm
	s_endpgm
	s_endpgm
	s_endpgm
	s_endpgm
	s_endpgm
	s_endpgm
	s_endpgm
	s_endpgm
	s_endpgm
	s_endpgm
	s_endpgm
	s_endpgm
	s_endpgm
	s_endpgm
	s_endpgm
	s_endpgm
	s_endpgm
	s_endpgm
	s_endpgm
	s_endpgm
	s_endpgm
	s_endpgm
	s_endpgm
	s_endpgm
	s_endpgm
	s_endpgm
	s_endpgm
	s_endpgm
	s_endpgm
	s_endpgm
	s_endpgm
	s_endpgm
	s_endpgm

.LBB8_27:
	ds_read_b128 v[72:75], v231
	ds_read_b128 v[80:83], v231 offset:1024
	ds_read_b128 v[88:91], v231 offset:2048
	ds_read_b128 v[92:95], v231 offset:3072
	s_add_u32 s40, s38, 0xfffd0080
	s_addc_u32 s41, s39, -1
	s_cmp_eq_u32 s87, 8
	s_cselect_b32 s43, s9, s41
	s_cselect_b32 s42, s8, s40
	s_cselect_b32 s41, s1, s86
	s_cselect_b32 s40, s0, s85
	v_lshl_add_u64 v[190:191], s[38:39], 0, v[184:185]
	s_add_i32 m0, s51, 0xc000
	ds_read_b128 v[136:139], v232
	ds_read_b128 v[148:151], v232 offset:1024
	ds_read_b128 v[152:155], v232 offset:2048
	ds_read_b128 v[156:159], v232 offset:3072
	ds_read_b128 v[160:163], v232 offset:4096
	ds_read_b128 v[164:167], v232 offset:5120
	ds_read_b128 v[168:171], v232 offset:6144
	ds_read_b128 v[172:175], v232 offset:7168
	global_load_lds_dwordx4 v[190:191], off
	v_lshl_add_u64 v[190:191], s[38:39], 0, v[186:187]
	s_add_i32 m0, s51, 0xe000
	s_nop 0
	global_load_lds_dwordx4 v[190:191], off
	s_waitcnt lgkmcnt(8)
	s_setprio 1
	s_barrier
	s_waitcnt lgkmcnt(0)
	v_mfma_f32_16x16x32_f16 v[144:147], v[72:75], v[136:139], v[144:147]
	v_mfma_f32_16x16x32_f16 v[140:143], v[88:91], v[136:139], v[140:143]
	v_mfma_f32_16x16x32_f16 v[124:127], v[72:75], v[152:155], v[124:127]
	v_mfma_f32_16x16x32_f16 v[120:123], v[88:91], v[152:155], v[120:123]
	v_mfma_f32_16x16x32_f16 v[108:111], v[72:75], v[160:163], v[108:111]
	v_mfma_f32_16x16x32_f16 v[104:107], v[88:91], v[160:163], v[104:107]
	v_mfma_f32_16x16x32_f16 v[84:87], v[72:75], v[168:171], v[84:87]
	v_mfma_f32_16x16x32_f16 v[76:79], v[88:91], v[168:171], v[76:79]
	v_mfma_f32_16x16x32_f16 v[144:147], v[80:83], v[148:151], v[144:147]
	v_mfma_f32_16x16x32_f16 v[140:143], v[92:95], v[148:151], v[140:143]
	v_mfma_f32_16x16x32_f16 v[124:127], v[80:83], v[156:159], v[124:127]
	v_mfma_f32_16x16x32_f16 v[120:123], v[92:95], v[156:159], v[120:123]
	v_mfma_f32_16x16x32_f16 v[108:111], v[80:83], v[164:167], v[108:111]
	v_mfma_f32_16x16x32_f16 v[104:107], v[92:95], v[164:167], v[104:107]
	v_mfma_f32_16x16x32_f16 v[84:87], v[80:83], v[172:175], v[84:87]
	v_mfma_f32_16x16x32_f16 v[76:79], v[92:95], v[172:175], v[76:79]
	s_barrier
	s_setprio 0
	s_add_i32 s88, s70, s50
	v_lshl_add_u64 v[206:207], s[40:41], 0, v[178:179]
	s_mov_b32 m0, s88
	ds_read_b128 v[190:193], v233
	ds_read_b128 v[194:197], v233 offset:1024
	ds_read_b128 v[198:201], v233 offset:2048
	ds_read_b128 v[202:205], v233 offset:3072
	global_load_lds_dwordx4 v[206:207], off
	v_lshl_add_u64 v[208:209], s[40:41], 0, v[182:183]
	s_add_i32 m0, s88, 0x2000
	s_nop 0
	global_load_lds_dwordx4 v[208:209], off
	s_setprio 1
	s_barrier
	s_waitcnt lgkmcnt(0)
	v_mfma_f32_16x16x32_f16 v[132:135], v[190:193], v[136:139], v[132:135]
	v_mfma_f32_16x16x32_f16 v[128:131], v[198:201], v[136:139], v[128:131]
	v_mfma_f32_16x16x32_f16 v[116:119], v[190:193], v[152:155], v[116:119]
	v_mfma_f32_16x16x32_f16 v[112:115], v[198:201], v[152:155], v[112:115]
	v_mfma_f32_16x16x32_f16 v[100:103], v[190:193], v[160:163], v[100:103]
	v_mfma_f32_16x16x32_f16 v[96:99], v[198:201], v[160:163], v[96:99]
	v_mfma_f32_16x16x32_f16 v[68:71], v[190:193], v[168:171], v[68:71]
	v_mfma_f32_16x16x32_f16 v[64:67], v[198:201], v[168:171], v[64:67]
	v_mfma_f32_16x16x32_f16 v[132:135], v[194:197], v[148:151], v[132:135]
	v_mfma_f32_16x16x32_f16 v[128:131], v[202:205], v[148:151], v[128:131]
	v_mfma_f32_16x16x32_f16 v[116:119], v[194:197], v[156:159], v[116:119]
	v_mfma_f32_16x16x32_f16 v[112:115], v[202:205], v[156:159], v[112:115]
	v_mfma_f32_16x16x32_f16 v[100:103], v[194:197], v[164:167], v[100:103]
	v_mfma_f32_16x16x32_f16 v[96:99], v[202:205], v[164:167], v[96:99]
	v_mfma_f32_16x16x32_f16 v[68:71], v[194:197], v[172:175], v[68:71]
	v_mfma_f32_16x16x32_f16 v[64:67], v[202:205], v[172:175], v[64:67]
	s_barrier
	s_setprio 0
	s_mov_b32 m0, s51
	v_lshl_add_u64 v[210:211], s[42:43], 0, v[176:177]
	ds_read_b128 v[136:139], v232 offset:16384
	ds_read_b128 v[148:151], v232 offset:17408
	ds_read_b128 v[152:155], v232 offset:18432
	ds_read_b128 v[156:159], v232 offset:19456
	ds_read_b128 v[160:163], v232 offset:20480
	ds_read_b128 v[164:167], v232 offset:21504
	ds_read_b128 v[168:171], v232 offset:22528
	ds_read_b128 v[172:175], v232 offset:23552
	global_load_lds_dwordx4 v[210:211], off
	v_lshl_add_u64 v[212:213], s[42:43], 0, v[180:181]
	s_mov_b32 m0, s52
	s_nop 0
	global_load_lds_dwordx4 v[212:213], off
	s_setprio 1
	s_barrier
	s_waitcnt lgkmcnt(0)
	v_mfma_f32_16x16x32_f16 v[60:63], v[72:75], v[136:139], v[60:63]
	v_mfma_f32_16x16x32_f16 v[56:59], v[88:91], v[136:139], v[56:59]
	v_mfma_f32_16x16x32_f16 v[44:47], v[72:75], v[152:155], v[44:47]
	v_mfma_f32_16x16x32_f16 v[40:43], v[88:91], v[152:155], v[40:43]
	v_mfma_f32_16x16x32_f16 v[28:31], v[72:75], v[160:163], v[28:31]
	v_mfma_f32_16x16x32_f16 v[24:27], v[88:91], v[160:163], v[24:27]
	v_mfma_f32_16x16x32_f16 v[12:15], v[72:75], v[168:171], v[12:15]
	v_mfma_f32_16x16x32_f16 v[8:11], v[88:91], v[168:171], v[8:11]
	v_mfma_f32_16x16x32_f16 v[60:63], v[80:83], v[148:151], v[60:63]
	v_mfma_f32_16x16x32_f16 v[56:59], v[92:95], v[148:151], v[56:59]
	v_mfma_f32_16x16x32_f16 v[44:47], v[80:83], v[156:159], v[44:47]
	v_mfma_f32_16x16x32_f16 v[40:43], v[92:95], v[156:159], v[40:43]
	v_mfma_f32_16x16x32_f16 v[28:31], v[80:83], v[164:167], v[28:31]
	v_mfma_f32_16x16x32_f16 v[24:27], v[92:95], v[164:167], v[24:27]
	v_mfma_f32_16x16x32_f16 v[12:15], v[80:83], v[172:175], v[12:15]
	v_mfma_f32_16x16x32_f16 v[8:11], v[92:95], v[172:175], v[8:11]
	s_barrier
	s_setprio 0
	s_add_u32 s88, s40, 0xc000
	s_addc_u32 s89, s41, 0
	s_add_i32 s90, s71, s50
	v_lshl_add_u64 v[72:73], s[88:89], 0, v[178:179]
	s_mov_b32 m0, s90
	s_nop 0
	global_load_lds_dwordx4 v[72:73], off
	v_lshl_add_u64 v[72:73], s[88:89], 0, v[182:183]
	s_add_i32 m0, s90, 0x2000
	s_nop 0
	global_load_lds_dwordx4 v[72:73], off
	s_waitcnt vmcnt(6)
	s_setprio 1
	s_barrier
	v_mfma_f32_16x16x32_f16 v[52:55], v[190:193], v[136:139], v[52:55]
	v_mfma_f32_16x16x32_f16 v[48:51], v[198:201], v[136:139], v[48:51]
	v_mfma_f32_16x16x32_f16 v[36:39], v[190:193], v[152:155], v[36:39]
	v_mfma_f32_16x16x32_f16 v[32:35], v[198:201], v[152:155], v[32:35]
	v_mfma_f32_16x16x32_f16 v[20:23], v[190:193], v[160:163], v[20:23]
	v_mfma_f32_16x16x32_f16 v[16:19], v[198:201], v[160:163], v[16:19]
	v_mfma_f32_16x16x32_f16 v[4:7], v[190:193], v[168:171], v[4:7]
	v_mfma_f32_16x16x32_f16 v[0:3], v[198:201], v[168:171], v[0:3]
	v_mfma_f32_16x16x32_f16 v[52:55], v[194:197], v[148:151], v[52:55]
	v_mfma_f32_16x16x32_f16 v[48:51], v[202:205], v[148:151], v[48:51]
	v_mfma_f32_16x16x32_f16 v[36:39], v[194:197], v[156:159], v[36:39]
	v_mfma_f32_16x16x32_f16 v[32:35], v[202:205], v[156:159], v[32:35]
	v_mfma_f32_16x16x32_f16 v[20:23], v[194:197], v[164:167], v[20:23]
	v_mfma_f32_16x16x32_f16 v[16:19], v[202:205], v[164:167], v[16:19]
	v_mfma_f32_16x16x32_f16 v[4:7], v[194:197], v[172:175], v[4:7]
	v_mfma_f32_16x16x32_f16 v[0:3], v[202:205], v[172:175], v[0:3]
	s_barrier
	s_setprio 0
	s_add_i32 s88, 0, 0x18000
	v_add_u32_e32 v92, s88, v228
	ds_read_b128 v[72:75], v92
	ds_read_b128 v[80:83], v92 offset:1024
	ds_read_b128 v[88:91], v92 offset:2048
	ds_read_b128 v[92:95], v92 offset:3072
	s_add_u32 s42, s42, 0x30000
	s_addc_u32 s43, s43, 0
	s_mov_b32 m0, s53
	v_lshl_add_u64 v[190:191], s[42:43], 0, v[176:177]
	ds_read_b128 v[136:139], v232 offset:32768
	ds_read_b128 v[148:151], v232 offset:33792
	ds_read_b128 v[152:155], v232 offset:34816
	ds_read_b128 v[156:159], v232 offset:35840
	ds_read_b128 v[160:163], v232 offset:36864
	ds_read_b128 v[164:167], v232 offset:37888
	ds_read_b128 v[168:171], v232 offset:38912
	ds_read_b128 v[172:175], v232 offset:39936
	global_load_lds_dwordx4 v[190:191], off
	v_lshl_add_u64 v[190:191], s[42:43], 0, v[180:181]
	s_mov_b32 m0, s54
	s_nop 0
	global_load_lds_dwordx4 v[190:191], off
	s_waitcnt lgkmcnt(8)
	s_setprio 1
	s_barrier
	s_waitcnt lgkmcnt(0)
	v_mfma_f32_16x16x32_f16 v[144:147], v[72:75], v[136:139], v[144:147]
	v_mfma_f32_16x16x32_f16 v[140:143], v[88:91], v[136:139], v[140:143]
	v_mfma_f32_16x16x32_f16 v[124:127], v[72:75], v[152:155], v[124:127]
	v_mfma_f32_16x16x32_f16 v[120:123], v[88:91], v[152:155], v[120:123]
	v_mfma_f32_16x16x32_f16 v[108:111], v[72:75], v[160:163], v[108:111]
	v_mfma_f32_16x16x32_f16 v[104:107], v[88:91], v[160:163], v[104:107]
	v_mfma_f32_16x16x32_f16 v[84:87], v[72:75], v[168:171], v[84:87]
	v_mfma_f32_16x16x32_f16 v[76:79], v[88:91], v[168:171], v[76:79]
	v_mfma_f32_16x16x32_f16 v[144:147], v[80:83], v[148:151], v[144:147]
	v_mfma_f32_16x16x32_f16 v[140:143], v[92:95], v[148:151], v[140:143]
	v_mfma_f32_16x16x32_f16 v[124:127], v[80:83], v[156:159], v[124:127]
	v_mfma_f32_16x16x32_f16 v[120:123], v[92:95], v[156:159], v[120:123]
	v_mfma_f32_16x16x32_f16 v[108:111], v[80:83], v[164:167], v[108:111]
	v_mfma_f32_16x16x32_f16 v[104:107], v[92:95], v[164:167], v[104:107]
	v_mfma_f32_16x16x32_f16 v[84:87], v[80:83], v[172:175], v[84:87]
	v_mfma_f32_16x16x32_f16 v[76:79], v[92:95], v[172:175], v[76:79]
	s_barrier
	s_setprio 0
	s_add_i32 s42, 0, 0x1c000
	s_add_i32 s43, s88, s50
	v_add_u32_e32 v202, s42, v228
	v_lshl_add_u64 v[206:207], v[206:207], 0, s[36:37]
	s_mov_b32 m0, s43
	ds_read_b128 v[190:193], v202
	ds_read_b128 v[194:197], v202 offset:1024
	ds_read_b128 v[198:201], v202 offset:2048
	ds_read_b128 v[202:205], v202 offset:3072
	global_load_lds_dwordx4 v[206:207], off
	v_lshl_add_u64 v[206:207], v[208:209], 0, s[36:37]
	s_add_i32 m0, s43, 0x2000
	s_nop 0
	global_load_lds_dwordx4 v[206:207], off
	s_setprio 1
	s_barrier
	s_waitcnt lgkmcnt(0)
	v_mfma_f32_16x16x32_f16 v[132:135], v[190:193], v[136:139], v[132:135]
	v_mfma_f32_16x16x32_f16 v[128:131], v[198:201], v[136:139], v[128:131]
	v_mfma_f32_16x16x32_f16 v[116:119], v[190:193], v[152:155], v[116:119]
	v_mfma_f32_16x16x32_f16 v[112:115], v[198:201], v[152:155], v[112:115]
	v_mfma_f32_16x16x32_f16 v[100:103], v[190:193], v[160:163], v[100:103]
	v_mfma_f32_16x16x32_f16 v[96:99], v[198:201], v[160:163], v[96:99]
	v_mfma_f32_16x16x32_f16 v[68:71], v[190:193], v[168:171], v[68:71]
	v_mfma_f32_16x16x32_f16 v[64:67], v[198:201], v[168:171], v[64:67]
	v_mfma_f32_16x16x32_f16 v[132:135], v[194:197], v[148:151], v[132:135]
	v_mfma_f32_16x16x32_f16 v[128:131], v[202:205], v[148:151], v[128:131]
	v_mfma_f32_16x16x32_f16 v[116:119], v[194:197], v[156:159], v[116:119]
	v_mfma_f32_16x16x32_f16 v[112:115], v[202:205], v[156:159], v[112:115]
	v_mfma_f32_16x16x32_f16 v[100:103], v[194:197], v[164:167], v[100:103]
	v_mfma_f32_16x16x32_f16 v[96:99], v[202:205], v[164:167], v[96:99]
	v_mfma_f32_16x16x32_f16 v[68:71], v[194:197], v[172:175], v[68:71]
	v_mfma_f32_16x16x32_f16 v[64:67], v[202:205], v[172:175], v[64:67]
	s_barrier
	s_setprio 0
	s_mov_b32 m0, s59
	v_lshl_add_u64 v[206:207], v[210:211], 0, s[36:37]
	ds_read_b128 v[136:139], v232 offset:49152
	ds_read_b128 v[148:151], v232 offset:50176
	ds_read_b128 v[152:155], v232 offset:51200
	ds_read_b128 v[156:159], v232 offset:52224
	ds_read_b128 v[160:163], v232 offset:53248
	ds_read_b128 v[164:167], v232 offset:54272
	ds_read_b128 v[168:171], v232 offset:55296
	ds_read_b128 v[172:175], v232 offset:56320
	global_load_lds_dwordx4 v[206:207], off
	v_lshl_add_u64 v[206:207], v[212:213], 0, s[36:37]
	s_mov_b32 m0, s60
	s_nop 0
	global_load_lds_dwordx4 v[206:207], off
	s_setprio 1
	s_barrier
	s_waitcnt lgkmcnt(0)
	v_mfma_f32_16x16x32_f16 v[60:63], v[72:75], v[136:139], v[60:63]
	v_mfma_f32_16x16x32_f16 v[56:59], v[88:91], v[136:139], v[56:59]
	v_mfma_f32_16x16x32_f16 v[44:47], v[72:75], v[152:155], v[44:47]
	v_mfma_f32_16x16x32_f16 v[40:43], v[88:91], v[152:155], v[40:43]
	v_mfma_f32_16x16x32_f16 v[28:31], v[72:75], v[160:163], v[28:31]
	v_mfma_f32_16x16x32_f16 v[24:27], v[88:91], v[160:163], v[24:27]
	v_mfma_f32_16x16x32_f16 v[12:15], v[72:75], v[168:171], v[12:15]
	v_mfma_f32_16x16x32_f16 v[8:11], v[88:91], v[168:171], v[8:11]
	v_mfma_f32_16x16x32_f16 v[60:63], v[80:83], v[148:151], v[60:63]
	v_mfma_f32_16x16x32_f16 v[56:59], v[92:95], v[148:151], v[56:59]
	v_mfma_f32_16x16x32_f16 v[44:47], v[80:83], v[156:159], v[44:47]
	v_mfma_f32_16x16x32_f16 v[40:43], v[92:95], v[156:159], v[40:43]
	v_mfma_f32_16x16x32_f16 v[28:31], v[80:83], v[164:167], v[28:31]
	v_mfma_f32_16x16x32_f16 v[24:27], v[92:95], v[164:167], v[24:27]
	v_mfma_f32_16x16x32_f16 v[12:15], v[80:83], v[172:175], v[12:15]
	v_mfma_f32_16x16x32_f16 v[8:11], v[92:95], v[172:175], v[8:11]
	s_barrier
	s_setprio 0
	s_add_u32 s40, s40, 0xc080
	s_addc_u32 s41, s41, 0
	s_add_i32 s42, s42, s50
	v_lshl_add_u64 v[72:73], s[40:41], 0, v[178:179]
	s_mov_b32 m0, s42
	s_nop 0
	global_load_lds_dwordx4 v[72:73], off
	v_lshl_add_u64 v[72:73], s[40:41], 0, v[182:183]
	s_add_i32 m0, s42, 0x2000
	s_nop 0
	global_load_lds_dwordx4 v[72:73], off
	s_waitcnt vmcnt(6)
	s_setprio 1
	s_barrier
	v_mfma_f32_16x16x32_f16 v[52:55], v[190:193], v[136:139], v[52:55]
	v_mfma_f32_16x16x32_f16 v[48:51], v[198:201], v[136:139], v[48:51]
	v_mfma_f32_16x16x32_f16 v[36:39], v[190:193], v[152:155], v[36:39]
	v_mfma_f32_16x16x32_f16 v[32:35], v[198:201], v[152:155], v[32:35]
	v_mfma_f32_16x16x32_f16 v[20:23], v[190:193], v[160:163], v[20:23]
	v_mfma_f32_16x16x32_f16 v[16:19], v[198:201], v[160:163], v[16:19]
	v_mfma_f32_16x16x32_f16 v[4:7], v[190:193], v[168:171], v[4:7]
	v_mfma_f32_16x16x32_f16 v[0:3], v[198:201], v[168:171], v[0:3]
	v_mfma_f32_16x16x32_f16 v[52:55], v[194:197], v[148:151], v[52:55]
	v_mfma_f32_16x16x32_f16 v[48:51], v[202:205], v[148:151], v[48:51]
	v_mfma_f32_16x16x32_f16 v[36:39], v[194:197], v[156:159], v[36:39]
	v_mfma_f32_16x16x32_f16 v[32:35], v[202:205], v[156:159], v[32:35]
	v_mfma_f32_16x16x32_f16 v[20:23], v[194:197], v[164:167], v[20:23]
	v_mfma_f32_16x16x32_f16 v[16:19], v[202:205], v[164:167], v[16:19]
	v_mfma_f32_16x16x32_f16 v[4:7], v[194:197], v[172:175], v[4:7]
	v_mfma_f32_16x16x32_f16 v[0:3], v[202:205], v[172:175], v[0:3]
	s_barrier
	s_setprio 0
	s_add_i32 s87, s87, 2
	s_add_u32 s38, s38, 0x100
	s_addc_u32 s39, s39, 0
	s_add_u32 s85, s85, 0x100
	s_addc_u32 s86, s86, 0
	s_cmp_gt_u32 s87, 9
	s_cbranch_scc0 .LBB8_27
	s_lshl_b32 s92, s84, 8
	s_add_i32 s92, s92, s58
	s_lshl_b32 s93, s83, 8
	s_or_b32 s93, s93, s61
	v_lshlrev_b32_e32 v237, 2, v226
	s_lshl_b32 s96, s93, 2
	s_add_u32 s94, s16, s96
	s_addc_u32 s95, s17, 0
	global_load_dwordx4 v[72:75], v237, s[94:95] offset:0
	global_load_dwordx4 v[80:83], v237, s[94:95] offset:16
	global_load_dwordx4 v[88:91], v237, s[94:95] offset:128
	global_load_dwordx4 v[92:95], v237, s[94:95] offset:144
	s_add_u32 s94, s18, s96
	s_addc_u32 s95, s19, 0
	global_load_dwordx4 v[136:139], v237, s[94:95] offset:0
	global_load_dwordx4 v[148:151], v237, s[94:95] offset:16
	global_load_dwordx4 v[152:155], v237, s[94:95] offset:128
	global_load_dwordx4 v[156:159], v237, s[94:95] offset:144
	s_add_u32 s94, s14, s96
	s_addc_u32 s95, s15, 0
	global_load_dwordx4 v[160:163], v237, s[94:95] offset:0
	global_load_dwordx4 v[164:167], v237, s[94:95] offset:16
	global_load_dwordx4 v[168:171], v237, s[94:95] offset:128
	global_load_dwordx4 v[172:175], v237, s[94:95] offset:144
	v_lshlrev_b32_e32 v190, 3, v227
	s_lshl_b32 s96, s92, 3
	s_add_u32 s94, s12, s96
	s_addc_u32 s95, s13, 0
	global_load_dwordx2 v[238:239], v190, s[94:95] offset:0
	global_load_dwordx2 v[192:193], v190, s[94:95] offset:128
	global_load_dwordx2 v[194:195], v190, s[94:95] offset:256
	global_load_dwordx2 v[196:197], v190, s[94:95] offset:384
	global_load_dwordx2 v[198:199], v190, s[94:95] offset:1024
	global_load_dwordx2 v[200:201], v190, s[94:95] offset:1152
	global_load_dwordx2 v[202:203], v190, s[94:95] offset:1280
	global_load_dwordx2 v[204:205], v190, s[94:95] offset:1408
	v_mul_u32_u24_e32 v191, 0x600, v227
	v_lshl_add_u32 v191, v226, 1, v191
	s_mul_i32 s96, s92, 0x600
	s_lshl_b32 s97, s93, 1
	s_add_u32 s96, s96, s97
	s_add_u32 s98, s10, s96
	s_addc_u32 s99, s11, 0
	s_add_u32 s94, s98, 0x0
	s_addc_u32 s95, s99, 0
	global_load_dwordx4 v[208:211], v191, s[94:95] offset:0 nt
	global_load_dwordx4 v[212:215], v191, s[94:95] offset:64 nt
	s_add_u32 s94, s98, 0x6000
	s_addc_u32 s95, s99, 0
	global_load_dwordx4 v[216:219], v191, s[94:95] offset:0 nt
	global_load_dwordx4 v[220:223], v191, s[94:95] offset:64 nt
	v_add_u32_e32 v225, s92, v229
	v_mul_u32_u24_e32 v225, 0x600, v225
	s_lshl_b32 s97, s93, 1
	v_add3_u32 v225, v225, v230, s97
	v_mul_u32_u24_e32 v224, 0x60, v227
	s_mul_i32 s96, s92, 0x60
	s_lshl_b32 s97, s83, 5
	s_add_u32 s96, s96, s97
	s_lshr_b32 s97, s61, 3
	s_add_u32 s96, s96, s97
	s_add_u32 s96, s96, 0x800
	s_add_u32 s100, s28, s96
	s_addc_u32 s101, s29, 0
	s_waitcnt vmcnt(19)
	v_pk_add_f32 v[72:73], v[72:73], v[136:137]
	v_pk_add_f32 v[74:75], v[74:75], v[138:139]
	s_waitcnt vmcnt(18)
	v_pk_add_f32 v[80:81], v[80:81], v[148:149]
	v_pk_add_f32 v[82:83], v[82:83], v[150:151]
	s_waitcnt vmcnt(17)
	v_pk_add_f32 v[88:89], v[88:89], v[152:153]
	v_pk_add_f32 v[90:91], v[90:91], v[154:155]
	s_waitcnt vmcnt(16)
	v_pk_add_f32 v[92:93], v[92:93], v[156:157]
	v_pk_add_f32 v[94:95], v[94:95], v[158:159]
	v_pk_add_f32 v[144:145], v[144:145], v[72:73]
	v_pk_add_f32 v[146:147], v[146:147], v[74:75]
	v_pk_add_f32 v[124:125], v[124:125], v[72:73]
	v_pk_add_f32 v[126:127], v[126:127], v[74:75]
	v_pk_add_f32 v[108:109], v[108:109], v[72:73]
	v_pk_add_f32 v[110:111], v[110:111], v[74:75]
	v_pk_add_f32 v[84:85], v[84:85], v[72:73]
	v_pk_add_f32 v[86:87], v[86:87], v[74:75]
	v_pk_add_f32 v[60:61], v[60:61], v[72:73]
	v_pk_add_f32 v[62:63], v[62:63], v[74:75]
	v_pk_add_f32 v[44:45], v[44:45], v[72:73]
	v_pk_add_f32 v[46:47], v[46:47], v[74:75]
	v_pk_add_f32 v[28:29], v[28:29], v[72:73]
	v_pk_add_f32 v[30:31], v[30:31], v[74:75]
	v_pk_add_f32 v[12:13], v[12:13], v[72:73]
	v_pk_add_f32 v[14:15], v[14:15], v[74:75]
	v_pk_add_f32 v[140:141], v[140:141], v[80:81]
	v_pk_add_f32 v[142:143], v[142:143], v[82:83]
	v_pk_add_f32 v[120:121], v[120:121], v[80:81]
	v_pk_add_f32 v[122:123], v[122:123], v[82:83]
	v_pk_add_f32 v[104:105], v[104:105], v[80:81]
	v_pk_add_f32 v[106:107], v[106:107], v[82:83]
	v_pk_add_f32 v[76:77], v[76:77], v[80:81]
	v_pk_add_f32 v[78:79], v[78:79], v[82:83]
	v_pk_add_f32 v[56:57], v[56:57], v[80:81]
	v_pk_add_f32 v[58:59], v[58:59], v[82:83]
	v_pk_add_f32 v[40:41], v[40:41], v[80:81]
	v_pk_add_f32 v[42:43], v[42:43], v[82:83]
	v_pk_add_f32 v[24:25], v[24:25], v[80:81]
	v_pk_add_f32 v[26:27], v[26:27], v[82:83]
	v_pk_add_f32 v[8:9], v[8:9], v[80:81]
	v_pk_add_f32 v[10:11], v[10:11], v[82:83]
	v_pk_add_f32 v[132:133], v[132:133], v[88:89]
	v_pk_add_f32 v[134:135], v[134:135], v[90:91]
	v_pk_add_f32 v[116:117], v[116:117], v[88:89]
	v_pk_add_f32 v[118:119], v[118:119], v[90:91]
	v_pk_add_f32 v[100:101], v[100:101], v[88:89]
	v_pk_add_f32 v[102:103], v[102:103], v[90:91]
	v_pk_add_f32 v[68:69], v[68:69], v[88:89]
	v_pk_add_f32 v[70:71], v[70:71], v[90:91]
	v_pk_add_f32 v[52:53], v[52:53], v[88:89]
	v_pk_add_f32 v[54:55], v[54:55], v[90:91]
	v_pk_add_f32 v[36:37], v[36:37], v[88:89]
	v_pk_add_f32 v[38:39], v[38:39], v[90:91]
	v_pk_add_f32 v[20:21], v[20:21], v[88:89]
	v_pk_add_f32 v[22:23], v[22:23], v[90:91]
	v_pk_add_f32 v[4:5], v[4:5], v[88:89]
	v_pk_add_f32 v[6:7], v[6:7], v[90:91]
	v_pk_add_f32 v[128:129], v[128:129], v[92:93]
	v_pk_add_f32 v[130:131], v[130:131], v[94:95]
	v_pk_add_f32 v[112:113], v[112:113], v[92:93]
	v_pk_add_f32 v[114:115], v[114:115], v[94:95]
	v_pk_add_f32 v[96:97], v[96:97], v[92:93]
	v_pk_add_f32 v[98:99], v[98:99], v[94:95]
	v_pk_add_f32 v[64:65], v[64:65], v[92:93]
	v_pk_add_f32 v[66:67], v[66:67], v[94:95]
	v_pk_add_f32 v[48:49], v[48:49], v[92:93]
	v_pk_add_f32 v[50:51], v[50:51], v[94:95]
	v_pk_add_f32 v[32:33], v[32:33], v[92:93]
	v_pk_add_f32 v[34:35], v[34:35], v[94:95]
	v_pk_add_f32 v[16:17], v[16:17], v[92:93]
	v_pk_add_f32 v[18:19], v[18:19], v[94:95]
	v_pk_add_f32 v[0:1], v[0:1], v[92:93]
	v_pk_add_f32 v[2:3], v[2:3], v[94:95]
	s_add_u32 s94, s98, 0xc000
	s_addc_u32 s95, s99, 0
	global_load_dwordx4 v[240:243], v191, s[94:95] offset:0 nt
	global_load_dwordx4 v[244:247], v191, s[94:95] offset:64 nt
	s_add_u32 s94, s98, 0x12000
	s_addc_u32 s95, s99, 0
	global_load_dwordx4 v[248:251], v191, s[94:95] offset:0 nt
	global_load_dwordx4 v[252:255], v191, s[94:95] offset:64 nt
	s_add_u32 s94, s98, 0x30000
	s_addc_u32 s95, s99, 0
	global_load_dwordx4 v[136:139], v191, s[94:95] offset:0 nt
	global_load_dwordx4 v[148:151], v191, s[94:95] offset:64 nt
	s_add_u32 s94, s98, 0x36000
	s_addc_u32 s95, s99, 0
	global_load_dwordx4 v[152:155], v191, s[94:95] offset:0 nt
	global_load_dwordx4 v[156:159], v191, s[94:95] offset:64 nt
	s_waitcnt vmcnt(19)
	s_waitcnt vmcnt(11)
	v_cvt_f32_f16_e32 v72, v208
	v_cvt_f32_f16_sdwa v73, v208 dst_sel:DWORD dst_unused:UNUSED_PAD src0_sel:WORD_1
	v_cvt_f32_f16_e32 v74, v209
	v_cvt_f32_f16_sdwa v75, v209 dst_sel:DWORD dst_unused:UNUSED_PAD src0_sel:WORD_1
	v_cvt_f32_f16_e32 v80, v210
	v_cvt_f32_f16_sdwa v81, v210 dst_sel:DWORD dst_unused:UNUSED_PAD src0_sel:WORD_1
	v_cvt_f32_f16_e32 v82, v211
	v_cvt_f32_f16_sdwa v83, v211 dst_sel:DWORD dst_unused:UNUSED_PAD src0_sel:WORD_1
	v_sub_f32_e32 v72, v72, v238
	v_sub_f32_e32 v73, v73, v238
	v_sub_f32_e32 v74, v74, v238
	v_sub_f32_e32 v75, v75, v238
	v_sub_f32_e32 v80, v80, v238
	v_sub_f32_e32 v81, v81, v238
	v_sub_f32_e32 v82, v82, v238
	v_sub_f32_e32 v83, v83, v238
	v_pk_mul_f32 v[72:73], v[238:239], v[72:73] op_sel:[1,0]
	v_pk_mul_f32 v[74:75], v[238:239], v[74:75] op_sel:[1,0]
	v_pk_mul_f32 v[80:81], v[238:239], v[80:81] op_sel:[1,0]
	v_pk_mul_f32 v[82:83], v[238:239], v[82:83] op_sel:[1,0]
	v_pk_fma_f32 v[144:145], v[72:73], v[160:161], v[144:145]
	v_pk_fma_f32 v[146:147], v[74:75], v[162:163], v[146:147]
	v_pk_fma_f32 v[140:141], v[80:81], v[164:165], v[140:141]
	v_pk_fma_f32 v[142:143], v[82:83], v[166:167], v[142:143]
	v_cvt_pk_f16_f32 v144, v144, v145
	v_cvt_pk_f16_f32 v145, v146, v147
	v_cvt_pk_f16_f32 v146, v140, v141
	v_cvt_pk_f16_f32 v147, v142, v143
	ds_write_b128 v235, v[144:147]
	v_fma_mix_f32 v206, v144, 1.0, 0 op_sel_hi:[1,0,0]
	v_fma_mix_f32 v207, v144, v144, 0 op_sel_hi:[1,1,0]
	v_fma_mix_f32 v206, v144, 1.0, v206 op_sel:[1,0,0] op_sel_hi:[1,0,0]
	v_fma_mix_f32 v207, v144, v144, v207 op_sel:[1,1,0] op_sel_hi:[1,1,0]
	v_fma_mix_f32 v206, v145, 1.0, v206 op_sel_hi:[1,0,0]
	v_fma_mix_f32 v207, v145, v145, v207 op_sel_hi:[1,1,0]
	v_fma_mix_f32 v206, v145, 1.0, v206 op_sel:[1,0,0] op_sel_hi:[1,0,0]
	v_fma_mix_f32 v207, v145, v145, v207 op_sel:[1,1,0] op_sel_hi:[1,1,0]
	v_fma_mix_f32 v206, v146, 1.0, v206 op_sel_hi:[1,0,0]
	v_fma_mix_f32 v207, v146, v146, v207 op_sel_hi:[1,1,0]
	v_fma_mix_f32 v206, v146, 1.0, v206 op_sel:[1,0,0] op_sel_hi:[1,0,0]
	v_fma_mix_f32 v207, v146, v146, v207 op_sel:[1,1,0] op_sel_hi:[1,1,0]
	v_fma_mix_f32 v206, v147, 1.0, v206 op_sel_hi:[1,0,0]
	v_fma_mix_f32 v207, v147, v147, v207 op_sel_hi:[1,1,0]
	v_fma_mix_f32 v206, v147, 1.0, v206 op_sel:[1,0,0] op_sel_hi:[1,0,0]
	v_fma_mix_f32 v207, v147, v147, v207 op_sel:[1,1,0] op_sel_hi:[1,1,0]
	s_waitcnt vmcnt(10)
	v_cvt_f32_f16_e32 v72, v212
	v_cvt_f32_f16_sdwa v73, v212 dst_sel:DWORD dst_unused:UNUSED_PAD src0_sel:WORD_1
	v_cvt_f32_f16_e32 v74, v213
	v_cvt_f32_f16_sdwa v75, v213 dst_sel:DWORD dst_unused:UNUSED_PAD src0_sel:WORD_1
	v_cvt_f32_f16_e32 v80, v214
	v_cvt_f32_f16_sdwa v81, v214 dst_sel:DWORD dst_unused:UNUSED_PAD src0_sel:WORD_1
	v_cvt_f32_f16_e32 v82, v215
	v_cvt_f32_f16_sdwa v83, v215 dst_sel:DWORD dst_unused:UNUSED_PAD src0_sel:WORD_1
	v_sub_f32_e32 v72, v72, v238
	v_sub_f32_e32 v73, v73, v238
	v_sub_f32_e32 v74, v74, v238
	v_sub_f32_e32 v75, v75, v238
	v_sub_f32_e32 v80, v80, v238
	v_sub_f32_e32 v81, v81, v238
	v_sub_f32_e32 v82, v82, v238
	v_sub_f32_e32 v83, v83, v238
	v_pk_mul_f32 v[72:73], v[238:239], v[72:73] op_sel:[1,0]
	v_pk_mul_f32 v[74:75], v[238:239], v[74:75] op_sel:[1,0]
	v_pk_mul_f32 v[80:81], v[238:239], v[80:81] op_sel:[1,0]
	v_pk_mul_f32 v[82:83], v[238:239], v[82:83] op_sel:[1,0]
	v_pk_fma_f32 v[132:133], v[72:73], v[168:169], v[132:133]
	v_pk_fma_f32 v[134:135], v[74:75], v[170:171], v[134:135]
	v_pk_fma_f32 v[128:129], v[80:81], v[172:173], v[128:129]
	v_pk_fma_f32 v[130:131], v[82:83], v[174:175], v[130:131]
	v_cvt_pk_f16_f32 v132, v132, v133
	v_cvt_pk_f16_f32 v133, v134, v135
	v_cvt_pk_f16_f32 v134, v128, v129
	v_cvt_pk_f16_f32 v135, v130, v131
	ds_write_b128 v235, v[132:135] offset:64
	v_fma_mix_f32 v206, v132, 1.0, v206 op_sel_hi:[1,0,0]
	v_fma_mix_f32 v207, v132, v132, v207 op_sel_hi:[1,1,0]
	v_fma_mix_f32 v206, v132, 1.0, v206 op_sel:[1,0,0] op_sel_hi:[1,0,0]
	v_fma_mix_f32 v207, v132, v132, v207 op_sel:[1,1,0] op_sel_hi:[1,1,0]
	v_fma_mix_f32 v206, v133, 1.0, v206 op_sel_hi:[1,0,0]
	v_fma_mix_f32 v207, v133, v133, v207 op_sel_hi:[1,1,0]
	v_fma_mix_f32 v206, v133, 1.0, v206 op_sel:[1,0,0] op_sel_hi:[1,0,0]
	v_fma_mix_f32 v207, v133, v133, v207 op_sel:[1,1,0] op_sel_hi:[1,1,0]
	v_fma_mix_f32 v206, v134, 1.0, v206 op_sel_hi:[1,0,0]
	v_fma_mix_f32 v207, v134, v134, v207 op_sel_hi:[1,1,0]
	v_fma_mix_f32 v206, v134, 1.0, v206 op_sel:[1,0,0] op_sel_hi:[1,0,0]
	v_fma_mix_f32 v207, v134, v134, v207 op_sel:[1,1,0] op_sel_hi:[1,1,0]
	v_fma_mix_f32 v206, v135, 1.0, v206 op_sel_hi:[1,0,0]
	v_fma_mix_f32 v207, v135, v135, v207 op_sel_hi:[1,1,0]
	v_fma_mix_f32 v206, v135, 1.0, v206 op_sel:[1,0,0] op_sel_hi:[1,0,0]
	v_fma_mix_f32 v207, v135, v135, v207 op_sel:[1,1,0] op_sel_hi:[1,1,0]
	ds_read_b128 v[88:91], v236
	ds_read_b128 v[92:95], v236 offset:1152
	s_waitcnt vmcnt(9)
	v_cvt_f32_f16_e32 v72, v216
	v_cvt_f32_f16_sdwa v73, v216 dst_sel:DWORD dst_unused:UNUSED_PAD src0_sel:WORD_1
	v_cvt_f32_f16_e32 v74, v217
	v_cvt_f32_f16_sdwa v75, v217 dst_sel:DWORD dst_unused:UNUSED_PAD src0_sel:WORD_1
	v_cvt_f32_f16_e32 v80, v218
	v_cvt_f32_f16_sdwa v81, v218 dst_sel:DWORD dst_unused:UNUSED_PAD src0_sel:WORD_1
	v_cvt_f32_f16_e32 v82, v219
	v_cvt_f32_f16_sdwa v83, v219 dst_sel:DWORD dst_unused:UNUSED_PAD src0_sel:WORD_1
	v_sub_f32_e32 v72, v72, v192
	v_sub_f32_e32 v73, v73, v192
	v_sub_f32_e32 v74, v74, v192
	v_sub_f32_e32 v75, v75, v192
	v_sub_f32_e32 v80, v80, v192
	v_sub_f32_e32 v81, v81, v192
	v_sub_f32_e32 v82, v82, v192
	v_sub_f32_e32 v83, v83, v192
	v_pk_mul_f32 v[72:73], v[192:193], v[72:73] op_sel:[1,0]
	v_pk_mul_f32 v[74:75], v[192:193], v[74:75] op_sel:[1,0]
	v_pk_mul_f32 v[80:81], v[192:193], v[80:81] op_sel:[1,0]
	v_pk_mul_f32 v[82:83], v[192:193], v[82:83] op_sel:[1,0]
	v_pk_fma_f32 v[124:125], v[72:73], v[160:161], v[124:125]
	v_pk_fma_f32 v[126:127], v[74:75], v[162:163], v[126:127]
	v_pk_fma_f32 v[120:121], v[80:81], v[164:165], v[120:121]
	v_pk_fma_f32 v[122:123], v[82:83], v[166:167], v[122:123]
	v_cvt_pk_f16_f32 v124, v124, v125
	v_cvt_pk_f16_f32 v125, v126, v127
	v_cvt_pk_f16_f32 v126, v120, v121
	v_cvt_pk_f16_f32 v127, v122, v123
	s_waitcnt lgkmcnt(0)
	buffer_store_dwordx4 v[88:91], v225, s[24:27], 0 offen nt
	v_add_u32_e32 v82, 0x3000, v225
	buffer_store_dwordx4 v[92:95], v82, s[24:27], 0 offen nt
	ds_write_b128 v235, v[124:127]
	v_fma_mix_f32 v140, v124, 1.0, 0 op_sel_hi:[1,0,0]
	v_fma_mix_f32 v141, v124, v124, 0 op_sel_hi:[1,1,0]
	v_fma_mix_f32 v140, v124, 1.0, v140 op_sel:[1,0,0] op_sel_hi:[1,0,0]
	v_fma_mix_f32 v141, v124, v124, v141 op_sel:[1,1,0] op_sel_hi:[1,1,0]
	v_fma_mix_f32 v140, v125, 1.0, v140 op_sel_hi:[1,0,0]
	v_fma_mix_f32 v141, v125, v125, v141 op_sel_hi:[1,1,0]
	v_fma_mix_f32 v140, v125, 1.0, v140 op_sel:[1,0,0] op_sel_hi:[1,0,0]
	v_fma_mix_f32 v141, v125, v125, v141 op_sel:[1,1,0] op_sel_hi:[1,1,0]
	v_fma_mix_f32 v140, v126, 1.0, v140 op_sel_hi:[1,0,0]
	v_fma_mix_f32 v141, v126, v126, v141 op_sel_hi:[1,1,0]
	v_fma_mix_f32 v140, v126, 1.0, v140 op_sel:[1,0,0] op_sel_hi:[1,0,0]
	v_fma_mix_f32 v141, v126, v126, v141 op_sel:[1,1,0] op_sel_hi:[1,1,0]
	v_fma_mix_f32 v140, v127, 1.0, v140 op_sel_hi:[1,0,0]
	v_fma_mix_f32 v141, v127, v127, v141 op_sel_hi:[1,1,0]
	v_fma_mix_f32 v140, v127, 1.0, v140 op_sel:[1,0,0] op_sel_hi:[1,0,0]
	v_fma_mix_f32 v141, v127, v127, v141 op_sel:[1,1,0] op_sel_hi:[1,1,0]
	s_waitcnt vmcnt(10)
	v_cvt_f32_f16_e32 v72, v220
	v_cvt_f32_f16_sdwa v73, v220 dst_sel:DWORD dst_unused:UNUSED_PAD src0_sel:WORD_1
	v_cvt_f32_f16_e32 v74, v221
	v_cvt_f32_f16_sdwa v75, v221 dst_sel:DWORD dst_unused:UNUSED_PAD src0_sel:WORD_1
	v_cvt_f32_f16_e32 v80, v222
	v_cvt_f32_f16_sdwa v81, v222 dst_sel:DWORD dst_unused:UNUSED_PAD src0_sel:WORD_1
	v_cvt_f32_f16_e32 v82, v223
	v_cvt_f32_f16_sdwa v83, v223 dst_sel:DWORD dst_unused:UNUSED_PAD src0_sel:WORD_1
	v_sub_f32_e32 v72, v72, v192
	v_sub_f32_e32 v73, v73, v192
	v_sub_f32_e32 v74, v74, v192
	v_sub_f32_e32 v75, v75, v192
	v_sub_f32_e32 v80, v80, v192
	v_sub_f32_e32 v81, v81, v192
	v_sub_f32_e32 v82, v82, v192
	v_sub_f32_e32 v83, v83, v192
	v_pk_mul_f32 v[72:73], v[192:193], v[72:73] op_sel:[1,0]
	v_pk_mul_f32 v[74:75], v[192:193], v[74:75] op_sel:[1,0]
	v_pk_mul_f32 v[80:81], v[192:193], v[80:81] op_sel:[1,0]
	v_pk_mul_f32 v[82:83], v[192:193], v[82:83] op_sel:[1,0]
	v_pk_fma_f32 v[116:117], v[72:73], v[168:169], v[116:117]
	v_pk_fma_f32 v[118:119], v[74:75], v[170:171], v[118:119]
	v_pk_fma_f32 v[112:113], v[80:81], v[172:173], v[112:113]
	v_pk_fma_f32 v[114:115], v[82:83], v[174:175], v[114:115]
	v_cvt_pk_f16_f32 v116, v116, v117
	v_cvt_pk_f16_f32 v117, v118, v119
	v_cvt_pk_f16_f32 v118, v112, v113
	v_cvt_pk_f16_f32 v119, v114, v115
	ds_write_b128 v235, v[116:119] offset:64
	v_fma_mix_f32 v140, v116, 1.0, v140 op_sel_hi:[1,0,0]
	v_fma_mix_f32 v141, v116, v116, v141 op_sel_hi:[1,1,0]
	v_fma_mix_f32 v140, v116, 1.0, v140 op_sel:[1,0,0] op_sel_hi:[1,0,0]
	v_fma_mix_f32 v141, v116, v116, v141 op_sel:[1,1,0] op_sel_hi:[1,1,0]
	v_fma_mix_f32 v140, v117, 1.0, v140 op_sel_hi:[1,0,0]
	v_fma_mix_f32 v141, v117, v117, v141 op_sel_hi:[1,1,0]
	v_fma_mix_f32 v140, v117, 1.0, v140 op_sel:[1,0,0] op_sel_hi:[1,0,0]
	v_fma_mix_f32 v141, v117, v117, v141 op_sel:[1,1,0] op_sel_hi:[1,1,0]
	v_fma_mix_f32 v140, v118, 1.0, v140 op_sel_hi:[1,0,0]
	v_fma_mix_f32 v141, v118, v118, v141 op_sel_hi:[1,1,0]
	v_fma_mix_f32 v140, v118, 1.0, v140 op_sel:[1,0,0] op_sel_hi:[1,0,0]
	v_fma_mix_f32 v141, v118, v118, v141 op_sel:[1,1,0] op_sel_hi:[1,1,0]
	v_fma_mix_f32 v140, v119, 1.0, v140 op_sel_hi:[1,0,0]
	v_fma_mix_f32 v141, v119, v119, v141 op_sel_hi:[1,1,0]
	v_fma_mix_f32 v140, v119, 1.0, v140 op_sel:[1,0,0] op_sel_hi:[1,0,0]
	v_fma_mix_f32 v141, v119, v119, v141 op_sel:[1,1,0] op_sel_hi:[1,1,0]
	ds_read_b128 v[208:211], v236
	ds_read_b128 v[128:131], v236 offset:1152
	s_add_u32 s94, s98, 0x3c000
	s_addc_u32 s95, s99, 0
	global_load_dwordx4 v[212:215], v191, s[94:95] offset:0 nt
	global_load_dwordx4 v[144:147], v191, s[94:95] offset:64 nt
	s_add_u32 s94, s98, 0x42000
	s_addc_u32 s95, s99, 0
	global_load_dwordx4 v[132:135], v191, s[94:95] offset:0 nt
	global_load_dwordx4 v[88:91], v191, s[94:95] offset:64 nt
	s_waitcnt vmcnt(13)
	v_cvt_f32_f16_e32 v72, v240
	v_cvt_f32_f16_sdwa v73, v240 dst_sel:DWORD dst_unused:UNUSED_PAD src0_sel:WORD_1
	v_cvt_f32_f16_e32 v74, v241
	v_cvt_f32_f16_sdwa v75, v241 dst_sel:DWORD dst_unused:UNUSED_PAD src0_sel:WORD_1
	v_cvt_f32_f16_e32 v80, v242
	v_cvt_f32_f16_sdwa v81, v242 dst_sel:DWORD dst_unused:UNUSED_PAD src0_sel:WORD_1
	v_cvt_f32_f16_e32 v82, v243
	v_cvt_f32_f16_sdwa v83, v243 dst_sel:DWORD dst_unused:UNUSED_PAD src0_sel:WORD_1
	v_sub_f32_e32 v72, v72, v194
	v_sub_f32_e32 v73, v73, v194
	v_sub_f32_e32 v74, v74, v194
	v_sub_f32_e32 v75, v75, v194
	v_sub_f32_e32 v80, v80, v194
	v_sub_f32_e32 v81, v81, v194
	v_sub_f32_e32 v82, v82, v194
	v_sub_f32_e32 v83, v83, v194
	v_pk_mul_f32 v[72:73], v[194:195], v[72:73] op_sel:[1,0]
	v_pk_mul_f32 v[74:75], v[194:195], v[74:75] op_sel:[1,0]
	v_pk_mul_f32 v[80:81], v[194:195], v[80:81] op_sel:[1,0]
	v_pk_mul_f32 v[82:83], v[194:195], v[82:83] op_sel:[1,0]
	v_pk_fma_f32 v[108:109], v[72:73], v[160:161], v[108:109]
	v_pk_fma_f32 v[110:111], v[74:75], v[162:163], v[110:111]
	v_pk_fma_f32 v[104:105], v[80:81], v[164:165], v[104:105]
	v_pk_fma_f32 v[106:107], v[82:83], v[166:167], v[106:107]
	v_cvt_pk_f16_f32 v108, v108, v109
	v_cvt_pk_f16_f32 v109, v110, v111
	v_cvt_pk_f16_f32 v110, v104, v105
	v_cvt_pk_f16_f32 v111, v106, v107
	s_waitcnt lgkmcnt(0)
	v_add_u32_e32 v83, 0x6000, v225
	buffer_store_dwordx4 v[208:211], v83, s[24:27], 0 offen nt
	v_add_u32_e32 v82, 0x9000, v225
	buffer_store_dwordx4 v[128:131], v82, s[24:27], 0 offen nt
	ds_write_b128 v235, v[108:111]
	v_fma_mix_f32 v142, v108, 1.0, 0 op_sel_hi:[1,0,0]
	v_fma_mix_f32 v143, v108, v108, 0 op_sel_hi:[1,1,0]
	v_fma_mix_f32 v142, v108, 1.0, v142 op_sel:[1,0,0] op_sel_hi:[1,0,0]
	v_fma_mix_f32 v143, v108, v108, v143 op_sel:[1,1,0] op_sel_hi:[1,1,0]
	v_fma_mix_f32 v142, v109, 1.0, v142 op_sel_hi:[1,0,0]
	v_fma_mix_f32 v143, v109, v109, v143 op_sel_hi:[1,1,0]
	v_fma_mix_f32 v142, v109, 1.0, v142 op_sel:[1,0,0] op_sel_hi:[1,0,0]
	v_fma_mix_f32 v143, v109, v109, v143 op_sel:[1,1,0] op_sel_hi:[1,1,0]
	v_fma_mix_f32 v142, v110, 1.0, v142 op_sel_hi:[1,0,0]
	v_fma_mix_f32 v143, v110, v110, v143 op_sel_hi:[1,1,0]
	v_fma_mix_f32 v142, v110, 1.0, v142 op_sel:[1,0,0] op_sel_hi:[1,0,0]
	v_fma_mix_f32 v143, v110, v110, v143 op_sel:[1,1,0] op_sel_hi:[1,1,0]
	v_fma_mix_f32 v142, v111, 1.0, v142 op_sel_hi:[1,0,0]
	v_fma_mix_f32 v143, v111, v111, v143 op_sel_hi:[1,1,0]
	v_fma_mix_f32 v142, v111, 1.0, v142 op_sel:[1,0,0] op_sel_hi:[1,0,0]
	v_fma_mix_f32 v143, v111, v111, v143 op_sel:[1,1,0] op_sel_hi:[1,1,0]
	s_waitcnt vmcnt(14)
	v_cvt_f32_f16_e32 v72, v244
	v_cvt_f32_f16_sdwa v73, v244 dst_sel:DWORD dst_unused:UNUSED_PAD src0_sel:WORD_1
	v_cvt_f32_f16_e32 v74, v245
	v_cvt_f32_f16_sdwa v75, v245 dst_sel:DWORD dst_unused:UNUSED_PAD src0_sel:WORD_1
	v_cvt_f32_f16_e32 v80, v246
	v_cvt_f32_f16_sdwa v81, v246 dst_sel:DWORD dst_unused:UNUSED_PAD src0_sel:WORD_1
	v_cvt_f32_f16_e32 v82, v247
	v_cvt_f32_f16_sdwa v83, v247 dst_sel:DWORD dst_unused:UNUSED_PAD src0_sel:WORD_1
	v_sub_f32_e32 v72, v72, v194
	v_sub_f32_e32 v73, v73, v194
	v_sub_f32_e32 v74, v74, v194
	v_sub_f32_e32 v75, v75, v194
	v_sub_f32_e32 v80, v80, v194
	v_sub_f32_e32 v81, v81, v194
	v_sub_f32_e32 v82, v82, v194
	v_sub_f32_e32 v83, v83, v194
	v_pk_mul_f32 v[72:73], v[194:195], v[72:73] op_sel:[1,0]
	v_pk_mul_f32 v[74:75], v[194:195], v[74:75] op_sel:[1,0]
	v_pk_mul_f32 v[80:81], v[194:195], v[80:81] op_sel:[1,0]
	v_pk_mul_f32 v[82:83], v[194:195], v[82:83] op_sel:[1,0]
	v_pk_fma_f32 v[100:101], v[72:73], v[168:169], v[100:101]
	v_pk_fma_f32 v[102:103], v[74:75], v[170:171], v[102:103]
	v_pk_fma_f32 v[96:97], v[80:81], v[172:173], v[96:97]
	v_pk_fma_f32 v[98:99], v[82:83], v[174:175], v[98:99]
	v_cvt_pk_f16_f32 v100, v100, v101
	v_cvt_pk_f16_f32 v101, v102, v103
	v_cvt_pk_f16_f32 v102, v96, v97
	v_cvt_pk_f16_f32 v103, v98, v99
	ds_write_b128 v235, v[100:103] offset:64
	v_fma_mix_f32 v142, v100, 1.0, v142 op_sel_hi:[1,0,0]
	v_fma_mix_f32 v143, v100, v100, v143 op_sel_hi:[1,1,0]
	v_fma_mix_f32 v142, v100, 1.0, v142 op_sel:[1,0,0] op_sel_hi:[1,0,0]
	v_fma_mix_f32 v143, v100, v100, v143 op_sel:[1,1,0] op_sel_hi:[1,1,0]
	v_fma_mix_f32 v142, v101, 1.0, v142 op_sel_hi:[1,0,0]
	v_fma_mix_f32 v143, v101, v101, v143 op_sel_hi:[1,1,0]
	v_fma_mix_f32 v142, v101, 1.0, v142 op_sel:[1,0,0] op_sel_hi:[1,0,0]
	v_fma_mix_f32 v143, v101, v101, v143 op_sel:[1,1,0] op_sel_hi:[1,1,0]
	v_fma_mix_f32 v142, v102, 1.0, v142 op_sel_hi:[1,0,0]
	v_fma_mix_f32 v143, v102, v102, v143 op_sel_hi:[1,1,0]
	v_fma_mix_f32 v142, v102, 1.0, v142 op_sel:[1,0,0] op_sel_hi:[1,0,0]
	v_fma_mix_f32 v143, v102, v102, v143 op_sel:[1,1,0] op_sel_hi:[1,1,0]
	v_fma_mix_f32 v142, v103, 1.0, v142 op_sel_hi:[1,0,0]
	v_fma_mix_f32 v143, v103, v103, v143 op_sel_hi:[1,1,0]
	v_fma_mix_f32 v142, v103, 1.0, v142 op_sel:[1,0,0] op_sel_hi:[1,0,0]
	v_fma_mix_f32 v143, v103, v103, v143 op_sel:[1,1,0] op_sel_hi:[1,1,0]
	ds_read_b128 v[92:95], v236
	ds_read_b128 v[120:123], v236 offset:1152
	s_waitcnt vmcnt(13)
	v_cvt_f32_f16_e32 v72, v248
	v_cvt_f32_f16_sdwa v73, v248 dst_sel:DWORD dst_unused:UNUSED_PAD src0_sel:WORD_1
	v_cvt_f32_f16_e32 v74, v249
	v_cvt_f32_f16_sdwa v75, v249 dst_sel:DWORD dst_unused:UNUSED_PAD src0_sel:WORD_1
	v_cvt_f32_f16_e32 v80, v250
	v_cvt_f32_f16_sdwa v81, v250 dst_sel:DWORD dst_unused:UNUSED_PAD src0_sel:WORD_1
	v_cvt_f32_f16_e32 v82, v251
	v_cvt_f32_f16_sdwa v83, v251 dst_sel:DWORD dst_unused:UNUSED_PAD src0_sel:WORD_1
	v_sub_f32_e32 v72, v72, v196
	v_sub_f32_e32 v73, v73, v196
	v_sub_f32_e32 v74, v74, v196
	v_sub_f32_e32 v75, v75, v196
	v_sub_f32_e32 v80, v80, v196
	v_sub_f32_e32 v81, v81, v196
	v_sub_f32_e32 v82, v82, v196
	v_sub_f32_e32 v83, v83, v196
	v_pk_mul_f32 v[72:73], v[196:197], v[72:73] op_sel:[1,0]
	v_pk_mul_f32 v[74:75], v[196:197], v[74:75] op_sel:[1,0]
	v_pk_mul_f32 v[80:81], v[196:197], v[80:81] op_sel:[1,0]
	v_pk_mul_f32 v[82:83], v[196:197], v[82:83] op_sel:[1,0]
	v_pk_fma_f32 v[84:85], v[72:73], v[160:161], v[84:85]
	v_pk_fma_f32 v[86:87], v[74:75], v[162:163], v[86:87]
	v_pk_fma_f32 v[76:77], v[80:81], v[164:165], v[76:77]
	v_pk_fma_f32 v[78:79], v[82:83], v[166:167], v[78:79]
	v_cvt_pk_f16_f32 v84, v84, v85
	v_cvt_pk_f16_f32 v85, v86, v87
	v_cvt_pk_f16_f32 v86, v76, v77
	v_cvt_pk_f16_f32 v87, v78, v79
	s_waitcnt lgkmcnt(0)
	v_add_u32_e32 v83, 0xc000, v225
	buffer_store_dwordx4 v[92:95], v83, s[24:27], 0 offen nt
	v_add_u32_e32 v82, 0xf000, v225
	buffer_store_dwordx4 v[120:123], v82, s[24:27], 0 offen nt
	ds_write_b128 v235, v[84:87]
	v_fma_mix_f32 v216, v84, 1.0, 0 op_sel_hi:[1,0,0]
	v_fma_mix_f32 v217, v84, v84, 0 op_sel_hi:[1,1,0]
	v_fma_mix_f32 v216, v84, 1.0, v216 op_sel:[1,0,0] op_sel_hi:[1,0,0]
	v_fma_mix_f32 v217, v84, v84, v217 op_sel:[1,1,0] op_sel_hi:[1,1,0]
	v_fma_mix_f32 v216, v85, 1.0, v216 op_sel_hi:[1,0,0]
	v_fma_mix_f32 v217, v85, v85, v217 op_sel_hi:[1,1,0]
	v_fma_mix_f32 v216, v85, 1.0, v216 op_sel:[1,0,0] op_sel_hi:[1,0,0]
	v_fma_mix_f32 v217, v85, v85, v217 op_sel:[1,1,0] op_sel_hi:[1,1,0]
	v_fma_mix_f32 v216, v86, 1.0, v216 op_sel_hi:[1,0,0]
	v_fma_mix_f32 v217, v86, v86, v217 op_sel_hi:[1,1,0]
	v_fma_mix_f32 v216, v86, 1.0, v216 op_sel:[1,0,0] op_sel_hi:[1,0,0]
	v_fma_mix_f32 v217, v86, v86, v217 op_sel:[1,1,0] op_sel_hi:[1,1,0]
	v_fma_mix_f32 v216, v87, 1.0, v216 op_sel_hi:[1,0,0]
	v_fma_mix_f32 v217, v87, v87, v217 op_sel_hi:[1,1,0]
	v_fma_mix_f32 v216, v87, 1.0, v216 op_sel:[1,0,0] op_sel_hi:[1,0,0]
	v_fma_mix_f32 v217, v87, v87, v217 op_sel:[1,1,0] op_sel_hi:[1,1,0]
	s_waitcnt vmcnt(14)
	v_cvt_f32_f16_e32 v72, v252
	v_cvt_f32_f16_sdwa v73, v252 dst_sel:DWORD dst_unused:UNUSED_PAD src0_sel:WORD_1
	v_cvt_f32_f16_e32 v74, v253
	v_cvt_f32_f16_sdwa v75, v253 dst_sel:DWORD dst_unused:UNUSED_PAD src0_sel:WORD_1
	v_cvt_f32_f16_e32 v80, v254
	v_cvt_f32_f16_sdwa v81, v254 dst_sel:DWORD dst_unused:UNUSED_PAD src0_sel:WORD_1
	v_cvt_f32_f16_e32 v82, v255
	v_cvt_f32_f16_sdwa v83, v255 dst_sel:DWORD dst_unused:UNUSED_PAD src0_sel:WORD_1
	v_sub_f32_e32 v72, v72, v196
	v_sub_f32_e32 v73, v73, v196
	v_sub_f32_e32 v74, v74, v196
	v_sub_f32_e32 v75, v75, v196
	v_sub_f32_e32 v80, v80, v196
	v_sub_f32_e32 v81, v81, v196
	v_sub_f32_e32 v82, v82, v196
	v_sub_f32_e32 v83, v83, v196
	v_pk_mul_f32 v[72:73], v[196:197], v[72:73] op_sel:[1,0]
	v_pk_mul_f32 v[74:75], v[196:197], v[74:75] op_sel:[1,0]
	v_pk_mul_f32 v[80:81], v[196:197], v[80:81] op_sel:[1,0]
	v_pk_mul_f32 v[82:83], v[196:197], v[82:83] op_sel:[1,0]
	v_pk_fma_f32 v[68:69], v[72:73], v[168:169], v[68:69]
	v_pk_fma_f32 v[70:71], v[74:75], v[170:171], v[70:71]
	v_pk_fma_f32 v[64:65], v[80:81], v[172:173], v[64:65]
	v_pk_fma_f32 v[66:67], v[82:83], v[174:175], v[66:67]
	v_cvt_pk_f16_f32 v68, v68, v69
	v_cvt_pk_f16_f32 v69, v70, v71
	v_cvt_pk_f16_f32 v70, v64, v65
	v_cvt_pk_f16_f32 v71, v66, v67
	ds_write_b128 v235, v[68:71] offset:64
	v_fma_mix_f32 v216, v68, 1.0, v216 op_sel_hi:[1,0,0]
	v_fma_mix_f32 v217, v68, v68, v217 op_sel_hi:[1,1,0]
	v_fma_mix_f32 v216, v68, 1.0, v216 op_sel:[1,0,0] op_sel_hi:[1,0,0]
	v_fma_mix_f32 v217, v68, v68, v217 op_sel:[1,1,0] op_sel_hi:[1,1,0]
	v_fma_mix_f32 v216, v69, 1.0, v216 op_sel_hi:[1,0,0]
	v_fma_mix_f32 v217, v69, v69, v217 op_sel_hi:[1,1,0]
	v_fma_mix_f32 v216, v69, 1.0, v216 op_sel:[1,0,0] op_sel_hi:[1,0,0]
	v_fma_mix_f32 v217, v69, v69, v217 op_sel:[1,1,0] op_sel_hi:[1,1,0]
	v_fma_mix_f32 v216, v70, 1.0, v216 op_sel_hi:[1,0,0]
	v_fma_mix_f32 v217, v70, v70, v217 op_sel_hi:[1,1,0]
	v_fma_mix_f32 v216, v70, 1.0, v216 op_sel:[1,0,0] op_sel_hi:[1,0,0]
	v_fma_mix_f32 v217, v70, v70, v217 op_sel:[1,1,0] op_sel_hi:[1,1,0]
	v_fma_mix_f32 v216, v71, 1.0, v216 op_sel_hi:[1,0,0]
	v_fma_mix_f32 v217, v71, v71, v217 op_sel_hi:[1,1,0]
	v_fma_mix_f32 v216, v71, 1.0, v216 op_sel:[1,0,0] op_sel_hi:[1,0,0]
	v_fma_mix_f32 v217, v71, v71, v217 op_sel:[1,1,0] op_sel_hi:[1,1,0]
	ds_read_b128 v[112:115], v236
	ds_read_b128 v[220:223], v236 offset:1152
	s_waitcnt vmcnt(13)
	v_cvt_f32_f16_e32 v72, v136
	v_cvt_f32_f16_sdwa v73, v136 dst_sel:DWORD dst_unused:UNUSED_PAD src0_sel:WORD_1
	v_cvt_f32_f16_e32 v74, v137
	v_cvt_f32_f16_sdwa v75, v137 dst_sel:DWORD dst_unused:UNUSED_PAD src0_sel:WORD_1
	v_cvt_f32_f16_e32 v80, v138
	v_cvt_f32_f16_sdwa v81, v138 dst_sel:DWORD dst_unused:UNUSED_PAD src0_sel:WORD_1
	v_cvt_f32_f16_e32 v82, v139
	v_cvt_f32_f16_sdwa v83, v139 dst_sel:DWORD dst_unused:UNUSED_PAD src0_sel:WORD_1
	v_sub_f32_e32 v72, v72, v198
	v_sub_f32_e32 v73, v73, v198
	v_sub_f32_e32 v74, v74, v198
	v_sub_f32_e32 v75, v75, v198
	v_sub_f32_e32 v80, v80, v198
	v_sub_f32_e32 v81, v81, v198
	v_sub_f32_e32 v82, v82, v198
	v_sub_f32_e32 v83, v83, v198
	v_pk_mul_f32 v[72:73], v[198:199], v[72:73] op_sel:[1,0]
	v_pk_mul_f32 v[74:75], v[198:199], v[74:75] op_sel:[1,0]
	v_pk_mul_f32 v[80:81], v[198:199], v[80:81] op_sel:[1,0]
	v_pk_mul_f32 v[82:83], v[198:199], v[82:83] op_sel:[1,0]
	v_pk_fma_f32 v[60:61], v[72:73], v[160:161], v[60:61]
	v_pk_fma_f32 v[62:63], v[74:75], v[162:163], v[62:63]
	v_pk_fma_f32 v[56:57], v[80:81], v[164:165], v[56:57]
	v_pk_fma_f32 v[58:59], v[82:83], v[166:167], v[58:59]
	v_cvt_pk_f16_f32 v60, v60, v61
	v_cvt_pk_f16_f32 v61, v62, v63
	v_cvt_pk_f16_f32 v62, v56, v57
	v_cvt_pk_f16_f32 v63, v58, v59
	s_waitcnt lgkmcnt(0)
	v_add_u32_e32 v83, 0x12000, v225
	buffer_store_dwordx4 v[112:115], v83, s[24:27], 0 offen nt
	v_add_u32_e32 v82, 0x15000, v225
	buffer_store_dwordx4 v[220:223], v82, s[24:27], 0 offen nt
	ds_write_b128 v235, v[60:63]
	v_fma_mix_f32 v218, v60, 1.0, 0 op_sel_hi:[1,0,0]
	v_fma_mix_f32 v219, v60, v60, 0 op_sel_hi:[1,1,0]
	v_fma_mix_f32 v218, v60, 1.0, v218 op_sel:[1,0,0] op_sel_hi:[1,0,0]
	v_fma_mix_f32 v219, v60, v60, v219 op_sel:[1,1,0] op_sel_hi:[1,1,0]
	v_fma_mix_f32 v218, v61, 1.0, v218 op_sel_hi:[1,0,0]
	v_fma_mix_f32 v219, v61, v61, v219 op_sel_hi:[1,1,0]
	v_fma_mix_f32 v218, v61, 1.0, v218 op_sel:[1,0,0] op_sel_hi:[1,0,0]
	v_fma_mix_f32 v219, v61, v61, v219 op_sel:[1,1,0] op_sel_hi:[1,1,0]
	v_fma_mix_f32 v218, v62, 1.0, v218 op_sel_hi:[1,0,0]
	v_fma_mix_f32 v219, v62, v62, v219 op_sel_hi:[1,1,0]
	v_fma_mix_f32 v218, v62, 1.0, v218 op_sel:[1,0,0] op_sel_hi:[1,0,0]
	v_fma_mix_f32 v219, v62, v62, v219 op_sel:[1,1,0] op_sel_hi:[1,1,0]
	v_fma_mix_f32 v218, v63, 1.0, v218 op_sel_hi:[1,0,0]
	v_fma_mix_f32 v219, v63, v63, v219 op_sel_hi:[1,1,0]
	v_fma_mix_f32 v218, v63, 1.0, v218 op_sel:[1,0,0] op_sel_hi:[1,0,0]
	v_fma_mix_f32 v219, v63, v63, v219 op_sel:[1,1,0] op_sel_hi:[1,1,0]
	s_waitcnt vmcnt(14)
	v_cvt_f32_f16_e32 v72, v148
	v_cvt_f32_f16_sdwa v73, v148 dst_sel:DWORD dst_unused:UNUSED_PAD src0_sel:WORD_1
	v_cvt_f32_f16_e32 v74, v149
	v_cvt_f32_f16_sdwa v75, v149 dst_sel:DWORD dst_unused:UNUSED_PAD src0_sel:WORD_1
	v_cvt_f32_f16_e32 v80, v150
	v_cvt_f32_f16_sdwa v81, v150 dst_sel:DWORD dst_unused:UNUSED_PAD src0_sel:WORD_1
	v_cvt_f32_f16_e32 v82, v151
	v_cvt_f32_f16_sdwa v83, v151 dst_sel:DWORD dst_unused:UNUSED_PAD src0_sel:WORD_1
	v_sub_f32_e32 v72, v72, v198
	v_sub_f32_e32 v73, v73, v198
	v_sub_f32_e32 v74, v74, v198
	v_sub_f32_e32 v75, v75, v198
	v_sub_f32_e32 v80, v80, v198
	v_sub_f32_e32 v81, v81, v198
	v_sub_f32_e32 v82, v82, v198
	v_sub_f32_e32 v83, v83, v198
	v_pk_mul_f32 v[72:73], v[198:199], v[72:73] op_sel:[1,0]
	v_pk_mul_f32 v[74:75], v[198:199], v[74:75] op_sel:[1,0]
	v_pk_mul_f32 v[80:81], v[198:199], v[80:81] op_sel:[1,0]
	v_pk_mul_f32 v[82:83], v[198:199], v[82:83] op_sel:[1,0]
	v_pk_fma_f32 v[52:53], v[72:73], v[168:169], v[52:53]
	v_pk_fma_f32 v[54:55], v[74:75], v[170:171], v[54:55]
	v_pk_fma_f32 v[48:49], v[80:81], v[172:173], v[48:49]
	v_pk_fma_f32 v[50:51], v[82:83], v[174:175], v[50:51]
	v_cvt_pk_f16_f32 v52, v52, v53
	v_cvt_pk_f16_f32 v53, v54, v55
	v_cvt_pk_f16_f32 v54, v48, v49
	v_cvt_pk_f16_f32 v55, v50, v51
	ds_write_b128 v235, v[52:55] offset:64
	v_fma_mix_f32 v218, v52, 1.0, v218 op_sel_hi:[1,0,0]
	v_fma_mix_f32 v219, v52, v52, v219 op_sel_hi:[1,1,0]
	v_fma_mix_f32 v218, v52, 1.0, v218 op_sel:[1,0,0] op_sel_hi:[1,0,0]
	v_fma_mix_f32 v219, v52, v52, v219 op_sel:[1,1,0] op_sel_hi:[1,1,0]
	v_fma_mix_f32 v218, v53, 1.0, v218 op_sel_hi:[1,0,0]
	v_fma_mix_f32 v219, v53, v53, v219 op_sel_hi:[1,1,0]
	v_fma_mix_f32 v218, v53, 1.0, v218 op_sel:[1,0,0] op_sel_hi:[1,0,0]
	v_fma_mix_f32 v219, v53, v53, v219 op_sel:[1,1,0] op_sel_hi:[1,1,0]
	v_fma_mix_f32 v218, v54, 1.0, v218 op_sel_hi:[1,0,0]
	v_fma_mix_f32 v219, v54, v54, v219 op_sel_hi:[1,1,0]
	v_fma_mix_f32 v218, v54, 1.0, v218 op_sel:[1,0,0] op_sel_hi:[1,0,0]
	v_fma_mix_f32 v219, v54, v54, v219 op_sel:[1,1,0] op_sel_hi:[1,1,0]
	v_fma_mix_f32 v218, v55, 1.0, v218 op_sel_hi:[1,0,0]
	v_fma_mix_f32 v219, v55, v55, v219 op_sel_hi:[1,1,0]
	v_fma_mix_f32 v218, v55, 1.0, v218 op_sel:[1,0,0] op_sel_hi:[1,0,0]
	v_fma_mix_f32 v219, v55, v55, v219 op_sel:[1,1,0] op_sel_hi:[1,1,0]
	ds_read_b128 v[124:127], v236
	ds_read_b128 v[116:119], v236 offset:1152
	s_waitcnt vmcnt(13)
	v_cvt_f32_f16_e32 v72, v152
	v_cvt_f32_f16_sdwa v73, v152 dst_sel:DWORD dst_unused:UNUSED_PAD src0_sel:WORD_1
	v_cvt_f32_f16_e32 v74, v153
	v_cvt_f32_f16_sdwa v75, v153 dst_sel:DWORD dst_unused:UNUSED_PAD src0_sel:WORD_1
	v_cvt_f32_f16_e32 v80, v154
	v_cvt_f32_f16_sdwa v81, v154 dst_sel:DWORD dst_unused:UNUSED_PAD src0_sel:WORD_1
	v_cvt_f32_f16_e32 v82, v155
	v_cvt_f32_f16_sdwa v83, v155 dst_sel:DWORD dst_unused:UNUSED_PAD src0_sel:WORD_1
	v_sub_f32_e32 v72, v72, v200
	v_sub_f32_e32 v73, v73, v200
	v_sub_f32_e32 v74, v74, v200
	v_sub_f32_e32 v75, v75, v200
	v_sub_f32_e32 v80, v80, v200
	v_sub_f32_e32 v81, v81, v200
	v_sub_f32_e32 v82, v82, v200
	v_sub_f32_e32 v83, v83, v200
	v_pk_mul_f32 v[72:73], v[200:201], v[72:73] op_sel:[1,0]
	v_pk_mul_f32 v[74:75], v[200:201], v[74:75] op_sel:[1,0]
	v_pk_mul_f32 v[80:81], v[200:201], v[80:81] op_sel:[1,0]
	v_pk_mul_f32 v[82:83], v[200:201], v[82:83] op_sel:[1,0]
	v_pk_fma_f32 v[44:45], v[72:73], v[160:161], v[44:45]
	v_pk_fma_f32 v[46:47], v[74:75], v[162:163], v[46:47]
	v_pk_fma_f32 v[40:41], v[80:81], v[164:165], v[40:41]
	v_pk_fma_f32 v[42:43], v[82:83], v[166:167], v[42:43]
	v_cvt_pk_f16_f32 v44, v44, v45
	v_cvt_pk_f16_f32 v45, v46, v47
	v_cvt_pk_f16_f32 v46, v40, v41
	v_cvt_pk_f16_f32 v47, v42, v43
	s_waitcnt lgkmcnt(0)
	v_add_u32_e32 v83, 0x30000, v225
	buffer_store_dwordx4 v[124:127], v83, s[24:27], 0 offen nt
	v_add_u32_e32 v82, 0x33000, v225
	buffer_store_dwordx4 v[116:119], v82, s[24:27], 0 offen nt
	ds_write_b128 v235, v[44:47]
	v_fma_mix_f32 v208, v44, 1.0, 0 op_sel_hi:[1,0,0]
	v_fma_mix_f32 v209, v44, v44, 0 op_sel_hi:[1,1,0]
	v_fma_mix_f32 v208, v44, 1.0, v208 op_sel:[1,0,0] op_sel_hi:[1,0,0]
	v_fma_mix_f32 v209, v44, v44, v209 op_sel:[1,1,0] op_sel_hi:[1,1,0]
	v_fma_mix_f32 v208, v45, 1.0, v208 op_sel_hi:[1,0,0]
	v_fma_mix_f32 v209, v45, v45, v209 op_sel_hi:[1,1,0]
	v_fma_mix_f32 v208, v45, 1.0, v208 op_sel:[1,0,0] op_sel_hi:[1,0,0]
	v_fma_mix_f32 v209, v45, v45, v209 op_sel:[1,1,0] op_sel_hi:[1,1,0]
	v_fma_mix_f32 v208, v46, 1.0, v208 op_sel_hi:[1,0,0]
	v_fma_mix_f32 v209, v46, v46, v209 op_sel_hi:[1,1,0]
	v_fma_mix_f32 v208, v46, 1.0, v208 op_sel:[1,0,0] op_sel_hi:[1,0,0]
	v_fma_mix_f32 v209, v46, v46, v209 op_sel:[1,1,0] op_sel_hi:[1,1,0]
	v_fma_mix_f32 v208, v47, 1.0, v208 op_sel_hi:[1,0,0]
	v_fma_mix_f32 v209, v47, v47, v209 op_sel_hi:[1,1,0]
	v_fma_mix_f32 v208, v47, 1.0, v208 op_sel:[1,0,0] op_sel_hi:[1,0,0]
	v_fma_mix_f32 v209, v47, v47, v209 op_sel:[1,1,0] op_sel_hi:[1,1,0]
	s_waitcnt vmcnt(14)
	v_cvt_f32_f16_e32 v72, v156
	v_cvt_f32_f16_sdwa v73, v156 dst_sel:DWORD dst_unused:UNUSED_PAD src0_sel:WORD_1
	v_cvt_f32_f16_e32 v74, v157
	v_cvt_f32_f16_sdwa v75, v157 dst_sel:DWORD dst_unused:UNUSED_PAD src0_sel:WORD_1
	v_cvt_f32_f16_e32 v80, v158
	v_cvt_f32_f16_sdwa v81, v158 dst_sel:DWORD dst_unused:UNUSED_PAD src0_sel:WORD_1
	v_cvt_f32_f16_e32 v82, v159
	v_cvt_f32_f16_sdwa v83, v159 dst_sel:DWORD dst_unused:UNUSED_PAD src0_sel:WORD_1
	v_sub_f32_e32 v72, v72, v200
	v_sub_f32_e32 v73, v73, v200
	v_sub_f32_e32 v74, v74, v200
	v_sub_f32_e32 v75, v75, v200
	v_sub_f32_e32 v80, v80, v200
	v_sub_f32_e32 v81, v81, v200
	v_sub_f32_e32 v82, v82, v200
	v_sub_f32_e32 v83, v83, v200
	v_pk_mul_f32 v[72:73], v[200:201], v[72:73] op_sel:[1,0]
	v_pk_mul_f32 v[74:75], v[200:201], v[74:75] op_sel:[1,0]
	v_pk_mul_f32 v[80:81], v[200:201], v[80:81] op_sel:[1,0]
	v_pk_mul_f32 v[82:83], v[200:201], v[82:83] op_sel:[1,0]
	v_pk_fma_f32 v[36:37], v[72:73], v[168:169], v[36:37]
	v_pk_fma_f32 v[38:39], v[74:75], v[170:171], v[38:39]
	v_pk_fma_f32 v[32:33], v[80:81], v[172:173], v[32:33]
	v_pk_fma_f32 v[34:35], v[82:83], v[174:175], v[34:35]
	v_cvt_pk_f16_f32 v36, v36, v37
	v_cvt_pk_f16_f32 v37, v38, v39
	v_cvt_pk_f16_f32 v38, v32, v33
	v_cvt_pk_f16_f32 v39, v34, v35
	ds_write_b128 v235, v[36:39] offset:64
	v_fma_mix_f32 v208, v36, 1.0, v208 op_sel_hi:[1,0,0]
	v_fma_mix_f32 v209, v36, v36, v209 op_sel_hi:[1,1,0]
	v_fma_mix_f32 v208, v36, 1.0, v208 op_sel:[1,0,0] op_sel_hi:[1,0,0]
	v_fma_mix_f32 v209, v36, v36, v209 op_sel:[1,1,0] op_sel_hi:[1,1,0]
	v_fma_mix_f32 v208, v37, 1.0, v208 op_sel_hi:[1,0,0]
	v_fma_mix_f32 v209, v37, v37, v209 op_sel_hi:[1,1,0]
	v_fma_mix_f32 v208, v37, 1.0, v208 op_sel:[1,0,0] op_sel_hi:[1,0,0]
	v_fma_mix_f32 v209, v37, v37, v209 op_sel:[1,1,0] op_sel_hi:[1,1,0]
	v_fma_mix_f32 v208, v38, 1.0, v208 op_sel_hi:[1,0,0]
	v_fma_mix_f32 v209, v38, v38, v209 op_sel_hi:[1,1,0]
	v_fma_mix_f32 v208, v38, 1.0, v208 op_sel:[1,0,0] op_sel_hi:[1,0,0]
	v_fma_mix_f32 v209, v38, v38, v209 op_sel:[1,1,0] op_sel_hi:[1,1,0]
	v_fma_mix_f32 v208, v39, 1.0, v208 op_sel_hi:[1,0,0]
	v_fma_mix_f32 v209, v39, v39, v209 op_sel_hi:[1,1,0]
	v_fma_mix_f32 v208, v39, 1.0, v208 op_sel:[1,0,0] op_sel_hi:[1,0,0]
	v_fma_mix_f32 v209, v39, v39, v209 op_sel:[1,1,0] op_sel_hi:[1,1,0]
	ds_read_b128 v[128:131], v236
	ds_read_b128 v[104:107], v236 offset:1152
	s_waitcnt vmcnt(11)
	v_cvt_f32_f16_e32 v72, v212
	v_cvt_f32_f16_sdwa v73, v212 dst_sel:DWORD dst_unused:UNUSED_PAD src0_sel:WORD_1
	v_cvt_f32_f16_e32 v74, v213
	v_cvt_f32_f16_sdwa v75, v213 dst_sel:DWORD dst_unused:UNUSED_PAD src0_sel:WORD_1
	v_cvt_f32_f16_e32 v80, v214
	v_cvt_f32_f16_sdwa v81, v214 dst_sel:DWORD dst_unused:UNUSED_PAD src0_sel:WORD_1
	v_cvt_f32_f16_e32 v82, v215
	v_cvt_f32_f16_sdwa v83, v215 dst_sel:DWORD dst_unused:UNUSED_PAD src0_sel:WORD_1
	v_sub_f32_e32 v72, v72, v202
	v_sub_f32_e32 v73, v73, v202
	v_sub_f32_e32 v74, v74, v202
	v_sub_f32_e32 v75, v75, v202
	v_sub_f32_e32 v80, v80, v202
	v_sub_f32_e32 v81, v81, v202
	v_sub_f32_e32 v82, v82, v202
	v_sub_f32_e32 v83, v83, v202
	v_pk_mul_f32 v[72:73], v[202:203], v[72:73] op_sel:[1,0]
	v_pk_mul_f32 v[74:75], v[202:203], v[74:75] op_sel:[1,0]
	v_pk_mul_f32 v[80:81], v[202:203], v[80:81] op_sel:[1,0]
	v_pk_mul_f32 v[82:83], v[202:203], v[82:83] op_sel:[1,0]
	v_pk_fma_f32 v[28:29], v[72:73], v[160:161], v[28:29]
	v_pk_fma_f32 v[30:31], v[74:75], v[162:163], v[30:31]
	v_pk_fma_f32 v[24:25], v[80:81], v[164:165], v[24:25]
	v_pk_fma_f32 v[26:27], v[82:83], v[166:167], v[26:27]
	v_cvt_pk_f16_f32 v28, v28, v29
	v_cvt_pk_f16_f32 v29, v30, v31
	v_cvt_pk_f16_f32 v30, v24, v25
	v_cvt_pk_f16_f32 v31, v26, v27
	s_waitcnt lgkmcnt(0)
	v_add_u32_e32 v83, 0x36000, v225
	buffer_store_dwordx4 v[128:131], v83, s[24:27], 0 offen nt
	v_add_u32_e32 v82, 0x39000, v225
	buffer_store_dwordx4 v[104:107], v82, s[24:27], 0 offen nt
	ds_write_b128 v235, v[28:31]
	v_fma_mix_f32 v210, v28, 1.0, 0 op_sel_hi:[1,0,0]
	v_fma_mix_f32 v211, v28, v28, 0 op_sel_hi:[1,1,0]
	v_fma_mix_f32 v210, v28, 1.0, v210 op_sel:[1,0,0] op_sel_hi:[1,0,0]
	v_fma_mix_f32 v211, v28, v28, v211 op_sel:[1,1,0] op_sel_hi:[1,1,0]
	v_fma_mix_f32 v210, v29, 1.0, v210 op_sel_hi:[1,0,0]
	v_fma_mix_f32 v211, v29, v29, v211 op_sel_hi:[1,1,0]
	v_fma_mix_f32 v210, v29, 1.0, v210 op_sel:[1,0,0] op_sel_hi:[1,0,0]
	v_fma_mix_f32 v211, v29, v29, v211 op_sel:[1,1,0] op_sel_hi:[1,1,0]
	v_fma_mix_f32 v210, v30, 1.0, v210 op_sel_hi:[1,0,0]
	v_fma_mix_f32 v211, v30, v30, v211 op_sel_hi:[1,1,0]
	v_fma_mix_f32 v210, v30, 1.0, v210 op_sel:[1,0,0] op_sel_hi:[1,0,0]
	v_fma_mix_f32 v211, v30, v30, v211 op_sel:[1,1,0] op_sel_hi:[1,1,0]
	v_fma_mix_f32 v210, v31, 1.0, v210 op_sel_hi:[1,0,0]
	v_fma_mix_f32 v211, v31, v31, v211 op_sel_hi:[1,1,0]
	v_fma_mix_f32 v210, v31, 1.0, v210 op_sel:[1,0,0] op_sel_hi:[1,0,0]
	v_fma_mix_f32 v211, v31, v31, v211 op_sel:[1,1,0] op_sel_hi:[1,1,0]
	s_waitcnt vmcnt(12)
	v_cvt_f32_f16_e32 v72, v144
	v_cvt_f32_f16_sdwa v73, v144 dst_sel:DWORD dst_unused:UNUSED_PAD src0_sel:WORD_1
	v_cvt_f32_f16_e32 v74, v145
	v_cvt_f32_f16_sdwa v75, v145 dst_sel:DWORD dst_unused:UNUSED_PAD src0_sel:WORD_1
	v_cvt_f32_f16_e32 v80, v146
	v_cvt_f32_f16_sdwa v81, v146 dst_sel:DWORD dst_unused:UNUSED_PAD src0_sel:WORD_1
	v_cvt_f32_f16_e32 v82, v147
	v_cvt_f32_f16_sdwa v83, v147 dst_sel:DWORD dst_unused:UNUSED_PAD src0_sel:WORD_1
	v_sub_f32_e32 v72, v72, v202
	v_sub_f32_e32 v73, v73, v202
	v_sub_f32_e32 v74, v74, v202
	v_sub_f32_e32 v75, v75, v202
	v_sub_f32_e32 v80, v80, v202
	v_sub_f32_e32 v81, v81, v202
	v_sub_f32_e32 v82, v82, v202
	v_sub_f32_e32 v83, v83, v202
	v_pk_mul_f32 v[72:73], v[202:203], v[72:73] op_sel:[1,0]
	v_pk_mul_f32 v[74:75], v[202:203], v[74:75] op_sel:[1,0]
	v_pk_mul_f32 v[80:81], v[202:203], v[80:81] op_sel:[1,0]
	v_pk_mul_f32 v[82:83], v[202:203], v[82:83] op_sel:[1,0]
	v_pk_fma_f32 v[20:21], v[72:73], v[168:169], v[20:21]
	v_pk_fma_f32 v[22:23], v[74:75], v[170:171], v[22:23]
	v_pk_fma_f32 v[16:17], v[80:81], v[172:173], v[16:17]
	v_pk_fma_f32 v[18:19], v[82:83], v[174:175], v[18:19]
	v_cvt_pk_f16_f32 v20, v20, v21
	v_cvt_pk_f16_f32 v21, v22, v23
	v_cvt_pk_f16_f32 v22, v16, v17
	v_cvt_pk_f16_f32 v23, v18, v19
	ds_write_b128 v235, v[20:23] offset:64
	v_fma_mix_f32 v210, v20, 1.0, v210 op_sel_hi:[1,0,0]
	v_fma_mix_f32 v211, v20, v20, v211 op_sel_hi:[1,1,0]
	v_fma_mix_f32 v210, v20, 1.0, v210 op_sel:[1,0,0] op_sel_hi:[1,0,0]
	v_fma_mix_f32 v211, v20, v20, v211 op_sel:[1,1,0] op_sel_hi:[1,1,0]
	v_fma_mix_f32 v210, v21, 1.0, v210 op_sel_hi:[1,0,0]
	v_fma_mix_f32 v211, v21, v21, v211 op_sel_hi:[1,1,0]
	v_fma_mix_f32 v210, v21, 1.0, v210 op_sel:[1,0,0] op_sel_hi:[1,0,0]
	v_fma_mix_f32 v211, v21, v21, v211 op_sel:[1,1,0] op_sel_hi:[1,1,0]
	v_fma_mix_f32 v210, v22, 1.0, v210 op_sel_hi:[1,0,0]
	v_fma_mix_f32 v211, v22, v22, v211 op_sel_hi:[1,1,0]
	v_fma_mix_f32 v210, v22, 1.0, v210 op_sel:[1,0,0] op_sel_hi:[1,0,0]
	v_fma_mix_f32 v211, v22, v22, v211 op_sel:[1,1,0] op_sel_hi:[1,1,0]
	v_fma_mix_f32 v210, v23, 1.0, v210 op_sel_hi:[1,0,0]
	v_fma_mix_f32 v211, v23, v23, v211 op_sel_hi:[1,1,0]
	v_fma_mix_f32 v210, v23, 1.0, v210 op_sel:[1,0,0] op_sel_hi:[1,0,0]
	v_fma_mix_f32 v211, v23, v23, v211 op_sel:[1,1,0] op_sel_hi:[1,1,0]
	ds_read_b128 v[240:243], v236
	ds_read_b128 v[96:99], v236 offset:1152
	s_waitcnt vmcnt(11)
	v_cvt_f32_f16_e32 v72, v132
	v_cvt_f32_f16_sdwa v73, v132 dst_sel:DWORD dst_unused:UNUSED_PAD src0_sel:WORD_1
	v_cvt_f32_f16_e32 v74, v133
	v_cvt_f32_f16_sdwa v75, v133 dst_sel:DWORD dst_unused:UNUSED_PAD src0_sel:WORD_1
	v_cvt_f32_f16_e32 v80, v134
	v_cvt_f32_f16_sdwa v81, v134 dst_sel:DWORD dst_unused:UNUSED_PAD src0_sel:WORD_1
	v_cvt_f32_f16_e32 v82, v135
	v_cvt_f32_f16_sdwa v83, v135 dst_sel:DWORD dst_unused:UNUSED_PAD src0_sel:WORD_1
	v_sub_f32_e32 v72, v72, v204
	v_sub_f32_e32 v73, v73, v204
	v_sub_f32_e32 v74, v74, v204
	v_sub_f32_e32 v75, v75, v204
	v_sub_f32_e32 v80, v80, v204
	v_sub_f32_e32 v81, v81, v204
	v_sub_f32_e32 v82, v82, v204
	v_sub_f32_e32 v83, v83, v204
	v_pk_mul_f32 v[72:73], v[204:205], v[72:73] op_sel:[1,0]
	v_pk_mul_f32 v[74:75], v[204:205], v[74:75] op_sel:[1,0]
	v_pk_mul_f32 v[80:81], v[204:205], v[80:81] op_sel:[1,0]
	v_pk_mul_f32 v[82:83], v[204:205], v[82:83] op_sel:[1,0]
	v_pk_fma_f32 v[12:13], v[72:73], v[160:161], v[12:13]
	v_pk_fma_f32 v[14:15], v[74:75], v[162:163], v[14:15]
	v_pk_fma_f32 v[8:9], v[80:81], v[164:165], v[8:9]
	v_pk_fma_f32 v[10:11], v[82:83], v[166:167], v[10:11]
	v_cvt_pk_f16_f32 v12, v12, v13
	v_cvt_pk_f16_f32 v13, v14, v15
	v_cvt_pk_f16_f32 v14, v8, v9
	v_cvt_pk_f16_f32 v15, v10, v11
	s_waitcnt lgkmcnt(0)
	v_add_u32_e32 v83, 0x3c000, v225
	buffer_store_dwordx4 v[240:243], v83, s[24:27], 0 offen nt
	v_add_u32_e32 v82, 0x3f000, v225
	buffer_store_dwordx4 v[96:99], v82, s[24:27], 0 offen nt
	ds_write_b128 v235, v[12:15]
	v_fma_mix_f32 v244, v12, 1.0, 0 op_sel_hi:[1,0,0]
	v_fma_mix_f32 v245, v12, v12, 0 op_sel_hi:[1,1,0]
	v_fma_mix_f32 v244, v12, 1.0, v244 op_sel:[1,0,0] op_sel_hi:[1,0,0]
	v_fma_mix_f32 v245, v12, v12, v245 op_sel:[1,1,0] op_sel_hi:[1,1,0]
	v_fma_mix_f32 v244, v13, 1.0, v244 op_sel_hi:[1,0,0]
	v_fma_mix_f32 v245, v13, v13, v245 op_sel_hi:[1,1,0]
	v_fma_mix_f32 v244, v13, 1.0, v244 op_sel:[1,0,0] op_sel_hi:[1,0,0]
	v_fma_mix_f32 v245, v13, v13, v245 op_sel:[1,1,0] op_sel_hi:[1,1,0]
	v_fma_mix_f32 v244, v14, 1.0, v244 op_sel_hi:[1,0,0]
	v_fma_mix_f32 v245, v14, v14, v245 op_sel_hi:[1,1,0]
	v_fma_mix_f32 v244, v14, 1.0, v244 op_sel:[1,0,0] op_sel_hi:[1,0,0]
	v_fma_mix_f32 v245, v14, v14, v245 op_sel:[1,1,0] op_sel_hi:[1,1,0]
	v_fma_mix_f32 v244, v15, 1.0, v244 op_sel_hi:[1,0,0]
	v_fma_mix_f32 v245, v15, v15, v245 op_sel_hi:[1,1,0]
	v_fma_mix_f32 v244, v15, 1.0, v244 op_sel:[1,0,0] op_sel_hi:[1,0,0]
	v_fma_mix_f32 v245, v15, v15, v245 op_sel:[1,1,0] op_sel_hi:[1,1,0]
	s_waitcnt vmcnt(12)
	v_cvt_f32_f16_e32 v72, v88
	v_cvt_f32_f16_sdwa v73, v88 dst_sel:DWORD dst_unused:UNUSED_PAD src0_sel:WORD_1
	v_cvt_f32_f16_e32 v74, v89
	v_cvt_f32_f16_sdwa v75, v89 dst_sel:DWORD dst_unused:UNUSED_PAD src0_sel:WORD_1
	v_cvt_f32_f16_e32 v80, v90
	v_cvt_f32_f16_sdwa v81, v90 dst_sel:DWORD dst_unused:UNUSED_PAD src0_sel:WORD_1
	v_cvt_f32_f16_e32 v82, v91
	v_cvt_f32_f16_sdwa v83, v91 dst_sel:DWORD dst_unused:UNUSED_PAD src0_sel:WORD_1
	v_sub_f32_e32 v72, v72, v204
	v_sub_f32_e32 v73, v73, v204
	v_sub_f32_e32 v74, v74, v204
	v_sub_f32_e32 v75, v75, v204
	v_sub_f32_e32 v80, v80, v204
	v_sub_f32_e32 v81, v81, v204
	v_sub_f32_e32 v82, v82, v204
	v_sub_f32_e32 v83, v83, v204
	v_pk_mul_f32 v[72:73], v[204:205], v[72:73] op_sel:[1,0]
	v_pk_mul_f32 v[74:75], v[204:205], v[74:75] op_sel:[1,0]
	v_pk_mul_f32 v[80:81], v[204:205], v[80:81] op_sel:[1,0]
	v_pk_mul_f32 v[82:83], v[204:205], v[82:83] op_sel:[1,0]
	v_pk_fma_f32 v[4:5], v[72:73], v[168:169], v[4:5]
	v_pk_fma_f32 v[6:7], v[74:75], v[170:171], v[6:7]
	v_pk_fma_f32 v[0:1], v[80:81], v[172:173], v[0:1]
	v_pk_fma_f32 v[2:3], v[82:83], v[174:175], v[2:3]
	v_cvt_pk_f16_f32 v4, v4, v5
	v_cvt_pk_f16_f32 v5, v6, v7
	v_cvt_pk_f16_f32 v6, v0, v1
	v_cvt_pk_f16_f32 v7, v2, v3
	ds_write_b128 v235, v[4:7] offset:64
	v_fma_mix_f32 v244, v4, 1.0, v244 op_sel_hi:[1,0,0]
	v_fma_mix_f32 v245, v4, v4, v245 op_sel_hi:[1,1,0]
	v_fma_mix_f32 v244, v4, 1.0, v244 op_sel:[1,0,0] op_sel_hi:[1,0,0]
	v_fma_mix_f32 v245, v4, v4, v245 op_sel:[1,1,0] op_sel_hi:[1,1,0]
	v_fma_mix_f32 v244, v5, 1.0, v244 op_sel_hi:[1,0,0]
	v_fma_mix_f32 v245, v5, v5, v245 op_sel_hi:[1,1,0]
	v_fma_mix_f32 v244, v5, 1.0, v244 op_sel:[1,0,0] op_sel_hi:[1,0,0]
	v_fma_mix_f32 v245, v5, v5, v245 op_sel:[1,1,0] op_sel_hi:[1,1,0]
	v_fma_mix_f32 v244, v6, 1.0, v244 op_sel_hi:[1,0,0]
	v_fma_mix_f32 v245, v6, v6, v245 op_sel_hi:[1,1,0]
	v_fma_mix_f32 v244, v6, 1.0, v244 op_sel:[1,0,0] op_sel_hi:[1,0,0]
	v_fma_mix_f32 v245, v6, v6, v245 op_sel:[1,1,0] op_sel_hi:[1,1,0]
	v_fma_mix_f32 v244, v7, 1.0, v244 op_sel_hi:[1,0,0]
	v_fma_mix_f32 v245, v7, v7, v245 op_sel_hi:[1,1,0]
	v_fma_mix_f32 v244, v7, 1.0, v244 op_sel:[1,0,0] op_sel_hi:[1,0,0]
	v_fma_mix_f32 v245, v7, v7, v245 op_sel:[1,1,0] op_sel_hi:[1,1,0]
	ds_read_b128 v[108:111], v236
	ds_read_b128 v[100:103], v236 offset:1152
	s_waitcnt lgkmcnt(0)
	v_add_u32_e32 v83, 0x42000, v225
	buffer_store_dwordx4 v[108:111], v83, s[24:27], 0 offen nt
	v_add_u32_e32 v82, 0x45000, v225
	buffer_store_dwordx4 v[100:103], v82, s[24:27], 0 offen nt
	v_xor_b32_e32 v246, 16, v234
	v_lshlrev_b32_e32 v246, 2, v246
	v_xor_b32_e32 v247, 32, v234
	v_lshlrev_b32_e32 v247, 2, v247
	ds_bpermute_b32 v92, v246, v206
	ds_bpermute_b32 v93, v246, v207
	ds_bpermute_b32 v94, v246, v140
	ds_bpermute_b32 v95, v246, v141
	ds_bpermute_b32 v120, v246, v142
	ds_bpermute_b32 v121, v246, v143
	ds_bpermute_b32 v122, v246, v216
	ds_bpermute_b32 v123, v246, v217
	s_waitcnt lgkmcnt(0)
	v_pk_add_f32 v[206:207], v[206:207], v[92:93]
	v_pk_add_f32 v[140:141], v[140:141], v[94:95]
	v_pk_add_f32 v[142:143], v[142:143], v[120:121]
	v_pk_add_f32 v[216:217], v[216:217], v[122:123]
	ds_bpermute_b32 v92, v246, v218
	ds_bpermute_b32 v93, v246, v219
	ds_bpermute_b32 v94, v246, v208
	ds_bpermute_b32 v95, v246, v209
	ds_bpermute_b32 v120, v246, v210
	ds_bpermute_b32 v121, v246, v211
	ds_bpermute_b32 v122, v246, v244
	ds_bpermute_b32 v123, v246, v245
	s_waitcnt lgkmcnt(0)
	v_pk_add_f32 v[218:219], v[218:219], v[92:93]
	v_pk_add_f32 v[208:209], v[208:209], v[94:95]
	v_pk_add_f32 v[210:211], v[210:211], v[120:121]
	v_pk_add_f32 v[244:245], v[244:245], v[122:123]
	ds_bpermute_b32 v92, v247, v206
	ds_bpermute_b32 v93, v247, v207
	ds_bpermute_b32 v94, v247, v140
	ds_bpermute_b32 v95, v247, v141
	ds_bpermute_b32 v120, v247, v142
	ds_bpermute_b32 v121, v247, v143
	ds_bpermute_b32 v122, v247, v216
	ds_bpermute_b32 v123, v247, v217
	s_waitcnt lgkmcnt(0)
	v_pk_add_f32 v[206:207], v[206:207], v[92:93]
	v_pk_add_f32 v[140:141], v[140:141], v[94:95]
	v_pk_add_f32 v[142:143], v[142:143], v[120:121]
	v_pk_add_f32 v[216:217], v[216:217], v[122:123]
	ds_bpermute_b32 v92, v247, v218
	ds_bpermute_b32 v93, v247, v219
	ds_bpermute_b32 v94, v247, v208
	ds_bpermute_b32 v95, v247, v209
	ds_bpermute_b32 v120, v247, v210
	ds_bpermute_b32 v121, v247, v211
	ds_bpermute_b32 v122, v247, v244
	ds_bpermute_b32 v123, v247, v245
	s_waitcnt lgkmcnt(0)
	v_pk_add_f32 v[218:219], v[218:219], v[92:93]
	v_pk_add_f32 v[208:209], v[208:209], v[94:95]
	v_pk_add_f32 v[210:211], v[210:211], v[120:121]
	v_pk_add_f32 v[244:245], v[244:245], v[122:123]
	global_store_dwordx2 v224, v[206:207], s[100:101] offset:-2048
	global_store_dwordx2 v224, v[140:141], s[100:101] offset:-512
	global_store_dwordx2 v224, v[142:143], s[100:101] offset:1024
	global_store_dwordx2 v224, v[216:217], s[100:101] offset:2560
	s_add_u32 s100, s100, 0x3000
	s_addc_u32 s101, s101, 0
	global_store_dwordx2 v224, v[218:219], s[100:101] offset:-2048
	global_store_dwordx2 v224, v[208:209], s[100:101] offset:-512
	global_store_dwordx2 v224, v[210:211], s[100:101] offset:1024
	global_store_dwordx2 v224, v[244:245], s[100:101] offset:2560
	s_mov_b32 s83, s81
	s_mov_b32 s84, s82
	s_mov_b64 s[40:41], s[0:1]
	s_mov_b64 s[38:39], s[8:9]
	s_mov_b64 vcc, s[6:7]
	s_cbranch_vccz .LBB8_12
	s_waitcnt vmcnt(0)
	s_cmpk_gt_u32 s44, 0xff
	s_cbranch_scc1 .LBB8_31
	s_barrier

.LBB8_32:
	s_endpgm
	s_endpgm
	s_endpgm
	s_endpgm
	s_endpgm
	s_endpgm
	s_endpgm
	s_endpgm
	s_endpgm
	s_endpgm
	s_endpgm
	s_endpgm
	s_endpgm
	s_endpgm
	s_endpgm
	s_endpgm
	s_endpgm
	s_endpgm
	s_endpgm
	s_endpgm
	s_endpgm
	s_endpgm
	s_endpgm
	s_endpgm
	s_endpgm
	s_endpgm
	s_endpgm
	s_endpgm
	s_endpgm
	s_endpgm
	s_endpgm
	s_endpgm
	s_endpgm
	s_endpgm
	s_endpgm
	s_endpgm
	s_endpgm
	s_endpgm
	s_endpgm
	s_endpgm
	s_endpgm
	s_endpgm
	s_endpgm
	s_endpgm
	s_endpgm
	s_endpgm
	s_endpgm
	s_endpgm
	s_endpgm
	s_endpgm
	s_endpgm
	s_endpgm

.LBB9_27:
	ds_read_b128 v[128:131], v172
	ds_read_b128 v[132:135], v172 offset:1024
	ds_read_b128 v[136:139], v172 offset:2048
	ds_read_b128 v[140:143], v172 offset:3072
	s_add_u32 s30, s28, 0xfffd0080
	s_addc_u32 s31, s29, -1
	s_cmp_eq_u32 s73, 8
	s_cselect_b32 s35, s9, s31
	s_cselect_b32 s34, s8, s30
	s_cselect_b32 s31, s1, s72
	s_cselect_b32 s30, s0, s71
	v_lshl_add_u64 v[202:203], s[28:29], 0, v[152:153]
	s_add_i32 m0, s43, 0xc000
	ds_read_b128 v[158:161], v173
	ds_read_b128 v[162:165], v173 offset:1024
	ds_read_b128 v[178:181], v173 offset:2048
	ds_read_b128 v[182:185], v173 offset:3072
	ds_read_b128 v[186:189], v173 offset:4096
	ds_read_b128 v[190:193], v173 offset:5120
	ds_read_b128 v[194:197], v173 offset:6144
	ds_read_b128 v[198:201], v173 offset:7168
	global_load_lds_dwordx4 v[202:203], off
	v_lshl_add_u64 v[202:203], s[28:29], 0, v[154:155]
	s_add_i32 m0, s43, 0xe000
	s_nop 0
	global_load_lds_dwordx4 v[202:203], off
	s_waitcnt lgkmcnt(8)
	s_setprio 1
	s_barrier
	s_waitcnt lgkmcnt(0)
	v_mfma_f32_16x16x32_f16 v[124:127], v[128:131], v[158:161], v[124:127]
	v_mfma_f32_16x16x32_f16 v[120:123], v[136:139], v[158:161], v[120:123]
	v_mfma_f32_16x16x32_f16 v[108:111], v[128:131], v[178:181], v[108:111]
	v_mfma_f32_16x16x32_f16 v[104:107], v[136:139], v[178:181], v[104:107]
	v_mfma_f32_16x16x32_f16 v[96:99], v[128:131], v[186:189], v[96:99]
	v_mfma_f32_16x16x32_f16 v[88:91], v[136:139], v[186:189], v[88:91]
	v_mfma_f32_16x16x32_f16 v[80:83], v[128:131], v[194:197], v[80:83]
	v_mfma_f32_16x16x32_f16 v[72:75], v[136:139], v[194:197], v[72:75]
	v_mfma_f32_16x16x32_f16 v[124:127], v[132:135], v[162:165], v[124:127]
	v_mfma_f32_16x16x32_f16 v[120:123], v[140:143], v[162:165], v[120:123]
	v_mfma_f32_16x16x32_f16 v[108:111], v[132:135], v[182:185], v[108:111]
	v_mfma_f32_16x16x32_f16 v[104:107], v[140:143], v[182:185], v[104:107]
	v_mfma_f32_16x16x32_f16 v[96:99], v[132:135], v[190:193], v[96:99]
	v_mfma_f32_16x16x32_f16 v[88:91], v[140:143], v[190:193], v[88:91]
	v_mfma_f32_16x16x32_f16 v[80:83], v[132:135], v[198:201], v[80:83]
	v_mfma_f32_16x16x32_f16 v[72:75], v[140:143], v[198:201], v[72:75]
	s_barrier
	s_setprio 0
	s_add_i32 s74, s65, s42
	v_lshl_add_u64 v[218:219], s[30:31], 0, v[146:147]
	s_mov_b32 m0, s74
	ds_read_b128 v[202:205], v174
	ds_read_b128 v[206:209], v174 offset:1024
	ds_read_b128 v[210:213], v174 offset:2048
	ds_read_b128 v[214:217], v174 offset:3072
	global_load_lds_dwordx4 v[218:219], off
	v_lshl_add_u64 v[220:221], s[30:31], 0, v[150:151]
	s_add_i32 m0, s74, 0x2000
	s_nop 0
	global_load_lds_dwordx4 v[220:221], off
	s_setprio 1
	s_barrier
	s_waitcnt lgkmcnt(0)
	v_mfma_f32_16x16x32_f16 v[116:119], v[202:205], v[158:161], v[116:119]
	v_mfma_f32_16x16x32_f16 v[112:115], v[210:213], v[158:161], v[112:115]
	v_mfma_f32_16x16x32_f16 v[100:103], v[202:205], v[178:181], v[100:103]
	v_mfma_f32_16x16x32_f16 v[92:95], v[210:213], v[178:181], v[92:95]
	v_mfma_f32_16x16x32_f16 v[84:87], v[202:205], v[186:189], v[84:87]
	v_mfma_f32_16x16x32_f16 v[76:79], v[210:213], v[186:189], v[76:79]
	v_mfma_f32_16x16x32_f16 v[68:71], v[202:205], v[194:197], v[68:71]
	v_mfma_f32_16x16x32_f16 v[64:67], v[210:213], v[194:197], v[64:67]
	v_mfma_f32_16x16x32_f16 v[116:119], v[206:209], v[162:165], v[116:119]
	v_mfma_f32_16x16x32_f16 v[112:115], v[214:217], v[162:165], v[112:115]
	v_mfma_f32_16x16x32_f16 v[100:103], v[206:209], v[182:185], v[100:103]
	v_mfma_f32_16x16x32_f16 v[92:95], v[214:217], v[182:185], v[92:95]
	v_mfma_f32_16x16x32_f16 v[84:87], v[206:209], v[190:193], v[84:87]
	v_mfma_f32_16x16x32_f16 v[76:79], v[214:217], v[190:193], v[76:79]
	v_mfma_f32_16x16x32_f16 v[68:71], v[206:209], v[198:201], v[68:71]
	v_mfma_f32_16x16x32_f16 v[64:67], v[214:217], v[198:201], v[64:67]
	s_barrier
	s_setprio 0
	s_mov_b32 m0, s43
	v_lshl_add_u64 v[222:223], s[34:35], 0, v[144:145]
	ds_read_b128 v[158:161], v173 offset:16384
	ds_read_b128 v[162:165], v173 offset:17408
	ds_read_b128 v[178:181], v173 offset:18432
	ds_read_b128 v[182:185], v173 offset:19456
	ds_read_b128 v[186:189], v173 offset:20480
	ds_read_b128 v[190:193], v173 offset:21504
	ds_read_b128 v[194:197], v173 offset:22528
	ds_read_b128 v[198:201], v173 offset:23552
	global_load_lds_dwordx4 v[222:223], off
	v_lshl_add_u64 v[224:225], s[34:35], 0, v[148:149]
	s_mov_b32 m0, s44
	s_nop 0
	global_load_lds_dwordx4 v[224:225], off
	s_setprio 1
	s_barrier
	s_waitcnt lgkmcnt(0)
	v_mfma_f32_16x16x32_f16 v[60:63], v[128:131], v[158:161], v[60:63]
	v_mfma_f32_16x16x32_f16 v[56:59], v[136:139], v[158:161], v[56:59]
	v_mfma_f32_16x16x32_f16 v[48:51], v[128:131], v[178:181], v[48:51]
	v_mfma_f32_16x16x32_f16 v[40:43], v[136:139], v[178:181], v[40:43]
	v_mfma_f32_16x16x32_f16 v[32:35], v[128:131], v[186:189], v[32:35]
	v_mfma_f32_16x16x32_f16 v[24:27], v[136:139], v[186:189], v[24:27]
	v_mfma_f32_16x16x32_f16 v[16:19], v[128:131], v[194:197], v[16:19]
	v_mfma_f32_16x16x32_f16 v[8:11], v[136:139], v[194:197], v[8:11]
	v_mfma_f32_16x16x32_f16 v[60:63], v[132:135], v[162:165], v[60:63]
	v_mfma_f32_16x16x32_f16 v[56:59], v[140:143], v[162:165], v[56:59]
	v_mfma_f32_16x16x32_f16 v[48:51], v[132:135], v[182:185], v[48:51]
	v_mfma_f32_16x16x32_f16 v[40:43], v[140:143], v[182:185], v[40:43]
	v_mfma_f32_16x16x32_f16 v[32:35], v[132:135], v[190:193], v[32:35]
	v_mfma_f32_16x16x32_f16 v[24:27], v[140:143], v[190:193], v[24:27]
	v_mfma_f32_16x16x32_f16 v[16:19], v[132:135], v[198:201], v[16:19]
	v_mfma_f32_16x16x32_f16 v[8:11], v[140:143], v[198:201], v[8:11]
	s_barrier
	s_setprio 0
	s_add_u32 s74, s30, 0xc000
	s_addc_u32 s75, s31, 0
	s_add_i32 s76, s66, s42
	v_lshl_add_u64 v[128:129], s[74:75], 0, v[146:147]
	s_mov_b32 m0, s76
	s_nop 0
	global_load_lds_dwordx4 v[128:129], off
	v_lshl_add_u64 v[128:129], s[74:75], 0, v[150:151]
	s_add_i32 m0, s76, 0x2000
	s_nop 0
	global_load_lds_dwordx4 v[128:129], off
	s_waitcnt vmcnt(6)
	s_setprio 1
	s_barrier
	v_mfma_f32_16x16x32_f16 v[52:55], v[202:205], v[158:161], v[52:55]
	v_mfma_f32_16x16x32_f16 v[44:47], v[210:213], v[158:161], v[44:47]
	v_mfma_f32_16x16x32_f16 v[36:39], v[202:205], v[178:181], v[36:39]
	v_mfma_f32_16x16x32_f16 v[28:31], v[210:213], v[178:181], v[28:31]
	v_mfma_f32_16x16x32_f16 v[20:23], v[202:205], v[186:189], v[20:23]
	v_mfma_f32_16x16x32_f16 v[12:15], v[210:213], v[186:189], v[12:15]
	v_mfma_f32_16x16x32_f16 v[4:7], v[202:205], v[194:197], v[4:7]
	v_mfma_f32_16x16x32_f16 v[0:3], v[210:213], v[194:197], v[0:3]
	v_mfma_f32_16x16x32_f16 v[52:55], v[206:209], v[162:165], v[52:55]
	v_mfma_f32_16x16x32_f16 v[44:47], v[214:217], v[162:165], v[44:47]
	v_mfma_f32_16x16x32_f16 v[36:39], v[206:209], v[182:185], v[36:39]
	v_mfma_f32_16x16x32_f16 v[28:31], v[214:217], v[182:185], v[28:31]
	v_mfma_f32_16x16x32_f16 v[20:23], v[206:209], v[190:193], v[20:23]
	v_mfma_f32_16x16x32_f16 v[12:15], v[214:217], v[190:193], v[12:15]
	v_mfma_f32_16x16x32_f16 v[4:7], v[206:209], v[198:201], v[4:7]
	v_mfma_f32_16x16x32_f16 v[0:3], v[214:217], v[198:201], v[0:3]
	s_barrier
	s_setprio 0
	s_add_i32 s74, 0, 0x18000
	v_add_u32_e32 v140, s74, v168
	ds_read_b128 v[128:131], v140
	ds_read_b128 v[132:135], v140 offset:1024
	ds_read_b128 v[136:139], v140 offset:2048
	ds_read_b128 v[140:143], v140 offset:3072
	s_add_u32 s34, s34, 0x30000
	s_addc_u32 s35, s35, 0
	s_mov_b32 m0, s45
	v_lshl_add_u64 v[202:203], s[34:35], 0, v[144:145]
	ds_read_b128 v[158:161], v173 offset:32768
	ds_read_b128 v[162:165], v173 offset:33792
	ds_read_b128 v[178:181], v173 offset:34816
	ds_read_b128 v[182:185], v173 offset:35840
	ds_read_b128 v[186:189], v173 offset:36864
	ds_read_b128 v[190:193], v173 offset:37888
	ds_read_b128 v[194:197], v173 offset:38912
	ds_read_b128 v[198:201], v173 offset:39936
	global_load_lds_dwordx4 v[202:203], off
	v_lshl_add_u64 v[202:203], s[34:35], 0, v[148:149]
	s_mov_b32 m0, s46
	s_nop 0
	global_load_lds_dwordx4 v[202:203], off
	s_waitcnt lgkmcnt(8)
	s_setprio 1
	s_barrier
	s_waitcnt lgkmcnt(0)
	v_mfma_f32_16x16x32_f16 v[124:127], v[128:131], v[158:161], v[124:127]
	v_mfma_f32_16x16x32_f16 v[120:123], v[136:139], v[158:161], v[120:123]
	v_mfma_f32_16x16x32_f16 v[108:111], v[128:131], v[178:181], v[108:111]
	v_mfma_f32_16x16x32_f16 v[104:107], v[136:139], v[178:181], v[104:107]
	v_mfma_f32_16x16x32_f16 v[96:99], v[128:131], v[186:189], v[96:99]
	v_mfma_f32_16x16x32_f16 v[88:91], v[136:139], v[186:189], v[88:91]
	v_mfma_f32_16x16x32_f16 v[80:83], v[128:131], v[194:197], v[80:83]
	v_mfma_f32_16x16x32_f16 v[72:75], v[136:139], v[194:197], v[72:75]
	v_mfma_f32_16x16x32_f16 v[124:127], v[132:135], v[162:165], v[124:127]
	v_mfma_f32_16x16x32_f16 v[120:123], v[140:143], v[162:165], v[120:123]
	v_mfma_f32_16x16x32_f16 v[108:111], v[132:135], v[182:185], v[108:111]
	v_mfma_f32_16x16x32_f16 v[104:107], v[140:143], v[182:185], v[104:107]
	v_mfma_f32_16x16x32_f16 v[96:99], v[132:135], v[190:193], v[96:99]
	v_mfma_f32_16x16x32_f16 v[88:91], v[140:143], v[190:193], v[88:91]
	v_mfma_f32_16x16x32_f16 v[80:83], v[132:135], v[198:201], v[80:83]
	v_mfma_f32_16x16x32_f16 v[72:75], v[140:143], v[198:201], v[72:75]
	s_barrier
	s_setprio 0
	s_add_i32 s34, 0, 0x1c000
	s_add_i32 s35, s74, s42
	v_add_u32_e32 v177, s34, v168
	v_lshl_add_u64 v[218:219], v[218:219], 0, s[26:27]
	s_mov_b32 m0, s35
	ds_read_b128 v[202:205], v177
	ds_read_b128 v[206:209], v177 offset:1024
	ds_read_b128 v[210:213], v177 offset:2048
	ds_read_b128 v[214:217], v177 offset:3072
	global_load_lds_dwordx4 v[218:219], off
	v_lshl_add_u64 v[218:219], v[220:221], 0, s[26:27]
	s_add_i32 m0, s35, 0x2000
	s_nop 0
	global_load_lds_dwordx4 v[218:219], off
	s_setprio 1
	s_barrier
	s_waitcnt lgkmcnt(0)
	v_mfma_f32_16x16x32_f16 v[116:119], v[202:205], v[158:161], v[116:119]
	v_mfma_f32_16x16x32_f16 v[112:115], v[210:213], v[158:161], v[112:115]
	v_mfma_f32_16x16x32_f16 v[100:103], v[202:205], v[178:181], v[100:103]
	v_mfma_f32_16x16x32_f16 v[92:95], v[210:213], v[178:181], v[92:95]
	v_mfma_f32_16x16x32_f16 v[84:87], v[202:205], v[186:189], v[84:87]
	v_mfma_f32_16x16x32_f16 v[76:79], v[210:213], v[186:189], v[76:79]
	v_mfma_f32_16x16x32_f16 v[68:71], v[202:205], v[194:197], v[68:71]
	v_mfma_f32_16x16x32_f16 v[64:67], v[210:213], v[194:197], v[64:67]
	v_mfma_f32_16x16x32_f16 v[116:119], v[206:209], v[162:165], v[116:119]
	v_mfma_f32_16x16x32_f16 v[112:115], v[214:217], v[162:165], v[112:115]
	v_mfma_f32_16x16x32_f16 v[100:103], v[206:209], v[182:185], v[100:103]
	v_mfma_f32_16x16x32_f16 v[92:95], v[214:217], v[182:185], v[92:95]
	v_mfma_f32_16x16x32_f16 v[84:87], v[206:209], v[190:193], v[84:87]
	v_mfma_f32_16x16x32_f16 v[76:79], v[214:217], v[190:193], v[76:79]
	v_mfma_f32_16x16x32_f16 v[68:71], v[206:209], v[198:201], v[68:71]
	v_mfma_f32_16x16x32_f16 v[64:67], v[214:217], v[198:201], v[64:67]
	s_barrier
	s_setprio 0
	s_mov_b32 m0, s49
	v_lshl_add_u64 v[218:219], v[222:223], 0, s[26:27]
	ds_read_b128 v[158:161], v173 offset:49152
	ds_read_b128 v[162:165], v173 offset:50176
	ds_read_b128 v[178:181], v173 offset:51200
	ds_read_b128 v[182:185], v173 offset:52224
	ds_read_b128 v[186:189], v173 offset:53248
	ds_read_b128 v[190:193], v173 offset:54272
	ds_read_b128 v[194:197], v173 offset:55296
	ds_read_b128 v[198:201], v173 offset:56320
	global_load_lds_dwordx4 v[218:219], off
	v_lshl_add_u64 v[218:219], v[224:225], 0, s[26:27]
	s_mov_b32 m0, s50
	s_nop 0
	global_load_lds_dwordx4 v[218:219], off
	s_setprio 1
	s_barrier
	s_waitcnt lgkmcnt(0)
	v_mfma_f32_16x16x32_f16 v[60:63], v[128:131], v[158:161], v[60:63]
	v_mfma_f32_16x16x32_f16 v[56:59], v[136:139], v[158:161], v[56:59]
	v_mfma_f32_16x16x32_f16 v[48:51], v[128:131], v[178:181], v[48:51]
	v_mfma_f32_16x16x32_f16 v[40:43], v[136:139], v[178:181], v[40:43]
	v_mfma_f32_16x16x32_f16 v[32:35], v[128:131], v[186:189], v[32:35]
	v_mfma_f32_16x16x32_f16 v[24:27], v[136:139], v[186:189], v[24:27]
	v_mfma_f32_16x16x32_f16 v[16:19], v[128:131], v[194:197], v[16:19]
	v_mfma_f32_16x16x32_f16 v[8:11], v[136:139], v[194:197], v[8:11]
	v_mfma_f32_16x16x32_f16 v[60:63], v[132:135], v[162:165], v[60:63]
	v_mfma_f32_16x16x32_f16 v[56:59], v[140:143], v[162:165], v[56:59]
	v_mfma_f32_16x16x32_f16 v[48:51], v[132:135], v[182:185], v[48:51]
	v_mfma_f32_16x16x32_f16 v[40:43], v[140:143], v[182:185], v[40:43]
	v_mfma_f32_16x16x32_f16 v[32:35], v[132:135], v[190:193], v[32:35]
	v_mfma_f32_16x16x32_f16 v[24:27], v[140:143], v[190:193], v[24:27]
	v_mfma_f32_16x16x32_f16 v[16:19], v[132:135], v[198:201], v[16:19]
	v_mfma_f32_16x16x32_f16 v[8:11], v[140:143], v[198:201], v[8:11]
	s_barrier
	s_setprio 0
	s_add_u32 s30, s30, 0xc080
	s_addc_u32 s31, s31, 0
	s_add_i32 s34, s34, s42
	v_lshl_add_u64 v[128:129], s[30:31], 0, v[146:147]
	s_mov_b32 m0, s34
	s_nop 0
	global_load_lds_dwordx4 v[128:129], off
	v_lshl_add_u64 v[128:129], s[30:31], 0, v[150:151]
	s_add_i32 m0, s34, 0x2000
	s_nop 0
	global_load_lds_dwordx4 v[128:129], off
	s_waitcnt vmcnt(6)
	s_setprio 1
	s_barrier
	v_mfma_f32_16x16x32_f16 v[52:55], v[202:205], v[158:161], v[52:55]
	v_mfma_f32_16x16x32_f16 v[44:47], v[210:213], v[158:161], v[44:47]
	v_mfma_f32_16x16x32_f16 v[36:39], v[202:205], v[178:181], v[36:39]
	v_mfma_f32_16x16x32_f16 v[28:31], v[210:213], v[178:181], v[28:31]
	v_mfma_f32_16x16x32_f16 v[20:23], v[202:205], v[186:189], v[20:23]
	v_mfma_f32_16x16x32_f16 v[12:15], v[210:213], v[186:189], v[12:15]
	v_mfma_f32_16x16x32_f16 v[4:7], v[202:205], v[194:197], v[4:7]
	v_mfma_f32_16x16x32_f16 v[0:3], v[210:213], v[194:197], v[0:3]
	v_mfma_f32_16x16x32_f16 v[52:55], v[206:209], v[162:165], v[52:55]
	v_mfma_f32_16x16x32_f16 v[44:47], v[214:217], v[162:165], v[44:47]
	v_mfma_f32_16x16x32_f16 v[36:39], v[206:209], v[182:185], v[36:39]
	v_mfma_f32_16x16x32_f16 v[28:31], v[214:217], v[182:185], v[28:31]
	v_mfma_f32_16x16x32_f16 v[20:23], v[206:209], v[190:193], v[20:23]
	v_mfma_f32_16x16x32_f16 v[12:15], v[214:217], v[190:193], v[12:15]
	v_mfma_f32_16x16x32_f16 v[4:7], v[206:209], v[198:201], v[4:7]
	v_mfma_f32_16x16x32_f16 v[0:3], v[214:217], v[198:201], v[0:3]
	s_barrier
	s_setprio 0
	s_add_i32 s73, s73, 2
	s_add_u32 s28, s28, 0x100
	s_addc_u32 s29, s29, 0
	s_add_u32 s71, s71, 0x100
	s_addc_u32 s72, s72, 0
	s_cmp_gt_u32 s73, 9
	s_cbranch_scc0 .LBB9_27
	s_lshl_b32 s28, s70, 8
	s_add_i32 s28, s28, s48
	s_lshl_b32 s29, s68, 8
	s_or_b32 s29, s29, s51
	s_waitcnt vmcnt(6)
	v_pk_fma_f32 v[126:127], v[126:127], v[226:227], v[236:237] op_sel_hi:[1,0,1]
	v_pk_fma_f32 v[124:125], v[124:125], v[226:227], v[234:235] op_sel_hi:[1,0,1]
	v_pk_fma_f32 v[122:123], v[122:123], v[226:227], v[240:241] op_sel_hi:[1,0,1]
	v_pk_fma_f32 v[120:121], v[120:121], v[226:227], v[238:239] op_sel_hi:[1,0,1]
	v_cvt_pk_f16_f32 v124, v124, v125
	v_cvt_pk_f16_f32 v125, v126, v127
	v_cvt_pk_f16_f32 v126, v120, v121
	v_cvt_pk_f16_f32 v123, v122, v123
	v_pk_fma_f32 v[118:119], v[118:119], v[226:227], v[244:245] op_sel_hi:[1,0,1]
	v_pk_fma_f32 v[116:117], v[116:117], v[226:227], v[242:243] op_sel_hi:[1,0,1]
	v_pk_fma_f32 v[114:115], v[114:115], v[226:227], v[248:249] op_sel_hi:[1,0,1]
	v_pk_fma_f32 v[112:113], v[112:113], v[226:227], v[246:247] op_sel_hi:[1,0,1]
	v_pk_max_f16 v120, v124, 0
	v_pk_max_f16 v121, v125, 0
	v_pk_max_f16 v122, v126, 0
	v_pk_max_f16 v123, v123, 0
	v_cvt_pk_f16_f32 v116, v116, v117
	v_cvt_pk_f16_f32 v117, v118, v119
	v_cvt_pk_f16_f32 v118, v112, v113
	v_cvt_pk_f16_f32 v115, v114, v115
	v_pk_fma_f32 v[110:111], v[110:111], v[226:227], v[236:237] op_sel:[0,1,0]
	v_pk_fma_f32 v[108:109], v[108:109], v[226:227], v[234:235] op_sel:[0,1,0]
	v_pk_fma_f32 v[106:107], v[106:107], v[226:227], v[240:241] op_sel:[0,1,0]
	v_pk_fma_f32 v[104:105], v[104:105], v[226:227], v[238:239] op_sel:[0,1,0]
	v_pk_fma_f32 v[102:103], v[102:103], v[226:227], v[244:245] op_sel:[0,1,0]
	v_pk_fma_f32 v[100:101], v[100:101], v[226:227], v[242:243] op_sel:[0,1,0]
	v_pk_fma_f32 v[94:95], v[94:95], v[226:227], v[248:249] op_sel:[0,1,0]
	v_pk_fma_f32 v[92:93], v[92:93], v[226:227], v[246:247] op_sel:[0,1,0]
	ds_write_b128 v175, v[120:123]
	v_or_b32_e32 v120, s28, v169
	v_pk_max_f16 v112, v116, 0
	v_pk_max_f16 v113, v117, 0
	v_pk_max_f16 v114, v118, 0
	v_pk_max_f16 v115, v115, 0
	v_cvt_pk_f16_f32 v108, v108, v109
	v_cvt_pk_f16_f32 v109, v110, v111
	v_cvt_pk_f16_f32 v110, v104, v105
	v_cvt_pk_f16_f32 v107, v106, v107
	v_cvt_pk_f16_f32 v100, v100, v101
	v_cvt_pk_f16_f32 v101, v102, v103
	v_cvt_pk_f16_f32 v102, v92, v93
	v_cvt_pk_f16_f32 v95, v94, v95
	ds_write_b128 v175, v[112:115] offset:64
	v_mul_lo_u32 v116, v120, s10
	v_pk_max_f16 v104, v108, 0
	v_pk_max_f16 v105, v109, 0
	v_pk_max_f16 v106, v110, 0
	v_pk_max_f16 v107, v107, 0
	v_pk_max_f16 v92, v100, 0
	v_pk_max_f16 v93, v101, 0
	v_pk_max_f16 v94, v102, 0
	v_pk_max_f16 v95, v95, 0
	ds_read_b128 v[112:115], v176
	v_add_u32_e32 v120, s29, v116
	ds_read_b128 v[116:119], v176 offset:1152
	ds_write_b128 v175, v[104:107]
	ds_write_b128 v175, v[92:95] offset:64
	ds_read_b128 v[92:95], v176
	ds_read_b128 v[100:103], v176 offset:1152
	v_lshlrev_b32_e32 v121, 1, v120
	v_add_u32_e32 v122, v121, v170
	v_add_u32_e32 v104, s55, v121
	s_waitcnt lgkmcnt(0)
	buffer_store_dwordx4 v[112:115], v122, s[20:23], 0 offen nt
	v_add_u32_e32 v105, v104, v170
	v_pk_fma_f32 v[90:91], v[90:91], v[228:229], v[240:241] op_sel_hi:[1,0,1]
	v_add_u32_e32 v112, v121, v171
	buffer_store_dwordx4 v[116:119], v112, s[20:23], 0 offen nt
	buffer_store_dwordx4 v[92:95], v105, s[20:23], 0 offen nt
	v_pk_fma_f32 v[88:89], v[88:89], v[228:229], v[238:239] op_sel_hi:[1,0,1]
	v_pk_fma_f32 v[86:87], v[86:87], v[228:229], v[244:245] op_sel_hi:[1,0,1]
	v_pk_fma_f32 v[92:93], v[98:99], v[228:229], v[236:237] op_sel_hi:[1,0,1]
	v_pk_fma_f32 v[94:95], v[96:97], v[228:229], v[234:235] op_sel_hi:[1,0,1]
	v_pk_fma_f32 v[84:85], v[84:85], v[228:229], v[242:243] op_sel_hi:[1,0,1]
	v_pk_fma_f32 v[78:79], v[78:79], v[228:229], v[248:249] op_sel_hi:[1,0,1]
	v_pk_fma_f32 v[76:77], v[76:77], v[228:229], v[246:247] op_sel_hi:[1,0,1]
	v_cvt_pk_f16_f32 v94, v94, v95
	v_cvt_pk_f16_f32 v92, v92, v93
	v_cvt_pk_f16_f32 v93, v88, v89
	v_cvt_pk_f16_f32 v91, v90, v91
	v_cvt_pk_f16_f32 v84, v84, v85
	v_cvt_pk_f16_f32 v85, v86, v87
	v_cvt_pk_f16_f32 v86, v76, v77
	v_cvt_pk_f16_f32 v79, v78, v79
	v_pk_max_f16 v88, v94, 0
	v_pk_max_f16 v89, v92, 0
	v_pk_max_f16 v90, v93, 0
	v_pk_max_f16 v91, v91, 0
	v_pk_max_f16 v76, v84, 0
	v_pk_max_f16 v77, v85, 0
	v_pk_max_f16 v78, v86, 0
	v_pk_max_f16 v79, v79, 0
	ds_write_b128 v175, v[88:91]
	ds_write_b128 v175, v[76:79] offset:64
	ds_read_b128 v[76:79], v176
	ds_read_b128 v[84:87], v176 offset:1152
	v_add_u32_e32 v88, s55, v104
	v_add_u32_e32 v105, v104, v171
	v_add_u32_e32 v89, v88, v170
	buffer_store_dwordx4 v[100:103], v105, s[20:23], 0 offen nt
	s_waitcnt lgkmcnt(1)
	buffer_store_dwordx4 v[76:79], v89, s[20:23], 0 offen nt
	v_pk_fma_f32 v[74:75], v[74:75], v[228:229], v[240:241] op_sel:[0,1,0]
	v_pk_fma_f32 v[72:73], v[72:73], v[228:229], v[238:239] op_sel:[0,1,0]
	v_add_u32_e32 v76, v88, v171
	s_waitcnt lgkmcnt(0)
	buffer_store_dwordx4 v[84:87], v76, s[20:23], 0 offen nt
	v_pk_fma_f32 v[76:77], v[82:83], v[228:229], v[236:237] op_sel:[0,1,0]
	v_pk_fma_f32 v[78:79], v[80:81], v[228:229], v[234:235] op_sel:[0,1,0]
	v_pk_fma_f32 v[70:71], v[70:71], v[228:229], v[244:245] op_sel:[0,1,0]
	v_pk_fma_f32 v[68:69], v[68:69], v[228:229], v[242:243] op_sel:[0,1,0]
	v_pk_fma_f32 v[66:67], v[66:67], v[228:229], v[248:249] op_sel:[0,1,0]
	v_pk_fma_f32 v[64:65], v[64:65], v[228:229], v[246:247] op_sel:[0,1,0]
	v_cvt_pk_f16_f32 v78, v78, v79
	v_cvt_pk_f16_f32 v76, v76, v77
	v_cvt_pk_f16_f32 v77, v72, v73
	v_cvt_pk_f16_f32 v75, v74, v75
	v_cvt_pk_f16_f32 v68, v68, v69
	v_cvt_pk_f16_f32 v69, v70, v71
	v_cvt_pk_f16_f32 v70, v64, v65
	v_cvt_pk_f16_f32 v67, v66, v67
	v_pk_fma_f32 v[62:63], v[62:63], v[230:231], v[236:237] op_sel_hi:[1,0,1]
	v_pk_fma_f32 v[60:61], v[60:61], v[230:231], v[234:235] op_sel_hi:[1,0,1]
	v_pk_fma_f32 v[58:59], v[58:59], v[230:231], v[240:241] op_sel_hi:[1,0,1]
	v_pk_fma_f32 v[56:57], v[56:57], v[230:231], v[238:239] op_sel_hi:[1,0,1]
	v_pk_fma_f32 v[54:55], v[54:55], v[230:231], v[244:245] op_sel_hi:[1,0,1]
	v_pk_fma_f32 v[52:53], v[52:53], v[230:231], v[242:243] op_sel_hi:[1,0,1]
	v_pk_fma_f32 v[46:47], v[46:47], v[230:231], v[248:249] op_sel_hi:[1,0,1]
	v_pk_fma_f32 v[44:45], v[44:45], v[230:231], v[246:247] op_sel_hi:[1,0,1]
	v_pk_max_f16 v72, v78, 0
	v_pk_max_f16 v73, v76, 0
	v_pk_max_f16 v74, v77, 0
	v_pk_max_f16 v75, v75, 0
	v_pk_max_f16 v64, v68, 0
	v_pk_max_f16 v65, v69, 0
	v_pk_max_f16 v66, v70, 0
	v_pk_max_f16 v67, v67, 0
	v_cvt_pk_f16_f32 v60, v60, v61
	v_cvt_pk_f16_f32 v61, v62, v63
	v_cvt_pk_f16_f32 v62, v56, v57
	v_cvt_pk_f16_f32 v59, v58, v59
	v_cvt_pk_f16_f32 v52, v52, v53
	v_cvt_pk_f16_f32 v53, v54, v55
	v_cvt_pk_f16_f32 v54, v44, v45
	v_cvt_pk_f16_f32 v47, v46, v47
	ds_write_b128 v175, v[72:75]
	ds_write_b128 v175, v[64:67] offset:64
	v_pk_max_f16 v56, v60, 0
	v_pk_max_f16 v57, v61, 0
	v_pk_max_f16 v58, v62, 0
	v_pk_max_f16 v59, v59, 0
	v_pk_max_f16 v44, v52, 0
	v_pk_max_f16 v45, v53, 0
	v_pk_max_f16 v46, v54, 0
	v_pk_max_f16 v47, v47, 0
	ds_read_b128 v[64:67], v176
	ds_read_b128 v[68:71], v176 offset:1152
	ds_write_b128 v175, v[56:59]
	ds_write_b128 v175, v[44:47] offset:64
	ds_read_b128 v[44:47], v176
	ds_read_b128 v[52:55], v176 offset:1152
	v_add_u32_e32 v72, s56, v120
	v_lshlrev_b32_e32 v73, 1, v72
	v_add_u32_e32 v74, v73, v170
	v_add_u32_e32 v56, s62, v88
	s_waitcnt lgkmcnt(5)
	buffer_store_dwordx4 v[64:67], v74, s[20:23], 0 offen nt
	v_add_u32_e32 v57, v56, v170
	v_pk_fma_f32 v[42:43], v[42:43], v[230:231], v[240:241] op_sel:[0,1,0]
	v_add_u32_e32 v64, v73, v171
	s_waitcnt lgkmcnt(4)
	buffer_store_dwordx4 v[68:71], v64, s[20:23], 0 offen nt
	s_waitcnt lgkmcnt(1)
	buffer_store_dwordx4 v[44:47], v57, s[20:23], 0 offen nt
	v_pk_fma_f32 v[40:41], v[40:41], v[230:231], v[238:239] op_sel:[0,1,0]
	v_pk_fma_f32 v[38:39], v[38:39], v[230:231], v[244:245] op_sel:[0,1,0]
	v_add_u32_e32 v44, v56, v171
	s_waitcnt lgkmcnt(0)
	buffer_store_dwordx4 v[52:55], v44, s[20:23], 0 offen nt
	v_pk_fma_f32 v[44:45], v[50:51], v[230:231], v[236:237] op_sel:[0,1,0]
	v_pk_fma_f32 v[46:47], v[48:49], v[230:231], v[234:235] op_sel:[0,1,0]
	v_pk_fma_f32 v[36:37], v[36:37], v[230:231], v[242:243] op_sel:[0,1,0]
	v_pk_fma_f32 v[30:31], v[30:31], v[230:231], v[248:249] op_sel:[0,1,0]
	v_pk_fma_f32 v[28:29], v[28:29], v[230:231], v[246:247] op_sel:[0,1,0]
	v_cvt_pk_f16_f32 v46, v46, v47
	v_cvt_pk_f16_f32 v44, v44, v45
	v_cvt_pk_f16_f32 v45, v40, v41
	v_cvt_pk_f16_f32 v43, v42, v43
	v_cvt_pk_f16_f32 v36, v36, v37
	v_cvt_pk_f16_f32 v37, v38, v39
	v_cvt_pk_f16_f32 v38, v28, v29
	v_cvt_pk_f16_f32 v31, v30, v31
	v_pk_max_f16 v40, v46, 0
	v_pk_max_f16 v41, v44, 0
	v_pk_max_f16 v42, v45, 0
	v_pk_max_f16 v43, v43, 0
	v_pk_max_f16 v28, v36, 0
	v_pk_max_f16 v29, v37, 0
	v_pk_max_f16 v30, v38, 0
	v_pk_max_f16 v31, v31, 0
	ds_write_b128 v175, v[40:43]
	ds_write_b128 v175, v[28:31] offset:64
	ds_read_b128 v[28:31], v176
	ds_read_b128 v[36:39], v176 offset:1152
	v_add_u32_e32 v40, s63, v72
	v_lshlrev_b32_e32 v41, 1, v40
	v_add_u32_e32 v42, v41, v170
	s_waitcnt lgkmcnt(1)
	buffer_store_dwordx4 v[28:31], v42, s[20:23], 0 offen nt
	v_pk_fma_f32 v[26:27], v[26:27], v[232:233], v[240:241] op_sel_hi:[1,0,1]
	v_pk_fma_f32 v[24:25], v[24:25], v[232:233], v[238:239] op_sel_hi:[1,0,1]
	v_add_u32_e32 v28, v41, v171
	s_waitcnt lgkmcnt(0)
	buffer_store_dwordx4 v[36:39], v28, s[20:23], 0 offen nt
	v_pk_fma_f32 v[28:29], v[34:35], v[232:233], v[236:237] op_sel_hi:[1,0,1]
	v_pk_fma_f32 v[30:31], v[32:33], v[232:233], v[234:235] op_sel_hi:[1,0,1]
	v_pk_fma_f32 v[22:23], v[22:23], v[232:233], v[244:245] op_sel_hi:[1,0,1]
	v_pk_fma_f32 v[20:21], v[20:21], v[232:233], v[242:243] op_sel_hi:[1,0,1]
	v_pk_fma_f32 v[14:15], v[14:15], v[232:233], v[248:249] op_sel_hi:[1,0,1]
	v_pk_fma_f32 v[12:13], v[12:13], v[232:233], v[246:247] op_sel_hi:[1,0,1]
	v_cvt_pk_f16_f32 v30, v30, v31
	v_cvt_pk_f16_f32 v28, v28, v29
	v_cvt_pk_f16_f32 v29, v24, v25
	v_cvt_pk_f16_f32 v27, v26, v27
	v_cvt_pk_f16_f32 v20, v20, v21
	v_cvt_pk_f16_f32 v21, v22, v23
	v_cvt_pk_f16_f32 v22, v12, v13
	v_cvt_pk_f16_f32 v15, v14, v15
	v_pk_max_f16 v24, v30, 0
	v_pk_max_f16 v25, v28, 0
	v_pk_max_f16 v26, v29, 0
	v_pk_max_f16 v27, v27, 0
	v_pk_max_f16 v12, v20, 0
	v_pk_max_f16 v13, v21, 0
	v_pk_max_f16 v14, v22, 0
	v_pk_max_f16 v15, v15, 0
	ds_write_b128 v175, v[24:27]
	ds_write_b128 v175, v[12:15] offset:64
	ds_read_b128 v[12:15], v176
	ds_read_b128 v[20:23], v176 offset:1152
	v_add_u32_e32 v24, s64, v40
	v_lshlrev_b32_e32 v25, 1, v24
	v_add_u32_e32 v26, v25, v170
	s_waitcnt lgkmcnt(1)
	buffer_store_dwordx4 v[12:15], v26, s[20:23], 0 offen nt
	v_pk_fma_f32 v[10:11], v[10:11], v[232:233], v[240:241] op_sel:[0,1,0]
	v_pk_fma_f32 v[8:9], v[8:9], v[232:233], v[238:239] op_sel:[0,1,0]
	v_pk_fma_f32 v[12:13], v[18:19], v[232:233], v[236:237] op_sel:[0,1,0]
	v_pk_fma_f32 v[14:15], v[16:17], v[232:233], v[234:235] op_sel:[0,1,0]
	v_pk_fma_f32 v[6:7], v[6:7], v[232:233], v[244:245] op_sel:[0,1,0]
	v_pk_fma_f32 v[4:5], v[4:5], v[232:233], v[242:243] op_sel:[0,1,0]
	v_pk_fma_f32 v[2:3], v[2:3], v[232:233], v[248:249] op_sel:[0,1,0]
	v_pk_fma_f32 v[0:1], v[0:1], v[232:233], v[246:247] op_sel:[0,1,0]
	v_cvt_pk_f16_f32 v14, v14, v15
	v_cvt_pk_f16_f32 v12, v12, v13
	v_cvt_pk_f16_f32 v13, v8, v9
	v_cvt_pk_f16_f32 v11, v10, v11
	v_cvt_pk_f16_f32 v4, v4, v5
	v_cvt_pk_f16_f32 v5, v6, v7
	v_cvt_pk_f16_f32 v6, v0, v1
	v_cvt_pk_f16_f32 v3, v2, v3
	v_pk_max_f16 v8, v14, 0
	v_pk_max_f16 v9, v12, 0
	v_pk_max_f16 v10, v13, 0
	v_pk_max_f16 v11, v11, 0
	v_pk_max_f16 v0, v4, 0
	v_pk_max_f16 v1, v5, 0
	v_pk_max_f16 v2, v6, 0
	v_pk_max_f16 v3, v3, 0
	ds_write_b128 v175, v[8:11]
	ds_write_b128 v175, v[0:3] offset:64
	ds_read_b128 v[0:3], v176
	ds_read_b128 v[4:7], v176 offset:1152
	v_add_lshl_u32 v8, v24, s64, 1
	v_add_u32_e32 v25, v25, v171
	v_add_u32_e32 v9, v8, v170
	s_waitcnt lgkmcnt(4)
	buffer_store_dwordx4 v[20:23], v25, s[20:23], 0 offen nt
	s_waitcnt lgkmcnt(1)
	buffer_store_dwordx4 v[0:3], v9, s[20:23], 0 offen nt
	s_mov_b32 s68, s67
	s_mov_b32 s70, s69
	v_add_u32_e32 v0, v8, v171
	s_mov_b64 s[30:31], s[0:1]
	s_mov_b64 s[28:29], s[8:9]
	s_mov_b64 vcc, s[6:7]
	s_waitcnt lgkmcnt(0)
	buffer_store_dwordx4 v[4:7], v0, s[20:23], 0 offen nt
	s_cbranch_vccz .LBB9_12
	s_waitcnt vmcnt(0)
	s_cmpk_gt_u32 s36, 0xff
	s_cbranch_scc1 .LBB9_31
	s_barrier

.LBB9_32:
	s_endpgm
	s_endpgm
	s_endpgm
	s_endpgm
	s_endpgm
	s_endpgm
	s_endpgm
	s_endpgm
	s_endpgm
	s_endpgm
	s_endpgm
	s_endpgm
	s_endpgm
	s_endpgm
	s_endpgm
	s_endpgm
	s_endpgm
	s_endpgm
	s_endpgm
	s_endpgm
	s_endpgm
	s_endpgm
	s_endpgm
	s_endpgm
	s_endpgm
	s_endpgm
	s_endpgm
	s_endpgm
	s_endpgm
	s_endpgm
	s_endpgm
	s_endpgm
	s_endpgm
	s_endpgm
	s_endpgm
	s_endpgm
	s_endpgm
	s_endpgm
	s_endpgm
	s_endpgm
	s_endpgm
	s_endpgm
	s_endpgm
	s_endpgm
	s_endpgm
	s_endpgm
	s_endpgm
	s_endpgm
	s_endpgm
	s_endpgm
	s_endpgm
	s_endpgm
	s_endpgm
	s_endpgm
	s_endpgm
	s_endpgm
	s_endpgm
	s_endpgm
	s_endpgm
	s_endpgm
	s_endpgm
	s_endpgm
	s_endpgm

.LBB10_27:
	ds_read_b128 v[72:75], v231
	ds_read_b128 v[80:83], v231 offset:1024
	ds_read_b128 v[88:91], v231 offset:2048
	ds_read_b128 v[92:95], v231 offset:3072
	s_add_u32 s40, s38, 0xfff40080
	s_addc_u32 s41, s39, -1
	s_cmp_eq_u32 s87, 44
	s_cselect_b32 s43, s9, s41
	s_cselect_b32 s42, s8, s40
	s_cselect_b32 s41, s1, s86
	s_cselect_b32 s40, s0, s85
	v_lshl_add_u64 v[190:191], s[38:39], 0, v[184:185]
	s_add_i32 m0, s51, 0xc000
	ds_read_b128 v[136:139], v232
	ds_read_b128 v[148:151], v232 offset:1024
	ds_read_b128 v[152:155], v232 offset:2048
	ds_read_b128 v[156:159], v232 offset:3072
	ds_read_b128 v[160:163], v232 offset:4096
	ds_read_b128 v[164:167], v232 offset:5120
	ds_read_b128 v[168:171], v232 offset:6144
	ds_read_b128 v[172:175], v232 offset:7168
	global_load_lds_dwordx4 v[190:191], off
	v_lshl_add_u64 v[190:191], s[38:39], 0, v[186:187]
	s_add_i32 m0, s51, 0xe000
	s_nop 0
	global_load_lds_dwordx4 v[190:191], off
	s_waitcnt lgkmcnt(8)
	s_setprio 1
	s_barrier
	s_waitcnt lgkmcnt(0)
	v_mfma_f32_16x16x32_f16 v[144:147], v[72:75], v[136:139], v[144:147]
	v_mfma_f32_16x16x32_f16 v[140:143], v[88:91], v[136:139], v[140:143]
	v_mfma_f32_16x16x32_f16 v[124:127], v[72:75], v[152:155], v[124:127]
	v_mfma_f32_16x16x32_f16 v[120:123], v[88:91], v[152:155], v[120:123]
	v_mfma_f32_16x16x32_f16 v[108:111], v[72:75], v[160:163], v[108:111]
	v_mfma_f32_16x16x32_f16 v[104:107], v[88:91], v[160:163], v[104:107]
	v_mfma_f32_16x16x32_f16 v[84:87], v[72:75], v[168:171], v[84:87]
	v_mfma_f32_16x16x32_f16 v[76:79], v[88:91], v[168:171], v[76:79]
	v_mfma_f32_16x16x32_f16 v[144:147], v[80:83], v[148:151], v[144:147]
	v_mfma_f32_16x16x32_f16 v[140:143], v[92:95], v[148:151], v[140:143]
	v_mfma_f32_16x16x32_f16 v[124:127], v[80:83], v[156:159], v[124:127]
	v_mfma_f32_16x16x32_f16 v[120:123], v[92:95], v[156:159], v[120:123]
	v_mfma_f32_16x16x32_f16 v[108:111], v[80:83], v[164:167], v[108:111]
	v_mfma_f32_16x16x32_f16 v[104:107], v[92:95], v[164:167], v[104:107]
	v_mfma_f32_16x16x32_f16 v[84:87], v[80:83], v[172:175], v[84:87]
	v_mfma_f32_16x16x32_f16 v[76:79], v[92:95], v[172:175], v[76:79]
	s_barrier
	s_setprio 0
	s_add_i32 s88, s69, s50
	v_lshl_add_u64 v[206:207], s[40:41], 0, v[178:179]
	s_mov_b32 m0, s88
	ds_read_b128 v[190:193], v233
	ds_read_b128 v[194:197], v233 offset:1024
	ds_read_b128 v[198:201], v233 offset:2048
	ds_read_b128 v[202:205], v233 offset:3072
	global_load_lds_dwordx4 v[206:207], off
	v_lshl_add_u64 v[208:209], s[40:41], 0, v[182:183]
	s_add_i32 m0, s88, 0x2000
	s_nop 0
	global_load_lds_dwordx4 v[208:209], off
	s_setprio 1
	s_barrier
	s_waitcnt lgkmcnt(0)
	v_mfma_f32_16x16x32_f16 v[132:135], v[190:193], v[136:139], v[132:135]
	v_mfma_f32_16x16x32_f16 v[128:131], v[198:201], v[136:139], v[128:131]
	v_mfma_f32_16x16x32_f16 v[116:119], v[190:193], v[152:155], v[116:119]
	v_mfma_f32_16x16x32_f16 v[112:115], v[198:201], v[152:155], v[112:115]
	v_mfma_f32_16x16x32_f16 v[100:103], v[190:193], v[160:163], v[100:103]
	v_mfma_f32_16x16x32_f16 v[96:99], v[198:201], v[160:163], v[96:99]
	v_mfma_f32_16x16x32_f16 v[68:71], v[190:193], v[168:171], v[68:71]
	v_mfma_f32_16x16x32_f16 v[64:67], v[198:201], v[168:171], v[64:67]
	v_mfma_f32_16x16x32_f16 v[132:135], v[194:197], v[148:151], v[132:135]
	v_mfma_f32_16x16x32_f16 v[128:131], v[202:205], v[148:151], v[128:131]
	v_mfma_f32_16x16x32_f16 v[116:119], v[194:197], v[156:159], v[116:119]
	v_mfma_f32_16x16x32_f16 v[112:115], v[202:205], v[156:159], v[112:115]
	v_mfma_f32_16x16x32_f16 v[100:103], v[194:197], v[164:167], v[100:103]
	v_mfma_f32_16x16x32_f16 v[96:99], v[202:205], v[164:167], v[96:99]
	v_mfma_f32_16x16x32_f16 v[68:71], v[194:197], v[172:175], v[68:71]
	v_mfma_f32_16x16x32_f16 v[64:67], v[202:205], v[172:175], v[64:67]
	s_barrier
	s_setprio 0
	s_mov_b32 m0, s51
	v_lshl_add_u64 v[210:211], s[42:43], 0, v[176:177]
	ds_read_b128 v[136:139], v232 offset:16384
	ds_read_b128 v[148:151], v232 offset:17408
	ds_read_b128 v[152:155], v232 offset:18432
	ds_read_b128 v[156:159], v232 offset:19456
	ds_read_b128 v[160:163], v232 offset:20480
	ds_read_b128 v[164:167], v232 offset:21504
	ds_read_b128 v[168:171], v232 offset:22528
	ds_read_b128 v[172:175], v232 offset:23552
	global_load_lds_dwordx4 v[210:211], off
	v_lshl_add_u64 v[212:213], s[42:43], 0, v[180:181]
	s_mov_b32 m0, s52
	s_nop 0
	global_load_lds_dwordx4 v[212:213], off
	s_setprio 1
	s_barrier
	s_waitcnt lgkmcnt(0)
	v_mfma_f32_16x16x32_f16 v[60:63], v[72:75], v[136:139], v[60:63]
	v_mfma_f32_16x16x32_f16 v[56:59], v[88:91], v[136:139], v[56:59]
	v_mfma_f32_16x16x32_f16 v[44:47], v[72:75], v[152:155], v[44:47]
	v_mfma_f32_16x16x32_f16 v[40:43], v[88:91], v[152:155], v[40:43]
	v_mfma_f32_16x16x32_f16 v[28:31], v[72:75], v[160:163], v[28:31]
	v_mfma_f32_16x16x32_f16 v[24:27], v[88:91], v[160:163], v[24:27]
	v_mfma_f32_16x16x32_f16 v[12:15], v[72:75], v[168:171], v[12:15]
	v_mfma_f32_16x16x32_f16 v[8:11], v[88:91], v[168:171], v[8:11]
	v_mfma_f32_16x16x32_f16 v[60:63], v[80:83], v[148:151], v[60:63]
	v_mfma_f32_16x16x32_f16 v[56:59], v[92:95], v[148:151], v[56:59]
	v_mfma_f32_16x16x32_f16 v[44:47], v[80:83], v[156:159], v[44:47]
	v_mfma_f32_16x16x32_f16 v[40:43], v[92:95], v[156:159], v[40:43]
	v_mfma_f32_16x16x32_f16 v[28:31], v[80:83], v[164:167], v[28:31]
	v_mfma_f32_16x16x32_f16 v[24:27], v[92:95], v[164:167], v[24:27]
	v_mfma_f32_16x16x32_f16 v[12:15], v[80:83], v[172:175], v[12:15]
	v_mfma_f32_16x16x32_f16 v[8:11], v[92:95], v[172:175], v[8:11]
	s_barrier
	s_setprio 0
	s_add_u32 s88, s40, 0x30000
	s_addc_u32 s89, s41, 0
	s_add_i32 s90, s70, s50
	v_lshl_add_u64 v[72:73], s[88:89], 0, v[178:179]
	s_mov_b32 m0, s90
	s_nop 0
	global_load_lds_dwordx4 v[72:73], off
	v_lshl_add_u64 v[72:73], s[88:89], 0, v[182:183]
	s_add_i32 m0, s90, 0x2000
	s_nop 0
	global_load_lds_dwordx4 v[72:73], off
	s_waitcnt vmcnt(6)
	s_setprio 1
	s_barrier
	v_mfma_f32_16x16x32_f16 v[52:55], v[190:193], v[136:139], v[52:55]
	v_mfma_f32_16x16x32_f16 v[48:51], v[198:201], v[136:139], v[48:51]
	v_mfma_f32_16x16x32_f16 v[36:39], v[190:193], v[152:155], v[36:39]
	v_mfma_f32_16x16x32_f16 v[32:35], v[198:201], v[152:155], v[32:35]
	v_mfma_f32_16x16x32_f16 v[20:23], v[190:193], v[160:163], v[20:23]
	v_mfma_f32_16x16x32_f16 v[16:19], v[198:201], v[160:163], v[16:19]
	v_mfma_f32_16x16x32_f16 v[4:7], v[190:193], v[168:171], v[4:7]
	v_mfma_f32_16x16x32_f16 v[0:3], v[198:201], v[168:171], v[0:3]
	v_mfma_f32_16x16x32_f16 v[52:55], v[194:197], v[148:151], v[52:55]
	v_mfma_f32_16x16x32_f16 v[48:51], v[202:205], v[148:151], v[48:51]
	v_mfma_f32_16x16x32_f16 v[36:39], v[194:197], v[156:159], v[36:39]
	v_mfma_f32_16x16x32_f16 v[32:35], v[202:205], v[156:159], v[32:35]
	v_mfma_f32_16x16x32_f16 v[20:23], v[194:197], v[164:167], v[20:23]
	v_mfma_f32_16x16x32_f16 v[16:19], v[202:205], v[164:167], v[16:19]
	v_mfma_f32_16x16x32_f16 v[4:7], v[194:197], v[172:175], v[4:7]
	v_mfma_f32_16x16x32_f16 v[0:3], v[202:205], v[172:175], v[0:3]
	s_barrier
	s_setprio 0
	s_add_i32 s88, 0, 0x18000
	v_add_u32_e32 v92, s88, v228
	ds_read_b128 v[72:75], v92
	ds_read_b128 v[80:83], v92 offset:1024
	ds_read_b128 v[88:91], v92 offset:2048
	ds_read_b128 v[92:95], v92 offset:3072
	s_add_u32 s42, s42, 0xc0000
	s_addc_u32 s43, s43, 0
	s_mov_b32 m0, s53
	v_lshl_add_u64 v[190:191], s[42:43], 0, v[176:177]
	ds_read_b128 v[136:139], v232 offset:32768
	ds_read_b128 v[148:151], v232 offset:33792
	ds_read_b128 v[152:155], v232 offset:34816
	ds_read_b128 v[156:159], v232 offset:35840
	ds_read_b128 v[160:163], v232 offset:36864
	ds_read_b128 v[164:167], v232 offset:37888
	ds_read_b128 v[168:171], v232 offset:38912
	ds_read_b128 v[172:175], v232 offset:39936
	global_load_lds_dwordx4 v[190:191], off
	v_lshl_add_u64 v[190:191], s[42:43], 0, v[180:181]
	s_mov_b32 m0, s54
	s_nop 0
	global_load_lds_dwordx4 v[190:191], off
	s_waitcnt lgkmcnt(8)
	s_setprio 1
	s_barrier
	s_waitcnt lgkmcnt(0)
	v_mfma_f32_16x16x32_f16 v[144:147], v[72:75], v[136:139], v[144:147]
	v_mfma_f32_16x16x32_f16 v[140:143], v[88:91], v[136:139], v[140:143]
	v_mfma_f32_16x16x32_f16 v[124:127], v[72:75], v[152:155], v[124:127]
	v_mfma_f32_16x16x32_f16 v[120:123], v[88:91], v[152:155], v[120:123]
	v_mfma_f32_16x16x32_f16 v[108:111], v[72:75], v[160:163], v[108:111]
	v_mfma_f32_16x16x32_f16 v[104:107], v[88:91], v[160:163], v[104:107]
	v_mfma_f32_16x16x32_f16 v[84:87], v[72:75], v[168:171], v[84:87]
	v_mfma_f32_16x16x32_f16 v[76:79], v[88:91], v[168:171], v[76:79]
	v_mfma_f32_16x16x32_f16 v[144:147], v[80:83], v[148:151], v[144:147]
	v_mfma_f32_16x16x32_f16 v[140:143], v[92:95], v[148:151], v[140:143]
	v_mfma_f32_16x16x32_f16 v[124:127], v[80:83], v[156:159], v[124:127]
	v_mfma_f32_16x16x32_f16 v[120:123], v[92:95], v[156:159], v[120:123]
	v_mfma_f32_16x16x32_f16 v[108:111], v[80:83], v[164:167], v[108:111]
	v_mfma_f32_16x16x32_f16 v[104:107], v[92:95], v[164:167], v[104:107]
	v_mfma_f32_16x16x32_f16 v[84:87], v[80:83], v[172:175], v[84:87]
	v_mfma_f32_16x16x32_f16 v[76:79], v[92:95], v[172:175], v[76:79]
	s_barrier
	s_setprio 0
	s_add_i32 s42, 0, 0x1c000
	s_add_i32 s43, s88, s50
	v_add_u32_e32 v202, s42, v228
	v_lshl_add_u64 v[206:207], v[206:207], 0, s[36:37]
	s_mov_b32 m0, s43
	ds_read_b128 v[190:193], v202
	ds_read_b128 v[194:197], v202 offset:1024
	ds_read_b128 v[198:201], v202 offset:2048
	ds_read_b128 v[202:205], v202 offset:3072
	global_load_lds_dwordx4 v[206:207], off
	v_lshl_add_u64 v[206:207], v[208:209], 0, s[36:37]
	s_add_i32 m0, s43, 0x2000
	s_nop 0
	global_load_lds_dwordx4 v[206:207], off
	s_setprio 1
	s_barrier
	s_waitcnt lgkmcnt(0)
	v_mfma_f32_16x16x32_f16 v[132:135], v[190:193], v[136:139], v[132:135]
	v_mfma_f32_16x16x32_f16 v[128:131], v[198:201], v[136:139], v[128:131]
	v_mfma_f32_16x16x32_f16 v[116:119], v[190:193], v[152:155], v[116:119]
	v_mfma_f32_16x16x32_f16 v[112:115], v[198:201], v[152:155], v[112:115]
	v_mfma_f32_16x16x32_f16 v[100:103], v[190:193], v[160:163], v[100:103]
	v_mfma_f32_16x16x32_f16 v[96:99], v[198:201], v[160:163], v[96:99]
	v_mfma_f32_16x16x32_f16 v[68:71], v[190:193], v[168:171], v[68:71]
	v_mfma_f32_16x16x32_f16 v[64:67], v[198:201], v[168:171], v[64:67]
	v_mfma_f32_16x16x32_f16 v[132:135], v[194:197], v[148:151], v[132:135]
	v_mfma_f32_16x16x32_f16 v[128:131], v[202:205], v[148:151], v[128:131]
	v_mfma_f32_16x16x32_f16 v[116:119], v[194:197], v[156:159], v[116:119]
	v_mfma_f32_16x16x32_f16 v[112:115], v[202:205], v[156:159], v[112:115]
	v_mfma_f32_16x16x32_f16 v[100:103], v[194:197], v[164:167], v[100:103]
	v_mfma_f32_16x16x32_f16 v[96:99], v[202:205], v[164:167], v[96:99]
	v_mfma_f32_16x16x32_f16 v[68:71], v[194:197], v[172:175], v[68:71]
	v_mfma_f32_16x16x32_f16 v[64:67], v[202:205], v[172:175], v[64:67]
	s_barrier
	s_setprio 0
	s_mov_b32 m0, s58
	v_lshl_add_u64 v[206:207], v[210:211], 0, s[36:37]
	ds_read_b128 v[136:139], v232 offset:49152
	ds_read_b128 v[148:151], v232 offset:50176
	ds_read_b128 v[152:155], v232 offset:51200
	ds_read_b128 v[156:159], v232 offset:52224
	ds_read_b128 v[160:163], v232 offset:53248
	ds_read_b128 v[164:167], v232 offset:54272
	ds_read_b128 v[168:171], v232 offset:55296
	ds_read_b128 v[172:175], v232 offset:56320
	global_load_lds_dwordx4 v[206:207], off
	v_lshl_add_u64 v[206:207], v[212:213], 0, s[36:37]
	s_mov_b32 m0, s59
	s_nop 0
	global_load_lds_dwordx4 v[206:207], off
	s_setprio 1
	s_barrier
	s_waitcnt lgkmcnt(0)
	v_mfma_f32_16x16x32_f16 v[60:63], v[72:75], v[136:139], v[60:63]
	v_mfma_f32_16x16x32_f16 v[56:59], v[88:91], v[136:139], v[56:59]
	v_mfma_f32_16x16x32_f16 v[44:47], v[72:75], v[152:155], v[44:47]
	v_mfma_f32_16x16x32_f16 v[40:43], v[88:91], v[152:155], v[40:43]
	v_mfma_f32_16x16x32_f16 v[28:31], v[72:75], v[160:163], v[28:31]
	v_mfma_f32_16x16x32_f16 v[24:27], v[88:91], v[160:163], v[24:27]
	v_mfma_f32_16x16x32_f16 v[12:15], v[72:75], v[168:171], v[12:15]
	v_mfma_f32_16x16x32_f16 v[8:11], v[88:91], v[168:171], v[8:11]
	v_mfma_f32_16x16x32_f16 v[60:63], v[80:83], v[148:151], v[60:63]
	v_mfma_f32_16x16x32_f16 v[56:59], v[92:95], v[148:151], v[56:59]
	v_mfma_f32_16x16x32_f16 v[44:47], v[80:83], v[156:159], v[44:47]
	v_mfma_f32_16x16x32_f16 v[40:43], v[92:95], v[156:159], v[40:43]
	v_mfma_f32_16x16x32_f16 v[28:31], v[80:83], v[164:167], v[28:31]
	v_mfma_f32_16x16x32_f16 v[24:27], v[92:95], v[164:167], v[24:27]
	v_mfma_f32_16x16x32_f16 v[12:15], v[80:83], v[172:175], v[12:15]
	v_mfma_f32_16x16x32_f16 v[8:11], v[92:95], v[172:175], v[8:11]
	s_barrier
	s_setprio 0
	s_add_u32 s40, s40, 0x30080
	s_addc_u32 s41, s41, 0
	s_add_i32 s42, s42, s50
	v_lshl_add_u64 v[72:73], s[40:41], 0, v[178:179]
	s_mov_b32 m0, s42
	s_nop 0
	global_load_lds_dwordx4 v[72:73], off
	v_lshl_add_u64 v[72:73], s[40:41], 0, v[182:183]
	s_add_i32 m0, s42, 0x2000
	s_nop 0
	global_load_lds_dwordx4 v[72:73], off
	s_waitcnt vmcnt(6)
	s_setprio 1
	s_barrier
	v_mfma_f32_16x16x32_f16 v[52:55], v[190:193], v[136:139], v[52:55]
	v_mfma_f32_16x16x32_f16 v[48:51], v[198:201], v[136:139], v[48:51]
	v_mfma_f32_16x16x32_f16 v[36:39], v[190:193], v[152:155], v[36:39]
	v_mfma_f32_16x16x32_f16 v[32:35], v[198:201], v[152:155], v[32:35]
	v_mfma_f32_16x16x32_f16 v[20:23], v[190:193], v[160:163], v[20:23]
	v_mfma_f32_16x16x32_f16 v[16:19], v[198:201], v[160:163], v[16:19]
	v_mfma_f32_16x16x32_f16 v[4:7], v[190:193], v[168:171], v[4:7]
	v_mfma_f32_16x16x32_f16 v[0:3], v[198:201], v[168:171], v[0:3]
	v_mfma_f32_16x16x32_f16 v[52:55], v[194:197], v[148:151], v[52:55]
	v_mfma_f32_16x16x32_f16 v[48:51], v[202:205], v[148:151], v[48:51]
	v_mfma_f32_16x16x32_f16 v[36:39], v[194:197], v[156:159], v[36:39]
	v_mfma_f32_16x16x32_f16 v[32:35], v[202:205], v[156:159], v[32:35]
	v_mfma_f32_16x16x32_f16 v[20:23], v[194:197], v[164:167], v[20:23]
	v_mfma_f32_16x16x32_f16 v[16:19], v[202:205], v[164:167], v[16:19]
	v_mfma_f32_16x16x32_f16 v[4:7], v[194:197], v[172:175], v[4:7]
	v_mfma_f32_16x16x32_f16 v[0:3], v[202:205], v[172:175], v[0:3]
	s_barrier
	s_setprio 0
	s_add_i32 s87, s87, 2
	s_add_u32 s38, s38, 0x100
	s_addc_u32 s39, s39, 0
	s_add_u32 s85, s85, 0x100
	s_addc_u32 s86, s86, 0
	s_cmp_gt_u32 s87, 45
	s_cbranch_scc0 .LBB10_27
	s_lshl_b32 s92, s84, 8
	s_add_i32 s92, s92, s57
	s_lshl_b32 s93, s83, 8
	s_or_b32 s93, s93, s60
	v_lshlrev_b32_e32 v237, 2, v226
	s_lshl_b32 s96, s93, 2
	s_add_u32 s94, s16, s96
	s_addc_u32 s95, s17, 0
	global_load_dwordx4 v[72:75], v237, s[94:95] offset:0
	global_load_dwordx4 v[80:83], v237, s[94:95] offset:16
	global_load_dwordx4 v[88:91], v237, s[94:95] offset:128
	global_load_dwordx4 v[92:95], v237, s[94:95] offset:144
	s_add_u32 s94, s18, s96
	s_addc_u32 s95, s19, 0
	global_load_dwordx4 v[136:139], v237, s[94:95] offset:0
	global_load_dwordx4 v[148:151], v237, s[94:95] offset:16
	global_load_dwordx4 v[152:155], v237, s[94:95] offset:128
	global_load_dwordx4 v[156:159], v237, s[94:95] offset:144
	s_add_u32 s94, s14, s96
	s_addc_u32 s95, s15, 0
	global_load_dwordx4 v[160:163], v237, s[94:95] offset:0
	global_load_dwordx4 v[164:167], v237, s[94:95] offset:16
	global_load_dwordx4 v[168:171], v237, s[94:95] offset:128
	global_load_dwordx4 v[172:175], v237, s[94:95] offset:144
	v_lshlrev_b32_e32 v190, 3, v227
	s_lshl_b32 s96, s92, 3
	s_add_u32 s94, s12, s96
	s_addc_u32 s95, s13, 0
	global_load_dwordx2 v[238:239], v190, s[94:95] offset:0
	global_load_dwordx2 v[192:193], v190, s[94:95] offset:128
	global_load_dwordx2 v[194:195], v190, s[94:95] offset:256
	global_load_dwordx2 v[196:197], v190, s[94:95] offset:384
	global_load_dwordx2 v[198:199], v190, s[94:95] offset:1024
	global_load_dwordx2 v[200:201], v190, s[94:95] offset:1152
	global_load_dwordx2 v[202:203], v190, s[94:95] offset:1280
	global_load_dwordx2 v[204:205], v190, s[94:95] offset:1408
	v_mul_u32_u24_e32 v191, 0x600, v227
	v_lshl_add_u32 v191, v226, 1, v191
	s_mul_i32 s96, s92, 0x600
	s_lshl_b32 s97, s93, 1
	s_add_u32 s96, s96, s97
	s_add_u32 s98, s10, s96
	s_addc_u32 s99, s11, 0
	s_add_u32 s94, s98, 0x0
	s_addc_u32 s95, s99, 0
	global_load_dwordx4 v[208:211], v191, s[94:95] offset:0 nt
	global_load_dwordx4 v[212:215], v191, s[94:95] offset:64 nt
	s_add_u32 s94, s98, 0x6000
	s_addc_u32 s95, s99, 0
	global_load_dwordx4 v[216:219], v191, s[94:95] offset:0 nt
	global_load_dwordx4 v[220:223], v191, s[94:95] offset:64 nt
	v_add_u32_e32 v225, s92, v229
	v_mul_u32_u24_e32 v225, 0x600, v225
	s_lshl_b32 s97, s93, 1
	v_add3_u32 v225, v225, v230, s97
	v_mul_u32_u24_e32 v224, 0x60, v227
	s_mul_i32 s96, s92, 0x60
	s_lshl_b32 s97, s83, 5
	s_add_u32 s96, s96, s97
	s_lshr_b32 s97, s60, 3
	s_add_u32 s96, s96, s97
	s_add_u32 s96, s96, 0x800
	s_add_u32 s100, s28, s96
	s_addc_u32 s101, s29, 0
	s_waitcnt vmcnt(19)
	v_pk_add_f32 v[72:73], v[72:73], v[136:137]
	v_pk_add_f32 v[74:75], v[74:75], v[138:139]
	s_waitcnt vmcnt(18)
	v_pk_add_f32 v[80:81], v[80:81], v[148:149]
	v_pk_add_f32 v[82:83], v[82:83], v[150:151]
	s_waitcnt vmcnt(17)
	v_pk_add_f32 v[88:89], v[88:89], v[152:153]
	v_pk_add_f32 v[90:91], v[90:91], v[154:155]
	s_waitcnt vmcnt(16)
	v_pk_add_f32 v[92:93], v[92:93], v[156:157]
	v_pk_add_f32 v[94:95], v[94:95], v[158:159]
	v_pk_add_f32 v[144:145], v[144:145], v[72:73]
	v_pk_add_f32 v[146:147], v[146:147], v[74:75]
	v_pk_add_f32 v[124:125], v[124:125], v[72:73]
	v_pk_add_f32 v[126:127], v[126:127], v[74:75]
	v_pk_add_f32 v[108:109], v[108:109], v[72:73]
	v_pk_add_f32 v[110:111], v[110:111], v[74:75]
	v_pk_add_f32 v[84:85], v[84:85], v[72:73]
	v_pk_add_f32 v[86:87], v[86:87], v[74:75]
	v_pk_add_f32 v[60:61], v[60:61], v[72:73]
	v_pk_add_f32 v[62:63], v[62:63], v[74:75]
	v_pk_add_f32 v[44:45], v[44:45], v[72:73]
	v_pk_add_f32 v[46:47], v[46:47], v[74:75]
	v_pk_add_f32 v[28:29], v[28:29], v[72:73]
	v_pk_add_f32 v[30:31], v[30:31], v[74:75]
	v_pk_add_f32 v[12:13], v[12:13], v[72:73]
	v_pk_add_f32 v[14:15], v[14:15], v[74:75]
	v_pk_add_f32 v[140:141], v[140:141], v[80:81]
	v_pk_add_f32 v[142:143], v[142:143], v[82:83]
	v_pk_add_f32 v[120:121], v[120:121], v[80:81]
	v_pk_add_f32 v[122:123], v[122:123], v[82:83]
	v_pk_add_f32 v[104:105], v[104:105], v[80:81]
	v_pk_add_f32 v[106:107], v[106:107], v[82:83]
	v_pk_add_f32 v[76:77], v[76:77], v[80:81]
	v_pk_add_f32 v[78:79], v[78:79], v[82:83]
	v_pk_add_f32 v[56:57], v[56:57], v[80:81]
	v_pk_add_f32 v[58:59], v[58:59], v[82:83]
	v_pk_add_f32 v[40:41], v[40:41], v[80:81]
	v_pk_add_f32 v[42:43], v[42:43], v[82:83]
	v_pk_add_f32 v[24:25], v[24:25], v[80:81]
	v_pk_add_f32 v[26:27], v[26:27], v[82:83]
	v_pk_add_f32 v[8:9], v[8:9], v[80:81]
	v_pk_add_f32 v[10:11], v[10:11], v[82:83]
	v_pk_add_f32 v[132:133], v[132:133], v[88:89]
	v_pk_add_f32 v[134:135], v[134:135], v[90:91]
	v_pk_add_f32 v[116:117], v[116:117], v[88:89]
	v_pk_add_f32 v[118:119], v[118:119], v[90:91]
	v_pk_add_f32 v[100:101], v[100:101], v[88:89]
	v_pk_add_f32 v[102:103], v[102:103], v[90:91]
	v_pk_add_f32 v[68:69], v[68:69], v[88:89]
	v_pk_add_f32 v[70:71], v[70:71], v[90:91]
	v_pk_add_f32 v[52:53], v[52:53], v[88:89]
	v_pk_add_f32 v[54:55], v[54:55], v[90:91]
	v_pk_add_f32 v[36:37], v[36:37], v[88:89]
	v_pk_add_f32 v[38:39], v[38:39], v[90:91]
	v_pk_add_f32 v[20:21], v[20:21], v[88:89]
	v_pk_add_f32 v[22:23], v[22:23], v[90:91]
	v_pk_add_f32 v[4:5], v[4:5], v[88:89]
	v_pk_add_f32 v[6:7], v[6:7], v[90:91]
	v_pk_add_f32 v[128:129], v[128:129], v[92:93]
	v_pk_add_f32 v[130:131], v[130:131], v[94:95]
	v_pk_add_f32 v[112:113], v[112:113], v[92:93]
	v_pk_add_f32 v[114:115], v[114:115], v[94:95]
	v_pk_add_f32 v[96:97], v[96:97], v[92:93]
	v_pk_add_f32 v[98:99], v[98:99], v[94:95]
	v_pk_add_f32 v[64:65], v[64:65], v[92:93]
	v_pk_add_f32 v[66:67], v[66:67], v[94:95]
	v_pk_add_f32 v[48:49], v[48:49], v[92:93]
	v_pk_add_f32 v[50:51], v[50:51], v[94:95]
	v_pk_add_f32 v[32:33], v[32:33], v[92:93]
	v_pk_add_f32 v[34:35], v[34:35], v[94:95]
	v_pk_add_f32 v[16:17], v[16:17], v[92:93]
	v_pk_add_f32 v[18:19], v[18:19], v[94:95]
	v_pk_add_f32 v[0:1], v[0:1], v[92:93]
	v_pk_add_f32 v[2:3], v[2:3], v[94:95]
	s_add_u32 s94, s98, 0xc000
	s_addc_u32 s95, s99, 0
	global_load_dwordx4 v[240:243], v191, s[94:95] offset:0 nt
	global_load_dwordx4 v[244:247], v191, s[94:95] offset:64 nt
	s_add_u32 s94, s98, 0x12000
	s_addc_u32 s95, s99, 0
	global_load_dwordx4 v[248:251], v191, s[94:95] offset:0 nt
	global_load_dwordx4 v[252:255], v191, s[94:95] offset:64 nt
	s_add_u32 s94, s98, 0x30000
	s_addc_u32 s95, s99, 0
	global_load_dwordx4 v[136:139], v191, s[94:95] offset:0 nt
	global_load_dwordx4 v[148:151], v191, s[94:95] offset:64 nt
	s_add_u32 s94, s98, 0x36000
	s_addc_u32 s95, s99, 0
	global_load_dwordx4 v[152:155], v191, s[94:95] offset:0 nt
	global_load_dwordx4 v[156:159], v191, s[94:95] offset:64 nt
	s_waitcnt vmcnt(19)
	s_waitcnt vmcnt(11)
	v_cvt_f32_f16_e32 v72, v208
	v_cvt_f32_f16_sdwa v73, v208 dst_sel:DWORD dst_unused:UNUSED_PAD src0_sel:WORD_1
	v_cvt_f32_f16_e32 v74, v209
	v_cvt_f32_f16_sdwa v75, v209 dst_sel:DWORD dst_unused:UNUSED_PAD src0_sel:WORD_1
	v_cvt_f32_f16_e32 v80, v210
	v_cvt_f32_f16_sdwa v81, v210 dst_sel:DWORD dst_unused:UNUSED_PAD src0_sel:WORD_1
	v_cvt_f32_f16_e32 v82, v211
	v_cvt_f32_f16_sdwa v83, v211 dst_sel:DWORD dst_unused:UNUSED_PAD src0_sel:WORD_1
	v_sub_f32_e32 v72, v72, v238
	v_sub_f32_e32 v73, v73, v238
	v_sub_f32_e32 v74, v74, v238
	v_sub_f32_e32 v75, v75, v238
	v_sub_f32_e32 v80, v80, v238
	v_sub_f32_e32 v81, v81, v238
	v_sub_f32_e32 v82, v82, v238
	v_sub_f32_e32 v83, v83, v238
	v_pk_mul_f32 v[72:73], v[238:239], v[72:73] op_sel:[1,0]
	v_pk_mul_f32 v[74:75], v[238:239], v[74:75] op_sel:[1,0]
	v_pk_mul_f32 v[80:81], v[238:239], v[80:81] op_sel:[1,0]
	v_pk_mul_f32 v[82:83], v[238:239], v[82:83] op_sel:[1,0]
	v_pk_fma_f32 v[144:145], v[72:73], v[160:161], v[144:145]
	v_pk_fma_f32 v[146:147], v[74:75], v[162:163], v[146:147]
	v_pk_fma_f32 v[140:141], v[80:81], v[164:165], v[140:141]
	v_pk_fma_f32 v[142:143], v[82:83], v[166:167], v[142:143]
	v_cvt_pk_f16_f32 v144, v144, v145
	v_cvt_pk_f16_f32 v145, v146, v147
	v_cvt_pk_f16_f32 v146, v140, v141
	v_cvt_pk_f16_f32 v147, v142, v143
	ds_write_b128 v235, v[144:147]
	v_fma_mix_f32 v206, v144, 1.0, 0 op_sel_hi:[1,0,0]
	v_fma_mix_f32 v207, v144, v144, 0 op_sel_hi:[1,1,0]
	v_fma_mix_f32 v206, v144, 1.0, v206 op_sel:[1,0,0] op_sel_hi:[1,0,0]
	v_fma_mix_f32 v207, v144, v144, v207 op_sel:[1,1,0] op_sel_hi:[1,1,0]
	v_fma_mix_f32 v206, v145, 1.0, v206 op_sel_hi:[1,0,0]
	v_fma_mix_f32 v207, v145, v145, v207 op_sel_hi:[1,1,0]
	v_fma_mix_f32 v206, v145, 1.0, v206 op_sel:[1,0,0] op_sel_hi:[1,0,0]
	v_fma_mix_f32 v207, v145, v145, v207 op_sel:[1,1,0] op_sel_hi:[1,1,0]
	v_fma_mix_f32 v206, v146, 1.0, v206 op_sel_hi:[1,0,0]
	v_fma_mix_f32 v207, v146, v146, v207 op_sel_hi:[1,1,0]
	v_fma_mix_f32 v206, v146, 1.0, v206 op_sel:[1,0,0] op_sel_hi:[1,0,0]
	v_fma_mix_f32 v207, v146, v146, v207 op_sel:[1,1,0] op_sel_hi:[1,1,0]
	v_fma_mix_f32 v206, v147, 1.0, v206 op_sel_hi:[1,0,0]
	v_fma_mix_f32 v207, v147, v147, v207 op_sel_hi:[1,1,0]
	v_fma_mix_f32 v206, v147, 1.0, v206 op_sel:[1,0,0] op_sel_hi:[1,0,0]
	v_fma_mix_f32 v207, v147, v147, v207 op_sel:[1,1,0] op_sel_hi:[1,1,0]
	s_waitcnt vmcnt(10)
	v_cvt_f32_f16_e32 v72, v212
	v_cvt_f32_f16_sdwa v73, v212 dst_sel:DWORD dst_unused:UNUSED_PAD src0_sel:WORD_1
	v_cvt_f32_f16_e32 v74, v213
	v_cvt_f32_f16_sdwa v75, v213 dst_sel:DWORD dst_unused:UNUSED_PAD src0_sel:WORD_1
	v_cvt_f32_f16_e32 v80, v214
	v_cvt_f32_f16_sdwa v81, v214 dst_sel:DWORD dst_unused:UNUSED_PAD src0_sel:WORD_1
	v_cvt_f32_f16_e32 v82, v215
	v_cvt_f32_f16_sdwa v83, v215 dst_sel:DWORD dst_unused:UNUSED_PAD src0_sel:WORD_1
	v_sub_f32_e32 v72, v72, v238
	v_sub_f32_e32 v73, v73, v238
	v_sub_f32_e32 v74, v74, v238
	v_sub_f32_e32 v75, v75, v238
	v_sub_f32_e32 v80, v80, v238
	v_sub_f32_e32 v81, v81, v238
	v_sub_f32_e32 v82, v82, v238
	v_sub_f32_e32 v83, v83, v238
	v_pk_mul_f32 v[72:73], v[238:239], v[72:73] op_sel:[1,0]
	v_pk_mul_f32 v[74:75], v[238:239], v[74:75] op_sel:[1,0]
	v_pk_mul_f32 v[80:81], v[238:239], v[80:81] op_sel:[1,0]
	v_pk_mul_f32 v[82:83], v[238:239], v[82:83] op_sel:[1,0]
	v_pk_fma_f32 v[132:133], v[72:73], v[168:169], v[132:133]
	v_pk_fma_f32 v[134:135], v[74:75], v[170:171], v[134:135]
	v_pk_fma_f32 v[128:129], v[80:81], v[172:173], v[128:129]
	v_pk_fma_f32 v[130:131], v[82:83], v[174:175], v[130:131]
	v_cvt_pk_f16_f32 v132, v132, v133
	v_cvt_pk_f16_f32 v133, v134, v135
	v_cvt_pk_f16_f32 v134, v128, v129
	v_cvt_pk_f16_f32 v135, v130, v131
	ds_write_b128 v235, v[132:135] offset:64
	v_fma_mix_f32 v206, v132, 1.0, v206 op_sel_hi:[1,0,0]
	v_fma_mix_f32 v207, v132, v132, v207 op_sel_hi:[1,1,0]
	v_fma_mix_f32 v206, v132, 1.0, v206 op_sel:[1,0,0] op_sel_hi:[1,0,0]
	v_fma_mix_f32 v207, v132, v132, v207 op_sel:[1,1,0] op_sel_hi:[1,1,0]
	v_fma_mix_f32 v206, v133, 1.0, v206 op_sel_hi:[1,0,0]
	v_fma_mix_f32 v207, v133, v133, v207 op_sel_hi:[1,1,0]
	v_fma_mix_f32 v206, v133, 1.0, v206 op_sel:[1,0,0] op_sel_hi:[1,0,0]
	v_fma_mix_f32 v207, v133, v133, v207 op_sel:[1,1,0] op_sel_hi:[1,1,0]
	v_fma_mix_f32 v206, v134, 1.0, v206 op_sel_hi:[1,0,0]
	v_fma_mix_f32 v207, v134, v134, v207 op_sel_hi:[1,1,0]
	v_fma_mix_f32 v206, v134, 1.0, v206 op_sel:[1,0,0] op_sel_hi:[1,0,0]
	v_fma_mix_f32 v207, v134, v134, v207 op_sel:[1,1,0] op_sel_hi:[1,1,0]
	v_fma_mix_f32 v206, v135, 1.0, v206 op_sel_hi:[1,0,0]
	v_fma_mix_f32 v207, v135, v135, v207 op_sel_hi:[1,1,0]
	v_fma_mix_f32 v206, v135, 1.0, v206 op_sel:[1,0,0] op_sel_hi:[1,0,0]
	v_fma_mix_f32 v207, v135, v135, v207 op_sel:[1,1,0] op_sel_hi:[1,1,0]
	ds_read_b128 v[88:91], v236
	ds_read_b128 v[92:95], v236 offset:1152
	s_waitcnt vmcnt(9)
	v_cvt_f32_f16_e32 v72, v216
	v_cvt_f32_f16_sdwa v73, v216 dst_sel:DWORD dst_unused:UNUSED_PAD src0_sel:WORD_1
	v_cvt_f32_f16_e32 v74, v217
	v_cvt_f32_f16_sdwa v75, v217 dst_sel:DWORD dst_unused:UNUSED_PAD src0_sel:WORD_1
	v_cvt_f32_f16_e32 v80, v218
	v_cvt_f32_f16_sdwa v81, v218 dst_sel:DWORD dst_unused:UNUSED_PAD src0_sel:WORD_1
	v_cvt_f32_f16_e32 v82, v219
	v_cvt_f32_f16_sdwa v83, v219 dst_sel:DWORD dst_unused:UNUSED_PAD src0_sel:WORD_1
	v_sub_f32_e32 v72, v72, v192
	v_sub_f32_e32 v73, v73, v192
	v_sub_f32_e32 v74, v74, v192
	v_sub_f32_e32 v75, v75, v192
	v_sub_f32_e32 v80, v80, v192
	v_sub_f32_e32 v81, v81, v192
	v_sub_f32_e32 v82, v82, v192
	v_sub_f32_e32 v83, v83, v192
	v_pk_mul_f32 v[72:73], v[192:193], v[72:73] op_sel:[1,0]
	v_pk_mul_f32 v[74:75], v[192:193], v[74:75] op_sel:[1,0]
	v_pk_mul_f32 v[80:81], v[192:193], v[80:81] op_sel:[1,0]
	v_pk_mul_f32 v[82:83], v[192:193], v[82:83] op_sel:[1,0]
	v_pk_fma_f32 v[124:125], v[72:73], v[160:161], v[124:125]
	v_pk_fma_f32 v[126:127], v[74:75], v[162:163], v[126:127]
	v_pk_fma_f32 v[120:121], v[80:81], v[164:165], v[120:121]
	v_pk_fma_f32 v[122:123], v[82:83], v[166:167], v[122:123]
	v_cvt_pk_f16_f32 v124, v124, v125
	v_cvt_pk_f16_f32 v125, v126, v127
	v_cvt_pk_f16_f32 v126, v120, v121
	v_cvt_pk_f16_f32 v127, v122, v123
	s_waitcnt lgkmcnt(0)
	buffer_store_dwordx4 v[88:91], v225, s[24:27], 0 offen nt
	v_add_u32_e32 v82, 0x3000, v225
	buffer_store_dwordx4 v[92:95], v82, s[24:27], 0 offen nt
	ds_write_b128 v235, v[124:127]
	v_fma_mix_f32 v140, v124, 1.0, 0 op_sel_hi:[1,0,0]
	v_fma_mix_f32 v141, v124, v124, 0 op_sel_hi:[1,1,0]
	v_fma_mix_f32 v140, v124, 1.0, v140 op_sel:[1,0,0] op_sel_hi:[1,0,0]
	v_fma_mix_f32 v141, v124, v124, v141 op_sel:[1,1,0] op_sel_hi:[1,1,0]
	v_fma_mix_f32 v140, v125, 1.0, v140 op_sel_hi:[1,0,0]
	v_fma_mix_f32 v141, v125, v125, v141 op_sel_hi:[1,1,0]
	v_fma_mix_f32 v140, v125, 1.0, v140 op_sel:[1,0,0] op_sel_hi:[1,0,0]
	v_fma_mix_f32 v141, v125, v125, v141 op_sel:[1,1,0] op_sel_hi:[1,1,0]
	v_fma_mix_f32 v140, v126, 1.0, v140 op_sel_hi:[1,0,0]
	v_fma_mix_f32 v141, v126, v126, v141 op_sel_hi:[1,1,0]
	v_fma_mix_f32 v140, v126, 1.0, v140 op_sel:[1,0,0] op_sel_hi:[1,0,0]
	v_fma_mix_f32 v141, v126, v126, v141 op_sel:[1,1,0] op_sel_hi:[1,1,0]
	v_fma_mix_f32 v140, v127, 1.0, v140 op_sel_hi:[1,0,0]
	v_fma_mix_f32 v141, v127, v127, v141 op_sel_hi:[1,1,0]
	v_fma_mix_f32 v140, v127, 1.0, v140 op_sel:[1,0,0] op_sel_hi:[1,0,0]
	v_fma_mix_f32 v141, v127, v127, v141 op_sel:[1,1,0] op_sel_hi:[1,1,0]
	s_waitcnt vmcnt(10)
	v_cvt_f32_f16_e32 v72, v220
	v_cvt_f32_f16_sdwa v73, v220 dst_sel:DWORD dst_unused:UNUSED_PAD src0_sel:WORD_1
	v_cvt_f32_f16_e32 v74, v221
	v_cvt_f32_f16_sdwa v75, v221 dst_sel:DWORD dst_unused:UNUSED_PAD src0_sel:WORD_1
	v_cvt_f32_f16_e32 v80, v222
	v_cvt_f32_f16_sdwa v81, v222 dst_sel:DWORD dst_unused:UNUSED_PAD src0_sel:WORD_1
	v_cvt_f32_f16_e32 v82, v223
	v_cvt_f32_f16_sdwa v83, v223 dst_sel:DWORD dst_unused:UNUSED_PAD src0_sel:WORD_1
	v_sub_f32_e32 v72, v72, v192
	v_sub_f32_e32 v73, v73, v192
	v_sub_f32_e32 v74, v74, v192
	v_sub_f32_e32 v75, v75, v192
	v_sub_f32_e32 v80, v80, v192
	v_sub_f32_e32 v81, v81, v192
	v_sub_f32_e32 v82, v82, v192
	v_sub_f32_e32 v83, v83, v192
	v_pk_mul_f32 v[72:73], v[192:193], v[72:73] op_sel:[1,0]
	v_pk_mul_f32 v[74:75], v[192:193], v[74:75] op_sel:[1,0]
	v_pk_mul_f32 v[80:81], v[192:193], v[80:81] op_sel:[1,0]
	v_pk_mul_f32 v[82:83], v[192:193], v[82:83] op_sel:[1,0]
	v_pk_fma_f32 v[116:117], v[72:73], v[168:169], v[116:117]
	v_pk_fma_f32 v[118:119], v[74:75], v[170:171], v[118:119]
	v_pk_fma_f32 v[112:113], v[80:81], v[172:173], v[112:113]
	v_pk_fma_f32 v[114:115], v[82:83], v[174:175], v[114:115]
	v_cvt_pk_f16_f32 v116, v116, v117
	v_cvt_pk_f16_f32 v117, v118, v119
	v_cvt_pk_f16_f32 v118, v112, v113
	v_cvt_pk_f16_f32 v119, v114, v115
	ds_write_b128 v235, v[116:119] offset:64
	v_fma_mix_f32 v140, v116, 1.0, v140 op_sel_hi:[1,0,0]
	v_fma_mix_f32 v141, v116, v116, v141 op_sel_hi:[1,1,0]
	v_fma_mix_f32 v140, v116, 1.0, v140 op_sel:[1,0,0] op_sel_hi:[1,0,0]
	v_fma_mix_f32 v141, v116, v116, v141 op_sel:[1,1,0] op_sel_hi:[1,1,0]
	v_fma_mix_f32 v140, v117, 1.0, v140 op_sel_hi:[1,0,0]
	v_fma_mix_f32 v141, v117, v117, v141 op_sel_hi:[1,1,0]
	v_fma_mix_f32 v140, v117, 1.0, v140 op_sel:[1,0,0] op_sel_hi:[1,0,0]
	v_fma_mix_f32 v141, v117, v117, v141 op_sel:[1,1,0] op_sel_hi:[1,1,0]
	v_fma_mix_f32 v140, v118, 1.0, v140 op_sel_hi:[1,0,0]
	v_fma_mix_f32 v141, v118, v118, v141 op_sel_hi:[1,1,0]
	v_fma_mix_f32 v140, v118, 1.0, v140 op_sel:[1,0,0] op_sel_hi:[1,0,0]
	v_fma_mix_f32 v141, v118, v118, v141 op_sel:[1,1,0] op_sel_hi:[1,1,0]
	v_fma_mix_f32 v140, v119, 1.0, v140 op_sel_hi:[1,0,0]
	v_fma_mix_f32 v141, v119, v119, v141 op_sel_hi:[1,1,0]
	v_fma_mix_f32 v140, v119, 1.0, v140 op_sel:[1,0,0] op_sel_hi:[1,0,0]
	v_fma_mix_f32 v141, v119, v119, v141 op_sel:[1,1,0] op_sel_hi:[1,1,0]
	ds_read_b128 v[208:211], v236
	ds_read_b128 v[128:131], v236 offset:1152
	s_add_u32 s94, s98, 0x3c000
	s_addc_u32 s95, s99, 0
	global_load_dwordx4 v[212:215], v191, s[94:95] offset:0 nt
	global_load_dwordx4 v[144:147], v191, s[94:95] offset:64 nt
	s_add_u32 s94, s98, 0x42000
	s_addc_u32 s95, s99, 0
	global_load_dwordx4 v[132:135], v191, s[94:95] offset:0 nt
	global_load_dwordx4 v[88:91], v191, s[94:95] offset:64 nt
	s_waitcnt vmcnt(13)
	v_cvt_f32_f16_e32 v72, v240
	v_cvt_f32_f16_sdwa v73, v240 dst_sel:DWORD dst_unused:UNUSED_PAD src0_sel:WORD_1
	v_cvt_f32_f16_e32 v74, v241
	v_cvt_f32_f16_sdwa v75, v241 dst_sel:DWORD dst_unused:UNUSED_PAD src0_sel:WORD_1
	v_cvt_f32_f16_e32 v80, v242
	v_cvt_f32_f16_sdwa v81, v242 dst_sel:DWORD dst_unused:UNUSED_PAD src0_sel:WORD_1
	v_cvt_f32_f16_e32 v82, v243
	v_cvt_f32_f16_sdwa v83, v243 dst_sel:DWORD dst_unused:UNUSED_PAD src0_sel:WORD_1
	v_sub_f32_e32 v72, v72, v194
	v_sub_f32_e32 v73, v73, v194
	v_sub_f32_e32 v74, v74, v194
	v_sub_f32_e32 v75, v75, v194
	v_sub_f32_e32 v80, v80, v194
	v_sub_f32_e32 v81, v81, v194
	v_sub_f32_e32 v82, v82, v194
	v_sub_f32_e32 v83, v83, v194
	v_pk_mul_f32 v[72:73], v[194:195], v[72:73] op_sel:[1,0]
	v_pk_mul_f32 v[74:75], v[194:195], v[74:75] op_sel:[1,0]
	v_pk_mul_f32 v[80:81], v[194:195], v[80:81] op_sel:[1,0]
	v_pk_mul_f32 v[82:83], v[194:195], v[82:83] op_sel:[1,0]
	v_pk_fma_f32 v[108:109], v[72:73], v[160:161], v[108:109]
	v_pk_fma_f32 v[110:111], v[74:75], v[162:163], v[110:111]
	v_pk_fma_f32 v[104:105], v[80:81], v[164:165], v[104:105]
	v_pk_fma_f32 v[106:107], v[82:83], v[166:167], v[106:107]
	v_cvt_pk_f16_f32 v108, v108, v109
	v_cvt_pk_f16_f32 v109, v110, v111
	v_cvt_pk_f16_f32 v110, v104, v105
	v_cvt_pk_f16_f32 v111, v106, v107
	s_waitcnt lgkmcnt(0)
	v_add_u32_e32 v83, 0x6000, v225
	buffer_store_dwordx4 v[208:211], v83, s[24:27], 0 offen nt
	v_add_u32_e32 v82, 0x9000, v225
	buffer_store_dwordx4 v[128:131], v82, s[24:27], 0 offen nt
	ds_write_b128 v235, v[108:111]
	v_fma_mix_f32 v142, v108, 1.0, 0 op_sel_hi:[1,0,0]
	v_fma_mix_f32 v143, v108, v108, 0 op_sel_hi:[1,1,0]
	v_fma_mix_f32 v142, v108, 1.0, v142 op_sel:[1,0,0] op_sel_hi:[1,0,0]
	v_fma_mix_f32 v143, v108, v108, v143 op_sel:[1,1,0] op_sel_hi:[1,1,0]
	v_fma_mix_f32 v142, v109, 1.0, v142 op_sel_hi:[1,0,0]
	v_fma_mix_f32 v143, v109, v109, v143 op_sel_hi:[1,1,0]
	v_fma_mix_f32 v142, v109, 1.0, v142 op_sel:[1,0,0] op_sel_hi:[1,0,0]
	v_fma_mix_f32 v143, v109, v109, v143 op_sel:[1,1,0] op_sel_hi:[1,1,0]
	v_fma_mix_f32 v142, v110, 1.0, v142 op_sel_hi:[1,0,0]
	v_fma_mix_f32 v143, v110, v110, v143 op_sel_hi:[1,1,0]
	v_fma_mix_f32 v142, v110, 1.0, v142 op_sel:[1,0,0] op_sel_hi:[1,0,0]
	v_fma_mix_f32 v143, v110, v110, v143 op_sel:[1,1,0] op_sel_hi:[1,1,0]
	v_fma_mix_f32 v142, v111, 1.0, v142 op_sel_hi:[1,0,0]
	v_fma_mix_f32 v143, v111, v111, v143 op_sel_hi:[1,1,0]
	v_fma_mix_f32 v142, v111, 1.0, v142 op_sel:[1,0,0] op_sel_hi:[1,0,0]
	v_fma_mix_f32 v143, v111, v111, v143 op_sel:[1,1,0] op_sel_hi:[1,1,0]
	s_waitcnt vmcnt(14)
	v_cvt_f32_f16_e32 v72, v244
	v_cvt_f32_f16_sdwa v73, v244 dst_sel:DWORD dst_unused:UNUSED_PAD src0_sel:WORD_1
	v_cvt_f32_f16_e32 v74, v245
	v_cvt_f32_f16_sdwa v75, v245 dst_sel:DWORD dst_unused:UNUSED_PAD src0_sel:WORD_1
	v_cvt_f32_f16_e32 v80, v246
	v_cvt_f32_f16_sdwa v81, v246 dst_sel:DWORD dst_unused:UNUSED_PAD src0_sel:WORD_1
	v_cvt_f32_f16_e32 v82, v247
	v_cvt_f32_f16_sdwa v83, v247 dst_sel:DWORD dst_unused:UNUSED_PAD src0_sel:WORD_1
	v_sub_f32_e32 v72, v72, v194
	v_sub_f32_e32 v73, v73, v194
	v_sub_f32_e32 v74, v74, v194
	v_sub_f32_e32 v75, v75, v194
	v_sub_f32_e32 v80, v80, v194
	v_sub_f32_e32 v81, v81, v194
	v_sub_f32_e32 v82, v82, v194
	v_sub_f32_e32 v83, v83, v194
	v_pk_mul_f32 v[72:73], v[194:195], v[72:73] op_sel:[1,0]
	v_pk_mul_f32 v[74:75], v[194:195], v[74:75] op_sel:[1,0]
	v_pk_mul_f32 v[80:81], v[194:195], v[80:81] op_sel:[1,0]
	v_pk_mul_f32 v[82:83], v[194:195], v[82:83] op_sel:[1,0]
	v_pk_fma_f32 v[100:101], v[72:73], v[168:169], v[100:101]
	v_pk_fma_f32 v[102:103], v[74:75], v[170:171], v[102:103]
	v_pk_fma_f32 v[96:97], v[80:81], v[172:173], v[96:97]
	v_pk_fma_f32 v[98:99], v[82:83], v[174:175], v[98:99]
	v_cvt_pk_f16_f32 v100, v100, v101
	v_cvt_pk_f16_f32 v101, v102, v103
	v_cvt_pk_f16_f32 v102, v96, v97
	v_cvt_pk_f16_f32 v103, v98, v99
	ds_write_b128 v235, v[100:103] offset:64
	v_fma_mix_f32 v142, v100, 1.0, v142 op_sel_hi:[1,0,0]
	v_fma_mix_f32 v143, v100, v100, v143 op_sel_hi:[1,1,0]
	v_fma_mix_f32 v142, v100, 1.0, v142 op_sel:[1,0,0] op_sel_hi:[1,0,0]
	v_fma_mix_f32 v143, v100, v100, v143 op_sel:[1,1,0] op_sel_hi:[1,1,0]
	v_fma_mix_f32 v142, v101, 1.0, v142 op_sel_hi:[1,0,0]
	v_fma_mix_f32 v143, v101, v101, v143 op_sel_hi:[1,1,0]
	v_fma_mix_f32 v142, v101, 1.0, v142 op_sel:[1,0,0] op_sel_hi:[1,0,0]
	v_fma_mix_f32 v143, v101, v101, v143 op_sel:[1,1,0] op_sel_hi:[1,1,0]
	v_fma_mix_f32 v142, v102, 1.0, v142 op_sel_hi:[1,0,0]
	v_fma_mix_f32 v143, v102, v102, v143 op_sel_hi:[1,1,0]
	v_fma_mix_f32 v142, v102, 1.0, v142 op_sel:[1,0,0] op_sel_hi:[1,0,0]
	v_fma_mix_f32 v143, v102, v102, v143 op_sel:[1,1,0] op_sel_hi:[1,1,0]
	v_fma_mix_f32 v142, v103, 1.0, v142 op_sel_hi:[1,0,0]
	v_fma_mix_f32 v143, v103, v103, v143 op_sel_hi:[1,1,0]
	v_fma_mix_f32 v142, v103, 1.0, v142 op_sel:[1,0,0] op_sel_hi:[1,0,0]
	v_fma_mix_f32 v143, v103, v103, v143 op_sel:[1,1,0] op_sel_hi:[1,1,0]
	ds_read_b128 v[92:95], v236
	ds_read_b128 v[120:123], v236 offset:1152
	s_waitcnt vmcnt(13)
	v_cvt_f32_f16_e32 v72, v248
	v_cvt_f32_f16_sdwa v73, v248 dst_sel:DWORD dst_unused:UNUSED_PAD src0_sel:WORD_1
	v_cvt_f32_f16_e32 v74, v249
	v_cvt_f32_f16_sdwa v75, v249 dst_sel:DWORD dst_unused:UNUSED_PAD src0_sel:WORD_1
	v_cvt_f32_f16_e32 v80, v250
	v_cvt_f32_f16_sdwa v81, v250 dst_sel:DWORD dst_unused:UNUSED_PAD src0_sel:WORD_1
	v_cvt_f32_f16_e32 v82, v251
	v_cvt_f32_f16_sdwa v83, v251 dst_sel:DWORD dst_unused:UNUSED_PAD src0_sel:WORD_1
	v_sub_f32_e32 v72, v72, v196
	v_sub_f32_e32 v73, v73, v196
	v_sub_f32_e32 v74, v74, v196
	v_sub_f32_e32 v75, v75, v196
	v_sub_f32_e32 v80, v80, v196
	v_sub_f32_e32 v81, v81, v196
	v_sub_f32_e32 v82, v82, v196
	v_sub_f32_e32 v83, v83, v196
	v_pk_mul_f32 v[72:73], v[196:197], v[72:73] op_sel:[1,0]
	v_pk_mul_f32 v[74:75], v[196:197], v[74:75] op_sel:[1,0]
	v_pk_mul_f32 v[80:81], v[196:197], v[80:81] op_sel:[1,0]
	v_pk_mul_f32 v[82:83], v[196:197], v[82:83] op_sel:[1,0]
	v_pk_fma_f32 v[84:85], v[72:73], v[160:161], v[84:85]
	v_pk_fma_f32 v[86:87], v[74:75], v[162:163], v[86:87]
	v_pk_fma_f32 v[76:77], v[80:81], v[164:165], v[76:77]
	v_pk_fma_f32 v[78:79], v[82:83], v[166:167], v[78:79]
	v_cvt_pk_f16_f32 v84, v84, v85
	v_cvt_pk_f16_f32 v85, v86, v87
	v_cvt_pk_f16_f32 v86, v76, v77
	v_cvt_pk_f16_f32 v87, v78, v79
	s_waitcnt lgkmcnt(0)
	v_add_u32_e32 v83, 0xc000, v225
	buffer_store_dwordx4 v[92:95], v83, s[24:27], 0 offen nt
	v_add_u32_e32 v82, 0xf000, v225
	buffer_store_dwordx4 v[120:123], v82, s[24:27], 0 offen nt
	ds_write_b128 v235, v[84:87]
	v_fma_mix_f32 v216, v84, 1.0, 0 op_sel_hi:[1,0,0]
	v_fma_mix_f32 v217, v84, v84, 0 op_sel_hi:[1,1,0]
	v_fma_mix_f32 v216, v84, 1.0, v216 op_sel:[1,0,0] op_sel_hi:[1,0,0]
	v_fma_mix_f32 v217, v84, v84, v217 op_sel:[1,1,0] op_sel_hi:[1,1,0]
	v_fma_mix_f32 v216, v85, 1.0, v216 op_sel_hi:[1,0,0]
	v_fma_mix_f32 v217, v85, v85, v217 op_sel_hi:[1,1,0]
	v_fma_mix_f32 v216, v85, 1.0, v216 op_sel:[1,0,0] op_sel_hi:[1,0,0]
	v_fma_mix_f32 v217, v85, v85, v217 op_sel:[1,1,0] op_sel_hi:[1,1,0]
	v_fma_mix_f32 v216, v86, 1.0, v216 op_sel_hi:[1,0,0]
	v_fma_mix_f32 v217, v86, v86, v217 op_sel_hi:[1,1,0]
	v_fma_mix_f32 v216, v86, 1.0, v216 op_sel:[1,0,0] op_sel_hi:[1,0,0]
	v_fma_mix_f32 v217, v86, v86, v217 op_sel:[1,1,0] op_sel_hi:[1,1,0]
	v_fma_mix_f32 v216, v87, 1.0, v216 op_sel_hi:[1,0,0]
	v_fma_mix_f32 v217, v87, v87, v217 op_sel_hi:[1,1,0]
	v_fma_mix_f32 v216, v87, 1.0, v216 op_sel:[1,0,0] op_sel_hi:[1,0,0]
	v_fma_mix_f32 v217, v87, v87, v217 op_sel:[1,1,0] op_sel_hi:[1,1,0]
	s_waitcnt vmcnt(14)
	v_cvt_f32_f16_e32 v72, v252
	v_cvt_f32_f16_sdwa v73, v252 dst_sel:DWORD dst_unused:UNUSED_PAD src0_sel:WORD_1
	v_cvt_f32_f16_e32 v74, v253
	v_cvt_f32_f16_sdwa v75, v253 dst_sel:DWORD dst_unused:UNUSED_PAD src0_sel:WORD_1
	v_cvt_f32_f16_e32 v80, v254
	v_cvt_f32_f16_sdwa v81, v254 dst_sel:DWORD dst_unused:UNUSED_PAD src0_sel:WORD_1
	v_cvt_f32_f16_e32 v82, v255
	v_cvt_f32_f16_sdwa v83, v255 dst_sel:DWORD dst_unused:UNUSED_PAD src0_sel:WORD_1
	v_sub_f32_e32 v72, v72, v196
	v_sub_f32_e32 v73, v73, v196
	v_sub_f32_e32 v74, v74, v196
	v_sub_f32_e32 v75, v75, v196
	v_sub_f32_e32 v80, v80, v196
	v_sub_f32_e32 v81, v81, v196
	v_sub_f32_e32 v82, v82, v196
	v_sub_f32_e32 v83, v83, v196
	v_pk_mul_f32 v[72:73], v[196:197], v[72:73] op_sel:[1,0]
	v_pk_mul_f32 v[74:75], v[196:197], v[74:75] op_sel:[1,0]
	v_pk_mul_f32 v[80:81], v[196:197], v[80:81] op_sel:[1,0]
	v_pk_mul_f32 v[82:83], v[196:197], v[82:83] op_sel:[1,0]
	v_pk_fma_f32 v[68:69], v[72:73], v[168:169], v[68:69]
	v_pk_fma_f32 v[70:71], v[74:75], v[170:171], v[70:71]
	v_pk_fma_f32 v[64:65], v[80:81], v[172:173], v[64:65]
	v_pk_fma_f32 v[66:67], v[82:83], v[174:175], v[66:67]
	v_cvt_pk_f16_f32 v68, v68, v69
	v_cvt_pk_f16_f32 v69, v70, v71
	v_cvt_pk_f16_f32 v70, v64, v65
	v_cvt_pk_f16_f32 v71, v66, v67
	ds_write_b128 v235, v[68:71] offset:64
	v_fma_mix_f32 v216, v68, 1.0, v216 op_sel_hi:[1,0,0]
	v_fma_mix_f32 v217, v68, v68, v217 op_sel_hi:[1,1,0]
	v_fma_mix_f32 v216, v68, 1.0, v216 op_sel:[1,0,0] op_sel_hi:[1,0,0]
	v_fma_mix_f32 v217, v68, v68, v217 op_sel:[1,1,0] op_sel_hi:[1,1,0]
	v_fma_mix_f32 v216, v69, 1.0, v216 op_sel_hi:[1,0,0]
	v_fma_mix_f32 v217, v69, v69, v217 op_sel_hi:[1,1,0]
	v_fma_mix_f32 v216, v69, 1.0, v216 op_sel:[1,0,0] op_sel_hi:[1,0,0]
	v_fma_mix_f32 v217, v69, v69, v217 op_sel:[1,1,0] op_sel_hi:[1,1,0]
	v_fma_mix_f32 v216, v70, 1.0, v216 op_sel_hi:[1,0,0]
	v_fma_mix_f32 v217, v70, v70, v217 op_sel_hi:[1,1,0]
	v_fma_mix_f32 v216, v70, 1.0, v216 op_sel:[1,0,0] op_sel_hi:[1,0,0]
	v_fma_mix_f32 v217, v70, v70, v217 op_sel:[1,1,0] op_sel_hi:[1,1,0]
	v_fma_mix_f32 v216, v71, 1.0, v216 op_sel_hi:[1,0,0]
	v_fma_mix_f32 v217, v71, v71, v217 op_sel_hi:[1,1,0]
	v_fma_mix_f32 v216, v71, 1.0, v216 op_sel:[1,0,0] op_sel_hi:[1,0,0]
	v_fma_mix_f32 v217, v71, v71, v217 op_sel:[1,1,0] op_sel_hi:[1,1,0]
	ds_read_b128 v[112:115], v236
	ds_read_b128 v[220:223], v236 offset:1152
	s_waitcnt vmcnt(13)
	v_cvt_f32_f16_e32 v72, v136
	v_cvt_f32_f16_sdwa v73, v136 dst_sel:DWORD dst_unused:UNUSED_PAD src0_sel:WORD_1
	v_cvt_f32_f16_e32 v74, v137
	v_cvt_f32_f16_sdwa v75, v137 dst_sel:DWORD dst_unused:UNUSED_PAD src0_sel:WORD_1
	v_cvt_f32_f16_e32 v80, v138
	v_cvt_f32_f16_sdwa v81, v138 dst_sel:DWORD dst_unused:UNUSED_PAD src0_sel:WORD_1
	v_cvt_f32_f16_e32 v82, v139
	v_cvt_f32_f16_sdwa v83, v139 dst_sel:DWORD dst_unused:UNUSED_PAD src0_sel:WORD_1
	v_sub_f32_e32 v72, v72, v198
	v_sub_f32_e32 v73, v73, v198
	v_sub_f32_e32 v74, v74, v198
	v_sub_f32_e32 v75, v75, v198
	v_sub_f32_e32 v80, v80, v198
	v_sub_f32_e32 v81, v81, v198
	v_sub_f32_e32 v82, v82, v198
	v_sub_f32_e32 v83, v83, v198
	v_pk_mul_f32 v[72:73], v[198:199], v[72:73] op_sel:[1,0]
	v_pk_mul_f32 v[74:75], v[198:199], v[74:75] op_sel:[1,0]
	v_pk_mul_f32 v[80:81], v[198:199], v[80:81] op_sel:[1,0]
	v_pk_mul_f32 v[82:83], v[198:199], v[82:83] op_sel:[1,0]
	v_pk_fma_f32 v[60:61], v[72:73], v[160:161], v[60:61]
	v_pk_fma_f32 v[62:63], v[74:75], v[162:163], v[62:63]
	v_pk_fma_f32 v[56:57], v[80:81], v[164:165], v[56:57]
	v_pk_fma_f32 v[58:59], v[82:83], v[166:167], v[58:59]
	v_cvt_pk_f16_f32 v60, v60, v61
	v_cvt_pk_f16_f32 v61, v62, v63
	v_cvt_pk_f16_f32 v62, v56, v57
	v_cvt_pk_f16_f32 v63, v58, v59
	s_waitcnt lgkmcnt(0)
	v_add_u32_e32 v83, 0x12000, v225
	buffer_store_dwordx4 v[112:115], v83, s[24:27], 0 offen nt
	v_add_u32_e32 v82, 0x15000, v225
	buffer_store_dwordx4 v[220:223], v82, s[24:27], 0 offen nt
	ds_write_b128 v235, v[60:63]
	v_fma_mix_f32 v218, v60, 1.0, 0 op_sel_hi:[1,0,0]
	v_fma_mix_f32 v219, v60, v60, 0 op_sel_hi:[1,1,0]
	v_fma_mix_f32 v218, v60, 1.0, v218 op_sel:[1,0,0] op_sel_hi:[1,0,0]
	v_fma_mix_f32 v219, v60, v60, v219 op_sel:[1,1,0] op_sel_hi:[1,1,0]
	v_fma_mix_f32 v218, v61, 1.0, v218 op_sel_hi:[1,0,0]
	v_fma_mix_f32 v219, v61, v61, v219 op_sel_hi:[1,1,0]
	v_fma_mix_f32 v218, v61, 1.0, v218 op_sel:[1,0,0] op_sel_hi:[1,0,0]
	v_fma_mix_f32 v219, v61, v61, v219 op_sel:[1,1,0] op_sel_hi:[1,1,0]
	v_fma_mix_f32 v218, v62, 1.0, v218 op_sel_hi:[1,0,0]
	v_fma_mix_f32 v219, v62, v62, v219 op_sel_hi:[1,1,0]
	v_fma_mix_f32 v218, v62, 1.0, v218 op_sel:[1,0,0] op_sel_hi:[1,0,0]
	v_fma_mix_f32 v219, v62, v62, v219 op_sel:[1,1,0] op_sel_hi:[1,1,0]
	v_fma_mix_f32 v218, v63, 1.0, v218 op_sel_hi:[1,0,0]
	v_fma_mix_f32 v219, v63, v63, v219 op_sel_hi:[1,1,0]
	v_fma_mix_f32 v218, v63, 1.0, v218 op_sel:[1,0,0] op_sel_hi:[1,0,0]
	v_fma_mix_f32 v219, v63, v63, v219 op_sel:[1,1,0] op_sel_hi:[1,1,0]
	s_waitcnt vmcnt(14)
	v_cvt_f32_f16_e32 v72, v148
	v_cvt_f32_f16_sdwa v73, v148 dst_sel:DWORD dst_unused:UNUSED_PAD src0_sel:WORD_1
	v_cvt_f32_f16_e32 v74, v149
	v_cvt_f32_f16_sdwa v75, v149 dst_sel:DWORD dst_unused:UNUSED_PAD src0_sel:WORD_1
	v_cvt_f32_f16_e32 v80, v150
	v_cvt_f32_f16_sdwa v81, v150 dst_sel:DWORD dst_unused:UNUSED_PAD src0_sel:WORD_1
	v_cvt_f32_f16_e32 v82, v151
	v_cvt_f32_f16_sdwa v83, v151 dst_sel:DWORD dst_unused:UNUSED_PAD src0_sel:WORD_1
	v_sub_f32_e32 v72, v72, v198
	v_sub_f32_e32 v73, v73, v198
	v_sub_f32_e32 v74, v74, v198
	v_sub_f32_e32 v75, v75, v198
	v_sub_f32_e32 v80, v80, v198
	v_sub_f32_e32 v81, v81, v198
	v_sub_f32_e32 v82, v82, v198
	v_sub_f32_e32 v83, v83, v198
	v_pk_mul_f32 v[72:73], v[198:199], v[72:73] op_sel:[1,0]
	v_pk_mul_f32 v[74:75], v[198:199], v[74:75] op_sel:[1,0]
	v_pk_mul_f32 v[80:81], v[198:199], v[80:81] op_sel:[1,0]
	v_pk_mul_f32 v[82:83], v[198:199], v[82:83] op_sel:[1,0]
	v_pk_fma_f32 v[52:53], v[72:73], v[168:169], v[52:53]
	v_pk_fma_f32 v[54:55], v[74:75], v[170:171], v[54:55]
	v_pk_fma_f32 v[48:49], v[80:81], v[172:173], v[48:49]
	v_pk_fma_f32 v[50:51], v[82:83], v[174:175], v[50:51]
	v_cvt_pk_f16_f32 v52, v52, v53
	v_cvt_pk_f16_f32 v53, v54, v55
	v_cvt_pk_f16_f32 v54, v48, v49
	v_cvt_pk_f16_f32 v55, v50, v51
	ds_write_b128 v235, v[52:55] offset:64
	v_fma_mix_f32 v218, v52, 1.0, v218 op_sel_hi:[1,0,0]
	v_fma_mix_f32 v219, v52, v52, v219 op_sel_hi:[1,1,0]
	v_fma_mix_f32 v218, v52, 1.0, v218 op_sel:[1,0,0] op_sel_hi:[1,0,0]
	v_fma_mix_f32 v219, v52, v52, v219 op_sel:[1,1,0] op_sel_hi:[1,1,0]
	v_fma_mix_f32 v218, v53, 1.0, v218 op_sel_hi:[1,0,0]
	v_fma_mix_f32 v219, v53, v53, v219 op_sel_hi:[1,1,0]
	v_fma_mix_f32 v218, v53, 1.0, v218 op_sel:[1,0,0] op_sel_hi:[1,0,0]
	v_fma_mix_f32 v219, v53, v53, v219 op_sel:[1,1,0] op_sel_hi:[1,1,0]
	v_fma_mix_f32 v218, v54, 1.0, v218 op_sel_hi:[1,0,0]
	v_fma_mix_f32 v219, v54, v54, v219 op_sel_hi:[1,1,0]
	v_fma_mix_f32 v218, v54, 1.0, v218 op_sel:[1,0,0] op_sel_hi:[1,0,0]
	v_fma_mix_f32 v219, v54, v54, v219 op_sel:[1,1,0] op_sel_hi:[1,1,0]
	v_fma_mix_f32 v218, v55, 1.0, v218 op_sel_hi:[1,0,0]
	v_fma_mix_f32 v219, v55, v55, v219 op_sel_hi:[1,1,0]
	v_fma_mix_f32 v218, v55, 1.0, v218 op_sel:[1,0,0] op_sel_hi:[1,0,0]
	v_fma_mix_f32 v219, v55, v55, v219 op_sel:[1,1,0] op_sel_hi:[1,1,0]
	ds_read_b128 v[124:127], v236
	ds_read_b128 v[116:119], v236 offset:1152
	s_waitcnt vmcnt(13)
	v_cvt_f32_f16_e32 v72, v152
	v_cvt_f32_f16_sdwa v73, v152 dst_sel:DWORD dst_unused:UNUSED_PAD src0_sel:WORD_1
	v_cvt_f32_f16_e32 v74, v153
	v_cvt_f32_f16_sdwa v75, v153 dst_sel:DWORD dst_unused:UNUSED_PAD src0_sel:WORD_1
	v_cvt_f32_f16_e32 v80, v154
	v_cvt_f32_f16_sdwa v81, v154 dst_sel:DWORD dst_unused:UNUSED_PAD src0_sel:WORD_1
	v_cvt_f32_f16_e32 v82, v155
	v_cvt_f32_f16_sdwa v83, v155 dst_sel:DWORD dst_unused:UNUSED_PAD src0_sel:WORD_1
	v_sub_f32_e32 v72, v72, v200
	v_sub_f32_e32 v73, v73, v200
	v_sub_f32_e32 v74, v74, v200
	v_sub_f32_e32 v75, v75, v200
	v_sub_f32_e32 v80, v80, v200
	v_sub_f32_e32 v81, v81, v200
	v_sub_f32_e32 v82, v82, v200
	v_sub_f32_e32 v83, v83, v200
	v_pk_mul_f32 v[72:73], v[200:201], v[72:73] op_sel:[1,0]
	v_pk_mul_f32 v[74:75], v[200:201], v[74:75] op_sel:[1,0]
	v_pk_mul_f32 v[80:81], v[200:201], v[80:81] op_sel:[1,0]
	v_pk_mul_f32 v[82:83], v[200:201], v[82:83] op_sel:[1,0]
	v_pk_fma_f32 v[44:45], v[72:73], v[160:161], v[44:45]
	v_pk_fma_f32 v[46:47], v[74:75], v[162:163], v[46:47]
	v_pk_fma_f32 v[40:41], v[80:81], v[164:165], v[40:41]
	v_pk_fma_f32 v[42:43], v[82:83], v[166:167], v[42:43]
	v_cvt_pk_f16_f32 v44, v44, v45
	v_cvt_pk_f16_f32 v45, v46, v47
	v_cvt_pk_f16_f32 v46, v40, v41
	v_cvt_pk_f16_f32 v47, v42, v43
	s_waitcnt lgkmcnt(0)
	v_add_u32_e32 v83, 0x30000, v225
	buffer_store_dwordx4 v[124:127], v83, s[24:27], 0 offen nt
	v_add_u32_e32 v82, 0x33000, v225
	buffer_store_dwordx4 v[116:119], v82, s[24:27], 0 offen nt
	ds_write_b128 v235, v[44:47]
	v_fma_mix_f32 v208, v44, 1.0, 0 op_sel_hi:[1,0,0]
	v_fma_mix_f32 v209, v44, v44, 0 op_sel_hi:[1,1,0]
	v_fma_mix_f32 v208, v44, 1.0, v208 op_sel:[1,0,0] op_sel_hi:[1,0,0]
	v_fma_mix_f32 v209, v44, v44, v209 op_sel:[1,1,0] op_sel_hi:[1,1,0]
	v_fma_mix_f32 v208, v45, 1.0, v208 op_sel_hi:[1,0,0]
	v_fma_mix_f32 v209, v45, v45, v209 op_sel_hi:[1,1,0]
	v_fma_mix_f32 v208, v45, 1.0, v208 op_sel:[1,0,0] op_sel_hi:[1,0,0]
	v_fma_mix_f32 v209, v45, v45, v209 op_sel:[1,1,0] op_sel_hi:[1,1,0]
	v_fma_mix_f32 v208, v46, 1.0, v208 op_sel_hi:[1,0,0]
	v_fma_mix_f32 v209, v46, v46, v209 op_sel_hi:[1,1,0]
	v_fma_mix_f32 v208, v46, 1.0, v208 op_sel:[1,0,0] op_sel_hi:[1,0,0]
	v_fma_mix_f32 v209, v46, v46, v209 op_sel:[1,1,0] op_sel_hi:[1,1,0]
	v_fma_mix_f32 v208, v47, 1.0, v208 op_sel_hi:[1,0,0]
	v_fma_mix_f32 v209, v47, v47, v209 op_sel_hi:[1,1,0]
	v_fma_mix_f32 v208, v47, 1.0, v208 op_sel:[1,0,0] op_sel_hi:[1,0,0]
	v_fma_mix_f32 v209, v47, v47, v209 op_sel:[1,1,0] op_sel_hi:[1,1,0]
	s_waitcnt vmcnt(14)
	v_cvt_f32_f16_e32 v72, v156
	v_cvt_f32_f16_sdwa v73, v156 dst_sel:DWORD dst_unused:UNUSED_PAD src0_sel:WORD_1
	v_cvt_f32_f16_e32 v74, v157
	v_cvt_f32_f16_sdwa v75, v157 dst_sel:DWORD dst_unused:UNUSED_PAD src0_sel:WORD_1
	v_cvt_f32_f16_e32 v80, v158
	v_cvt_f32_f16_sdwa v81, v158 dst_sel:DWORD dst_unused:UNUSED_PAD src0_sel:WORD_1
	v_cvt_f32_f16_e32 v82, v159
	v_cvt_f32_f16_sdwa v83, v159 dst_sel:DWORD dst_unused:UNUSED_PAD src0_sel:WORD_1
	v_sub_f32_e32 v72, v72, v200
	v_sub_f32_e32 v73, v73, v200
	v_sub_f32_e32 v74, v74, v200
	v_sub_f32_e32 v75, v75, v200
	v_sub_f32_e32 v80, v80, v200
	v_sub_f32_e32 v81, v81, v200
	v_sub_f32_e32 v82, v82, v200
	v_sub_f32_e32 v83, v83, v200
	v_pk_mul_f32 v[72:73], v[200:201], v[72:73] op_sel:[1,0]
	v_pk_mul_f32 v[74:75], v[200:201], v[74:75] op_sel:[1,0]
	v_pk_mul_f32 v[80:81], v[200:201], v[80:81] op_sel:[1,0]
	v_pk_mul_f32 v[82:83], v[200:201], v[82:83] op_sel:[1,0]
	v_pk_fma_f32 v[36:37], v[72:73], v[168:169], v[36:37]
	v_pk_fma_f32 v[38:39], v[74:75], v[170:171], v[38:39]
	v_pk_fma_f32 v[32:33], v[80:81], v[172:173], v[32:33]
	v_pk_fma_f32 v[34:35], v[82:83], v[174:175], v[34:35]
	v_cvt_pk_f16_f32 v36, v36, v37
	v_cvt_pk_f16_f32 v37, v38, v39
	v_cvt_pk_f16_f32 v38, v32, v33
	v_cvt_pk_f16_f32 v39, v34, v35
	ds_write_b128 v235, v[36:39] offset:64
	v_fma_mix_f32 v208, v36, 1.0, v208 op_sel_hi:[1,0,0]
	v_fma_mix_f32 v209, v36, v36, v209 op_sel_hi:[1,1,0]
	v_fma_mix_f32 v208, v36, 1.0, v208 op_sel:[1,0,0] op_sel_hi:[1,0,0]
	v_fma_mix_f32 v209, v36, v36, v209 op_sel:[1,1,0] op_sel_hi:[1,1,0]
	v_fma_mix_f32 v208, v37, 1.0, v208 op_sel_hi:[1,0,0]
	v_fma_mix_f32 v209, v37, v37, v209 op_sel_hi:[1,1,0]
	v_fma_mix_f32 v208, v37, 1.0, v208 op_sel:[1,0,0] op_sel_hi:[1,0,0]
	v_fma_mix_f32 v209, v37, v37, v209 op_sel:[1,1,0] op_sel_hi:[1,1,0]
	v_fma_mix_f32 v208, v38, 1.0, v208 op_sel_hi:[1,0,0]
	v_fma_mix_f32 v209, v38, v38, v209 op_sel_hi:[1,1,0]
	v_fma_mix_f32 v208, v38, 1.0, v208 op_sel:[1,0,0] op_sel_hi:[1,0,0]
	v_fma_mix_f32 v209, v38, v38, v209 op_sel:[1,1,0] op_sel_hi:[1,1,0]
	v_fma_mix_f32 v208, v39, 1.0, v208 op_sel_hi:[1,0,0]
	v_fma_mix_f32 v209, v39, v39, v209 op_sel_hi:[1,1,0]
	v_fma_mix_f32 v208, v39, 1.0, v208 op_sel:[1,0,0] op_sel_hi:[1,0,0]
	v_fma_mix_f32 v209, v39, v39, v209 op_sel:[1,1,0] op_sel_hi:[1,1,0]
	ds_read_b128 v[128:131], v236
	ds_read_b128 v[104:107], v236 offset:1152
	s_waitcnt vmcnt(11)
	v_cvt_f32_f16_e32 v72, v212
	v_cvt_f32_f16_sdwa v73, v212 dst_sel:DWORD dst_unused:UNUSED_PAD src0_sel:WORD_1
	v_cvt_f32_f16_e32 v74, v213
	v_cvt_f32_f16_sdwa v75, v213 dst_sel:DWORD dst_unused:UNUSED_PAD src0_sel:WORD_1
	v_cvt_f32_f16_e32 v80, v214
	v_cvt_f32_f16_sdwa v81, v214 dst_sel:DWORD dst_unused:UNUSED_PAD src0_sel:WORD_1
	v_cvt_f32_f16_e32 v82, v215
	v_cvt_f32_f16_sdwa v83, v215 dst_sel:DWORD dst_unused:UNUSED_PAD src0_sel:WORD_1
	v_sub_f32_e32 v72, v72, v202
	v_sub_f32_e32 v73, v73, v202
	v_sub_f32_e32 v74, v74, v202
	v_sub_f32_e32 v75, v75, v202
	v_sub_f32_e32 v80, v80, v202
	v_sub_f32_e32 v81, v81, v202
	v_sub_f32_e32 v82, v82, v202
	v_sub_f32_e32 v83, v83, v202
	v_pk_mul_f32 v[72:73], v[202:203], v[72:73] op_sel:[1,0]
	v_pk_mul_f32 v[74:75], v[202:203], v[74:75] op_sel:[1,0]
	v_pk_mul_f32 v[80:81], v[202:203], v[80:81] op_sel:[1,0]
	v_pk_mul_f32 v[82:83], v[202:203], v[82:83] op_sel:[1,0]
	v_pk_fma_f32 v[28:29], v[72:73], v[160:161], v[28:29]
	v_pk_fma_f32 v[30:31], v[74:75], v[162:163], v[30:31]
	v_pk_fma_f32 v[24:25], v[80:81], v[164:165], v[24:25]
	v_pk_fma_f32 v[26:27], v[82:83], v[166:167], v[26:27]
	v_cvt_pk_f16_f32 v28, v28, v29
	v_cvt_pk_f16_f32 v29, v30, v31
	v_cvt_pk_f16_f32 v30, v24, v25
	v_cvt_pk_f16_f32 v31, v26, v27
	s_waitcnt lgkmcnt(0)
	v_add_u32_e32 v83, 0x36000, v225
	buffer_store_dwordx4 v[128:131], v83, s[24:27], 0 offen nt
	v_add_u32_e32 v82, 0x39000, v225
	buffer_store_dwordx4 v[104:107], v82, s[24:27], 0 offen nt
	ds_write_b128 v235, v[28:31]
	v_fma_mix_f32 v210, v28, 1.0, 0 op_sel_hi:[1,0,0]
	v_fma_mix_f32 v211, v28, v28, 0 op_sel_hi:[1,1,0]
	v_fma_mix_f32 v210, v28, 1.0, v210 op_sel:[1,0,0] op_sel_hi:[1,0,0]
	v_fma_mix_f32 v211, v28, v28, v211 op_sel:[1,1,0] op_sel_hi:[1,1,0]
	v_fma_mix_f32 v210, v29, 1.0, v210 op_sel_hi:[1,0,0]
	v_fma_mix_f32 v211, v29, v29, v211 op_sel_hi:[1,1,0]
	v_fma_mix_f32 v210, v29, 1.0, v210 op_sel:[1,0,0] op_sel_hi:[1,0,0]
	v_fma_mix_f32 v211, v29, v29, v211 op_sel:[1,1,0] op_sel_hi:[1,1,0]
	v_fma_mix_f32 v210, v30, 1.0, v210 op_sel_hi:[1,0,0]
	v_fma_mix_f32 v211, v30, v30, v211 op_sel_hi:[1,1,0]
	v_fma_mix_f32 v210, v30, 1.0, v210 op_sel:[1,0,0] op_sel_hi:[1,0,0]
	v_fma_mix_f32 v211, v30, v30, v211 op_sel:[1,1,0] op_sel_hi:[1,1,0]
	v_fma_mix_f32 v210, v31, 1.0, v210 op_sel_hi:[1,0,0]
	v_fma_mix_f32 v211, v31, v31, v211 op_sel_hi:[1,1,0]
	v_fma_mix_f32 v210, v31, 1.0, v210 op_sel:[1,0,0] op_sel_hi:[1,0,0]
	v_fma_mix_f32 v211, v31, v31, v211 op_sel:[1,1,0] op_sel_hi:[1,1,0]
	s_waitcnt vmcnt(12)
	v_cvt_f32_f16_e32 v72, v144
	v_cvt_f32_f16_sdwa v73, v144 dst_sel:DWORD dst_unused:UNUSED_PAD src0_sel:WORD_1
	v_cvt_f32_f16_e32 v74, v145
	v_cvt_f32_f16_sdwa v75, v145 dst_sel:DWORD dst_unused:UNUSED_PAD src0_sel:WORD_1
	v_cvt_f32_f16_e32 v80, v146
	v_cvt_f32_f16_sdwa v81, v146 dst_sel:DWORD dst_unused:UNUSED_PAD src0_sel:WORD_1
	v_cvt_f32_f16_e32 v82, v147
	v_cvt_f32_f16_sdwa v83, v147 dst_sel:DWORD dst_unused:UNUSED_PAD src0_sel:WORD_1
	v_sub_f32_e32 v72, v72, v202
	v_sub_f32_e32 v73, v73, v202
	v_sub_f32_e32 v74, v74, v202
	v_sub_f32_e32 v75, v75, v202
	v_sub_f32_e32 v80, v80, v202
	v_sub_f32_e32 v81, v81, v202
	v_sub_f32_e32 v82, v82, v202
	v_sub_f32_e32 v83, v83, v202
	v_pk_mul_f32 v[72:73], v[202:203], v[72:73] op_sel:[1,0]
	v_pk_mul_f32 v[74:75], v[202:203], v[74:75] op_sel:[1,0]
	v_pk_mul_f32 v[80:81], v[202:203], v[80:81] op_sel:[1,0]
	v_pk_mul_f32 v[82:83], v[202:203], v[82:83] op_sel:[1,0]
	v_pk_fma_f32 v[20:21], v[72:73], v[168:169], v[20:21]
	v_pk_fma_f32 v[22:23], v[74:75], v[170:171], v[22:23]
	v_pk_fma_f32 v[16:17], v[80:81], v[172:173], v[16:17]
	v_pk_fma_f32 v[18:19], v[82:83], v[174:175], v[18:19]
	v_cvt_pk_f16_f32 v20, v20, v21
	v_cvt_pk_f16_f32 v21, v22, v23
	v_cvt_pk_f16_f32 v22, v16, v17
	v_cvt_pk_f16_f32 v23, v18, v19
	ds_write_b128 v235, v[20:23] offset:64
	v_fma_mix_f32 v210, v20, 1.0, v210 op_sel_hi:[1,0,0]
	v_fma_mix_f32 v211, v20, v20, v211 op_sel_hi:[1,1,0]
	v_fma_mix_f32 v210, v20, 1.0, v210 op_sel:[1,0,0] op_sel_hi:[1,0,0]
	v_fma_mix_f32 v211, v20, v20, v211 op_sel:[1,1,0] op_sel_hi:[1,1,0]
	v_fma_mix_f32 v210, v21, 1.0, v210 op_sel_hi:[1,0,0]
	v_fma_mix_f32 v211, v21, v21, v211 op_sel_hi:[1,1,0]
	v_fma_mix_f32 v210, v21, 1.0, v210 op_sel:[1,0,0] op_sel_hi:[1,0,0]
	v_fma_mix_f32 v211, v21, v21, v211 op_sel:[1,1,0] op_sel_hi:[1,1,0]
	v_fma_mix_f32 v210, v22, 1.0, v210 op_sel_hi:[1,0,0]
	v_fma_mix_f32 v211, v22, v22, v211 op_sel_hi:[1,1,0]
	v_fma_mix_f32 v210, v22, 1.0, v210 op_sel:[1,0,0] op_sel_hi:[1,0,0]
	v_fma_mix_f32 v211, v22, v22, v211 op_sel:[1,1,0] op_sel_hi:[1,1,0]
	v_fma_mix_f32 v210, v23, 1.0, v210 op_sel_hi:[1,0,0]
	v_fma_mix_f32 v211, v23, v23, v211 op_sel_hi:[1,1,0]
	v_fma_mix_f32 v210, v23, 1.0, v210 op_sel:[1,0,0] op_sel_hi:[1,0,0]
	v_fma_mix_f32 v211, v23, v23, v211 op_sel:[1,1,0] op_sel_hi:[1,1,0]
	ds_read_b128 v[240:243], v236
	ds_read_b128 v[96:99], v236 offset:1152
	s_waitcnt vmcnt(11)
	v_cvt_f32_f16_e32 v72, v132
	v_cvt_f32_f16_sdwa v73, v132 dst_sel:DWORD dst_unused:UNUSED_PAD src0_sel:WORD_1
	v_cvt_f32_f16_e32 v74, v133
	v_cvt_f32_f16_sdwa v75, v133 dst_sel:DWORD dst_unused:UNUSED_PAD src0_sel:WORD_1
	v_cvt_f32_f16_e32 v80, v134
	v_cvt_f32_f16_sdwa v81, v134 dst_sel:DWORD dst_unused:UNUSED_PAD src0_sel:WORD_1
	v_cvt_f32_f16_e32 v82, v135
	v_cvt_f32_f16_sdwa v83, v135 dst_sel:DWORD dst_unused:UNUSED_PAD src0_sel:WORD_1
	v_sub_f32_e32 v72, v72, v204
	v_sub_f32_e32 v73, v73, v204
	v_sub_f32_e32 v74, v74, v204
	v_sub_f32_e32 v75, v75, v204
	v_sub_f32_e32 v80, v80, v204
	v_sub_f32_e32 v81, v81, v204
	v_sub_f32_e32 v82, v82, v204
	v_sub_f32_e32 v83, v83, v204
	v_pk_mul_f32 v[72:73], v[204:205], v[72:73] op_sel:[1,0]
	v_pk_mul_f32 v[74:75], v[204:205], v[74:75] op_sel:[1,0]
	v_pk_mul_f32 v[80:81], v[204:205], v[80:81] op_sel:[1,0]
	v_pk_mul_f32 v[82:83], v[204:205], v[82:83] op_sel:[1,0]
	v_pk_fma_f32 v[12:13], v[72:73], v[160:161], v[12:13]
	v_pk_fma_f32 v[14:15], v[74:75], v[162:163], v[14:15]
	v_pk_fma_f32 v[8:9], v[80:81], v[164:165], v[8:9]
	v_pk_fma_f32 v[10:11], v[82:83], v[166:167], v[10:11]
	v_cvt_pk_f16_f32 v12, v12, v13
	v_cvt_pk_f16_f32 v13, v14, v15
	v_cvt_pk_f16_f32 v14, v8, v9
	v_cvt_pk_f16_f32 v15, v10, v11
	s_waitcnt lgkmcnt(0)
	v_add_u32_e32 v83, 0x3c000, v225
	buffer_store_dwordx4 v[240:243], v83, s[24:27], 0 offen nt
	v_add_u32_e32 v82, 0x3f000, v225
	buffer_store_dwordx4 v[96:99], v82, s[24:27], 0 offen nt
	ds_write_b128 v235, v[12:15]
	v_fma_mix_f32 v244, v12, 1.0, 0 op_sel_hi:[1,0,0]
	v_fma_mix_f32 v245, v12, v12, 0 op_sel_hi:[1,1,0]
	v_fma_mix_f32 v244, v12, 1.0, v244 op_sel:[1,0,0] op_sel_hi:[1,0,0]
	v_fma_mix_f32 v245, v12, v12, v245 op_sel:[1,1,0] op_sel_hi:[1,1,0]
	v_fma_mix_f32 v244, v13, 1.0, v244 op_sel_hi:[1,0,0]
	v_fma_mix_f32 v245, v13, v13, v245 op_sel_hi:[1,1,0]
	v_fma_mix_f32 v244, v13, 1.0, v244 op_sel:[1,0,0] op_sel_hi:[1,0,0]
	v_fma_mix_f32 v245, v13, v13, v245 op_sel:[1,1,0] op_sel_hi:[1,1,0]
	v_fma_mix_f32 v244, v14, 1.0, v244 op_sel_hi:[1,0,0]
	v_fma_mix_f32 v245, v14, v14, v245 op_sel_hi:[1,1,0]
	v_fma_mix_f32 v244, v14, 1.0, v244 op_sel:[1,0,0] op_sel_hi:[1,0,0]
	v_fma_mix_f32 v245, v14, v14, v245 op_sel:[1,1,0] op_sel_hi:[1,1,0]
	v_fma_mix_f32 v244, v15, 1.0, v244 op_sel_hi:[1,0,0]
	v_fma_mix_f32 v245, v15, v15, v245 op_sel_hi:[1,1,0]
	v_fma_mix_f32 v244, v15, 1.0, v244 op_sel:[1,0,0] op_sel_hi:[1,0,0]
	v_fma_mix_f32 v245, v15, v15, v245 op_sel:[1,1,0] op_sel_hi:[1,1,0]
	s_waitcnt vmcnt(12)
	v_cvt_f32_f16_e32 v72, v88
	v_cvt_f32_f16_sdwa v73, v88 dst_sel:DWORD dst_unused:UNUSED_PAD src0_sel:WORD_1
	v_cvt_f32_f16_e32 v74, v89
	v_cvt_f32_f16_sdwa v75, v89 dst_sel:DWORD dst_unused:UNUSED_PAD src0_sel:WORD_1
	v_cvt_f32_f16_e32 v80, v90
	v_cvt_f32_f16_sdwa v81, v90 dst_sel:DWORD dst_unused:UNUSED_PAD src0_sel:WORD_1
	v_cvt_f32_f16_e32 v82, v91
	v_cvt_f32_f16_sdwa v83, v91 dst_sel:DWORD dst_unused:UNUSED_PAD src0_sel:WORD_1
	v_sub_f32_e32 v72, v72, v204
	v_sub_f32_e32 v73, v73, v204
	v_sub_f32_e32 v74, v74, v204
	v_sub_f32_e32 v75, v75, v204
	v_sub_f32_e32 v80, v80, v204
	v_sub_f32_e32 v81, v81, v204
	v_sub_f32_e32 v82, v82, v204
	v_sub_f32_e32 v83, v83, v204
	v_pk_mul_f32 v[72:73], v[204:205], v[72:73] op_sel:[1,0]
	v_pk_mul_f32 v[74:75], v[204:205], v[74:75] op_sel:[1,0]
	v_pk_mul_f32 v[80:81], v[204:205], v[80:81] op_sel:[1,0]
	v_pk_mul_f32 v[82:83], v[204:205], v[82:83] op_sel:[1,0]
	v_pk_fma_f32 v[4:5], v[72:73], v[168:169], v[4:5]
	v_pk_fma_f32 v[6:7], v[74:75], v[170:171], v[6:7]
	v_pk_fma_f32 v[0:1], v[80:81], v[172:173], v[0:1]
	v_pk_fma_f32 v[2:3], v[82:83], v[174:175], v[2:3]
	v_cvt_pk_f16_f32 v4, v4, v5
	v_cvt_pk_f16_f32 v5, v6, v7
	v_cvt_pk_f16_f32 v6, v0, v1
	v_cvt_pk_f16_f32 v7, v2, v3
	ds_write_b128 v235, v[4:7] offset:64
	v_fma_mix_f32 v244, v4, 1.0, v244 op_sel_hi:[1,0,0]
	v_fma_mix_f32 v245, v4, v4, v245 op_sel_hi:[1,1,0]
	v_fma_mix_f32 v244, v4, 1.0, v244 op_sel:[1,0,0] op_sel_hi:[1,0,0]
	v_fma_mix_f32 v245, v4, v4, v245 op_sel:[1,1,0] op_sel_hi:[1,1,0]
	v_fma_mix_f32 v244, v5, 1.0, v244 op_sel_hi:[1,0,0]
	v_fma_mix_f32 v245, v5, v5, v245 op_sel_hi:[1,1,0]
	v_fma_mix_f32 v244, v5, 1.0, v244 op_sel:[1,0,0] op_sel_hi:[1,0,0]
	v_fma_mix_f32 v245, v5, v5, v245 op_sel:[1,1,0] op_sel_hi:[1,1,0]
	v_fma_mix_f32 v244, v6, 1.0, v244 op_sel_hi:[1,0,0]
	v_fma_mix_f32 v245, v6, v6, v245 op_sel_hi:[1,1,0]
	v_fma_mix_f32 v244, v6, 1.0, v244 op_sel:[1,0,0] op_sel_hi:[1,0,0]
	v_fma_mix_f32 v245, v6, v6, v245 op_sel:[1,1,0] op_sel_hi:[1,1,0]
	v_fma_mix_f32 v244, v7, 1.0, v244 op_sel_hi:[1,0,0]
	v_fma_mix_f32 v245, v7, v7, v245 op_sel_hi:[1,1,0]
	v_fma_mix_f32 v244, v7, 1.0, v244 op_sel:[1,0,0] op_sel_hi:[1,0,0]
	v_fma_mix_f32 v245, v7, v7, v245 op_sel:[1,1,0] op_sel_hi:[1,1,0]
	ds_read_b128 v[108:111], v236
	ds_read_b128 v[100:103], v236 offset:1152
	s_waitcnt lgkmcnt(0)
	v_add_u32_e32 v83, 0x42000, v225
	buffer_store_dwordx4 v[108:111], v83, s[24:27], 0 offen nt
	v_add_u32_e32 v82, 0x45000, v225
	buffer_store_dwordx4 v[100:103], v82, s[24:27], 0 offen nt
	v_xor_b32_e32 v246, 16, v234
	v_lshlrev_b32_e32 v246, 2, v246
	v_xor_b32_e32 v247, 32, v234
	v_lshlrev_b32_e32 v247, 2, v247
	ds_bpermute_b32 v92, v246, v206
	ds_bpermute_b32 v93, v246, v207
	ds_bpermute_b32 v94, v246, v140
	ds_bpermute_b32 v95, v246, v141
	ds_bpermute_b32 v120, v246, v142
	ds_bpermute_b32 v121, v246, v143
	ds_bpermute_b32 v122, v246, v216
	ds_bpermute_b32 v123, v246, v217
	s_waitcnt lgkmcnt(0)
	v_pk_add_f32 v[206:207], v[206:207], v[92:93]
	v_pk_add_f32 v[140:141], v[140:141], v[94:95]
	v_pk_add_f32 v[142:143], v[142:143], v[120:121]
	v_pk_add_f32 v[216:217], v[216:217], v[122:123]
	ds_bpermute_b32 v92, v246, v218
	ds_bpermute_b32 v93, v246, v219
	ds_bpermute_b32 v94, v246, v208
	ds_bpermute_b32 v95, v246, v209
	ds_bpermute_b32 v120, v246, v210
	ds_bpermute_b32 v121, v246, v211
	ds_bpermute_b32 v122, v246, v244
	ds_bpermute_b32 v123, v246, v245
	s_waitcnt lgkmcnt(0)
	v_pk_add_f32 v[218:219], v[218:219], v[92:93]
	v_pk_add_f32 v[208:209], v[208:209], v[94:95]
	v_pk_add_f32 v[210:211], v[210:211], v[120:121]
	v_pk_add_f32 v[244:245], v[244:245], v[122:123]
	ds_bpermute_b32 v92, v247, v206
	ds_bpermute_b32 v93, v247, v207
	ds_bpermute_b32 v94, v247, v140
	ds_bpermute_b32 v95, v247, v141
	ds_bpermute_b32 v120, v247, v142
	ds_bpermute_b32 v121, v247, v143
	ds_bpermute_b32 v122, v247, v216
	ds_bpermute_b32 v123, v247, v217
	s_waitcnt lgkmcnt(0)
	v_pk_add_f32 v[206:207], v[206:207], v[92:93]
	v_pk_add_f32 v[140:141], v[140:141], v[94:95]
	v_pk_add_f32 v[142:143], v[142:143], v[120:121]
	v_pk_add_f32 v[216:217], v[216:217], v[122:123]
	ds_bpermute_b32 v92, v247, v218
	ds_bpermute_b32 v93, v247, v219
	ds_bpermute_b32 v94, v247, v208
	ds_bpermute_b32 v95, v247, v209
	ds_bpermute_b32 v120, v247, v210
	ds_bpermute_b32 v121, v247, v211
	ds_bpermute_b32 v122, v247, v244
	ds_bpermute_b32 v123, v247, v245
	s_waitcnt lgkmcnt(0)
	v_pk_add_f32 v[218:219], v[218:219], v[92:93]
	v_pk_add_f32 v[208:209], v[208:209], v[94:95]
	v_pk_add_f32 v[210:211], v[210:211], v[120:121]
	v_pk_add_f32 v[244:245], v[244:245], v[122:123]
	global_store_dwordx2 v224, v[206:207], s[100:101] offset:-2048
	global_store_dwordx2 v224, v[140:141], s[100:101] offset:-512
	global_store_dwordx2 v224, v[142:143], s[100:101] offset:1024
	global_store_dwordx2 v224, v[216:217], s[100:101] offset:2560
	s_add_u32 s100, s100, 0x3000
	s_addc_u32 s101, s101, 0
	global_store_dwordx2 v224, v[218:219], s[100:101] offset:-2048
	global_store_dwordx2 v224, v[208:209], s[100:101] offset:-512
	global_store_dwordx2 v224, v[210:211], s[100:101] offset:1024
	global_store_dwordx2 v224, v[244:245], s[100:101] offset:2560
	s_mov_b32 s83, s81
	s_mov_b32 s84, s82
	s_mov_b64 s[40:41], s[0:1]
	s_mov_b64 s[38:39], s[8:9]
	s_mov_b64 vcc, s[6:7]
	s_cbranch_vccz .LBB10_12
	s_waitcnt vmcnt(0)
	s_cmpk_gt_u32 s44, 0xff
	s_cbranch_scc1 .LBB10_31
	s_barrier
